# LDS-DMA issue evened out over the K-loop load segments (2 per segment; As[1][1] refill phase 1->2, Bs[0][1] refill phase 5->6) with per-slot counted waits, all 14 fp8 GEMM K-loops
# speedup vs baseline: 1.0074x; 1.0074x over previous
.LBB0_220:
	s_add_u32 s40, s10, s38
	s_addc_u32 s41, s11, s39
	s_add_u32 s42, s40, 0x49800100
	ds_read_b128 v[144:147], v154
	ds_read_b128 v[170:173], v154 offset:2048
	ds_read_b128 v[148:151], v155
	ds_read_b128 v[174:177], v155 offset:2048
	s_addc_u32 s43, s41, 0
	s_add_u32 s67, s1, s38
	s_addc_u32 s68, s56, s39
	s_cmpk_eq_i32 s38, 0x700
	s_cselect_b64 vcc, -1, 0
	s_and_b64 s[40:41], vcc, exec
	ds_read_b128 v[178:181], v152
	ds_read_b128 v[186:189], v152 offset:2048
	ds_read_b128 v[182:185], v153
	ds_read_b128 v[190:193], v153 offset:2048
	ds_read_b128 v[196:199], v152 offset:4096
	ds_read_b128 v[204:207], v152 offset:6144
	ds_read_b128 v[200:203], v153 offset:4096
	ds_read_b128 v[208:211], v153 offset:6144
	s_waitcnt vmcnt(6)
	s_waitcnt lgkmcnt(8)
	s_barrier
	s_waitcnt lgkmcnt(0)
	s_setprio 1
	s_waitcnt lgkmcnt(0)
	v_mfma_f32_16x16x128_f8f6f4 v[124:127], v[144:151], v[178:185], v[124:127]
	v_mfma_f32_16x16x128_f8f6f4 v[120:123], v[170:177], v[178:185], v[120:123]
	v_mfma_f32_16x16x128_f8f6f4 v[108:111], v[144:151], v[186:193], v[108:111]
	v_mfma_f32_16x16x128_f8f6f4 v[104:107], v[170:177], v[186:193], v[104:107]
	v_mfma_f32_16x16x128_f8f6f4 v[92:95], v[144:151], v[196:203], v[92:95]
	v_mfma_f32_16x16x128_f8f6f4 v[88:91], v[170:177], v[196:203], v[88:91]
	v_mfma_f32_16x16x128_f8f6f4 v[76:79], v[144:151], v[204:211], v[76:79]
	v_mfma_f32_16x16x128_f8f6f4 v[72:75], v[170:177], v[204:211], v[72:75]
	s_setprio 0
	s_barrier
	ds_read_b128 v[222:225], v154 offset:16384
	ds_read_b128 v[230:233], v154 offset:18432
	ds_read_b128 v[226:229], v155 offset:16384
	ds_read_b128 v[234:237], v155 offset:18432
	v_cndmask_b32_e32 v132, v135, v165, vcc
	s_cselect_b32 s43, s13, s43
	s_cselect_b32 s42, s12, s42
	s_cselect_b32 s41, s37, s68
	s_cselect_b32 s40, s36, s67
	v_cndmask_b32_e32 v137, v136, v167, vcc
	v_lshl_add_u64 v[212:213], v[142:143], 0, s[38:39]
	s_add_i32 m0, s33, 0xc000
	s_nop 0
	global_load_lds_dwordx4 v[212:213], off
	v_lshl_add_u64 v[212:213], v[140:141], 0, s[38:39]
	s_add_i32 m0, s33, 0xe000
	v_cndmask_b32_e32 v220, v134, v166, vcc
	global_load_lds_dwordx4 v[212:213], off
	s_barrier
	s_waitcnt lgkmcnt(0)
	s_setprio 1
	s_waitcnt lgkmcnt(0)
	v_mfma_f32_16x16x128_f8f6f4 v[116:119], v[222:229], v[178:185], v[116:119]
	v_mfma_f32_16x16x128_f8f6f4 v[112:115], v[230:237], v[178:185], v[112:115]
	v_mfma_f32_16x16x128_f8f6f4 v[100:103], v[222:229], v[186:193], v[100:103]
	v_mfma_f32_16x16x128_f8f6f4 v[96:99], v[230:237], v[186:193], v[96:99]
	v_mfma_f32_16x16x128_f8f6f4 v[84:87], v[222:229], v[196:203], v[84:87]
	v_mfma_f32_16x16x128_f8f6f4 v[80:83], v[230:237], v[196:203], v[80:83]
	v_mfma_f32_16x16x128_f8f6f4 v[68:71], v[222:229], v[204:211], v[68:71]
	v_mfma_f32_16x16x128_f8f6f4 v[64:67], v[230:237], v[204:211], v[64:67]
	s_setprio 0
	s_barrier
	s_mov_b32 m0, s33
	ds_read_b128 v[186:189], v152 offset:16384
	ds_read_b128 v[196:199], v152 offset:18432
	ds_read_b128 v[190:193], v153 offset:16384
	ds_read_b128 v[200:203], v153 offset:18432
	ds_read_b128 v[204:207], v152 offset:20480
	ds_read_b128 v[212:215], v152 offset:22528
	ds_read_b128 v[208:211], v153 offset:20480
	ds_read_b128 v[216:219], v153 offset:22528
	global_load_lds_dwordx4 v132, s[42:43]
	s_mov_b32 m0, s46
	v_mov_b32_e32 v221, v133
	global_load_lds_dwordx4 v220, s[42:43]
	s_waitcnt lgkmcnt(8)
	s_barrier
	s_waitcnt lgkmcnt(0)
	v_lshl_add_u64 v[246:247], s[42:43], 0, v[132:133]
	v_lshl_add_u64 v[244:245], s[42:43], 0, v[220:221]
	s_setprio 1
	s_waitcnt lgkmcnt(0)
	v_mfma_f32_16x16x128_f8f6f4 v[60:63], v[144:151], v[186:193], v[60:63]
	v_mfma_f32_16x16x128_f8f6f4 v[56:59], v[170:177], v[186:193], v[56:59]
	v_mfma_f32_16x16x128_f8f6f4 v[44:47], v[144:151], v[196:203], v[44:47]
	v_mfma_f32_16x16x128_f8f6f4 v[40:43], v[170:177], v[196:203], v[40:43]
	v_mfma_f32_16x16x128_f8f6f4 v[28:31], v[144:151], v[204:211], v[28:31]
	v_mfma_f32_16x16x128_f8f6f4 v[24:27], v[170:177], v[204:211], v[24:27]
	v_mfma_f32_16x16x128_f8f6f4 v[12:15], v[144:151], v[212:219], v[12:15]
	v_mfma_f32_16x16x128_f8f6f4 v[8:11], v[170:177], v[212:219], v[8:11]
	s_setprio 0
	s_barrier
	s_mov_b32 m0, s44
	v_lshl_add_u64 v[144:145], s[40:41], 0, v[128:129]
	global_load_lds_dwordx4 v[144:145], off
	v_lshl_add_u64 v[146:147], s[40:41], 0, v[130:131]
	s_mov_b32 m0, s45
	s_nop 0
	global_load_lds_dwordx4 v[146:147], off
	s_waitcnt vmcnt(8)
	s_waitcnt lgkmcnt(0)
	s_barrier
	s_setprio 1
	s_waitcnt lgkmcnt(0)
	v_mfma_f32_16x16x128_f8f6f4 v[52:55], v[222:229], v[186:193], v[52:55]
	v_mfma_f32_16x16x128_f8f6f4 v[48:51], v[230:237], v[186:193], v[48:51]
	v_mfma_f32_16x16x128_f8f6f4 v[36:39], v[222:229], v[196:203], v[36:39]
	v_mfma_f32_16x16x128_f8f6f4 v[32:35], v[230:237], v[196:203], v[32:35]
	v_mfma_f32_16x16x128_f8f6f4 v[20:23], v[222:229], v[204:211], v[20:23]
	v_mfma_f32_16x16x128_f8f6f4 v[16:19], v[230:237], v[204:211], v[16:19]
	v_mfma_f32_16x16x128_f8f6f4 v[4:7], v[222:229], v[212:219], v[4:7]
	v_mfma_f32_16x16x128_f8f6f4 v[0:3], v[230:237], v[212:219], v[0:3]
	s_setprio 0
	s_barrier
	ds_read_b128 v[170:173], v154 offset:32768
	ds_read_b128 v[178:181], v154 offset:34816
	ds_read_b128 v[174:177], v155 offset:32768
	ds_read_b128 v[182:185], v155 offset:34816
	s_mov_b32 m0, s49
	ds_read_b128 v[186:189], v152 offset:32768
	ds_read_b128 v[196:199], v152 offset:34816
	ds_read_b128 v[190:193], v153 offset:32768
	ds_read_b128 v[200:203], v153 offset:34816
	ds_read_b128 v[204:207], v152 offset:36864
	ds_read_b128 v[212:215], v152 offset:38912
	ds_read_b128 v[208:211], v153 offset:36864
	ds_read_b128 v[216:219], v153 offset:38912
	v_cndmask_b32_e32 v132, v138, v168, vcc
	global_load_lds_dwordx4 v137, s[42:43]
	s_mov_b32 m0, s50
	s_nop 0
	global_load_lds_dwordx4 v132, s[42:43]
	s_waitcnt vmcnt(8)
	s_waitcnt lgkmcnt(8)
	s_barrier
	s_waitcnt lgkmcnt(0)
	s_setprio 1
	s_waitcnt lgkmcnt(0)
	v_mfma_f32_16x16x128_f8f6f4 v[124:127], v[170:177], v[186:193], v[124:127]
	v_mfma_f32_16x16x128_f8f6f4 v[120:123], v[178:185], v[186:193], v[120:123]
	v_mfma_f32_16x16x128_f8f6f4 v[108:111], v[170:177], v[196:203], v[108:111]
	v_mfma_f32_16x16x128_f8f6f4 v[104:107], v[178:185], v[196:203], v[104:107]
	v_mfma_f32_16x16x128_f8f6f4 v[92:95], v[170:177], v[204:211], v[92:95]
	v_mfma_f32_16x16x128_f8f6f4 v[88:91], v[178:185], v[204:211], v[88:91]
	v_mfma_f32_16x16x128_f8f6f4 v[76:79], v[170:177], v[212:219], v[76:79]
	v_mfma_f32_16x16x128_f8f6f4 v[72:75], v[178:185], v[212:219], v[72:75]
	s_setprio 0
	s_barrier
	ds_read_b128 v[222:225], v154 offset:49152
	ds_read_b128 v[230:233], v154 offset:51200
	ds_read_b128 v[226:229], v155 offset:49152
	ds_read_b128 v[234:237], v155 offset:51200
	s_add_u32 s42, s40, 0x4000
	s_addc_u32 s43, s41, 0
	v_lshl_add_u64 v[220:221], s[42:43], 0, v[128:129]
	s_mov_b32 m0, s47
	s_nop 0
	global_load_lds_dwordx4 v[220:221], off
	v_lshl_add_u64 v[220:221], s[42:43], 0, v[130:131]
	s_mov_b32 m0, s48
	s_nop 0
	global_load_lds_dwordx4 v[220:221], off
	s_waitcnt vmcnt(8)
	s_barrier
	s_waitcnt lgkmcnt(0)
	s_setprio 1
	s_waitcnt lgkmcnt(0)
	v_mfma_f32_16x16x128_f8f6f4 v[116:119], v[222:229], v[186:193], v[116:119]
	v_mfma_f32_16x16x128_f8f6f4 v[112:115], v[230:237], v[186:193], v[112:115]
	v_mfma_f32_16x16x128_f8f6f4 v[100:103], v[222:229], v[196:203], v[100:103]
	v_mfma_f32_16x16x128_f8f6f4 v[96:99], v[230:237], v[196:203], v[96:99]
	v_mfma_f32_16x16x128_f8f6f4 v[84:87], v[222:229], v[204:211], v[84:87]
	v_mfma_f32_16x16x128_f8f6f4 v[80:83], v[230:237], v[204:211], v[80:83]
	v_mfma_f32_16x16x128_f8f6f4 v[68:71], v[222:229], v[212:219], v[68:71]
	v_mfma_f32_16x16x128_f8f6f4 v[64:67], v[230:237], v[212:219], v[64:67]
	s_setprio 0
	s_barrier
	s_mov_b32 m0, s54
	v_lshl_add_u64 v[246:247], v[246:247], 0, s[24:25]
	ds_read_b128 v[186:189], v152 offset:49152
	ds_read_b128 v[196:199], v152 offset:51200
	ds_read_b128 v[190:193], v153 offset:49152
	ds_read_b128 v[200:203], v153 offset:51200
	ds_read_b128 v[204:207], v152 offset:53248
	ds_read_b128 v[212:215], v152 offset:55296
	ds_read_b128 v[208:211], v153 offset:53248
	ds_read_b128 v[216:219], v153 offset:55296
	global_load_lds_dwordx4 v[246:247], off
	v_lshl_add_u64 v[244:245], v[244:245], 0, s[24:25]
	s_mov_b32 m0, s55
	s_nop 0
	global_load_lds_dwordx4 v[244:245], off
	s_waitcnt lgkmcnt(8)
	s_barrier
	s_waitcnt lgkmcnt(0)
	s_setprio 1
	s_waitcnt lgkmcnt(0)
	v_mfma_f32_16x16x128_f8f6f4 v[60:63], v[170:177], v[186:193], v[60:63]
	v_mfma_f32_16x16x128_f8f6f4 v[56:59], v[178:185], v[186:193], v[56:59]
	v_mfma_f32_16x16x128_f8f6f4 v[44:47], v[170:177], v[196:203], v[44:47]
	v_mfma_f32_16x16x128_f8f6f4 v[40:43], v[178:185], v[196:203], v[40:43]
	v_mfma_f32_16x16x128_f8f6f4 v[28:31], v[170:177], v[204:211], v[28:31]
	v_mfma_f32_16x16x128_f8f6f4 v[24:27], v[178:185], v[204:211], v[24:27]
	v_mfma_f32_16x16x128_f8f6f4 v[12:15], v[170:177], v[212:219], v[12:15]
	v_mfma_f32_16x16x128_f8f6f4 v[8:11], v[178:185], v[212:219], v[8:11]
	s_setprio 0
	s_barrier
	s_mov_b32 m0, s52
	v_lshl_add_u64 v[144:145], v[144:145], 0, s[24:25]
	global_load_lds_dwordx4 v[144:145], off
	v_lshl_add_u64 v[144:145], v[146:147], 0, s[24:25]
	s_mov_b32 m0, s53
	s_nop 0
	global_load_lds_dwordx4 v[144:145], off
	s_waitcnt vmcnt(8)
	s_waitcnt lgkmcnt(0)
	s_barrier
	s_setprio 1
	s_waitcnt lgkmcnt(0)
	v_mfma_f32_16x16x128_f8f6f4 v[52:55], v[222:229], v[186:193], v[52:55]
	v_mfma_f32_16x16x128_f8f6f4 v[48:51], v[230:237], v[186:193], v[48:51]
	v_mfma_f32_16x16x128_f8f6f4 v[36:39], v[222:229], v[196:203], v[36:39]
	v_mfma_f32_16x16x128_f8f6f4 v[32:35], v[230:237], v[196:203], v[32:35]
	v_mfma_f32_16x16x128_f8f6f4 v[20:23], v[222:229], v[204:211], v[20:23]
	v_mfma_f32_16x16x128_f8f6f4 v[16:19], v[230:237], v[204:211], v[16:19]
	v_mfma_f32_16x16x128_f8f6f4 v[4:7], v[222:229], v[212:219], v[4:7]
	v_mfma_f32_16x16x128_f8f6f4 v[0:3], v[230:237], v[212:219], v[0:3]
	s_setprio 0
	s_barrier
	s_add_u32 s40, s40, 0x4080
	s_addc_u32 s41, s41, 0
	s_mov_b32 m0, s58
	v_lshl_add_u64 v[144:145], s[40:41], 0, v[128:129]
	global_load_lds_dwordx4 v[144:145], off
	v_lshl_add_u64 v[144:145], s[40:41], 0, v[130:131]
	s_mov_b32 m0, s59
	s_add_i32 s57, s57, 2
	global_load_lds_dwordx4 v[144:145], off
	s_add_u32 s38, s38, 0x100
	s_addc_u32 s39, s39, 0
	s_cmp_gt_u32 s57, 13
	s_cbranch_scc0 .LBB0_220
	s_and_b64 vcc, exec, s[28:29]
	s_cbranch_vccz .LBB0_223
	s_barrier

.LBB0_313:
	s_add_u32 s36, s6, s34
	s_addc_u32 s37, s7, s35
	s_add_u32 s38, s36, 0x4e000100
	ds_read_b128 v[158:161], v167
	ds_read_b128 v[172:175], v167 offset:2048
	ds_read_b128 v[162:165], v168
	ds_read_b128 v[176:179], v168 offset:2048
	s_addc_u32 s39, s37, 0
	s_add_u32 s70, s67, s34
	s_addc_u32 s71, s68, s35
	s_cmpk_eq_i32 s34, 0x200
	s_cselect_b64 vcc, -1, 0
	s_and_b64 s[36:37], vcc, exec
	ds_read_b128 v[180:183], v129
	ds_read_b128 v[196:199], v129 offset:2048
	ds_read_b128 v[184:187], v131
	ds_read_b128 v[200:203], v131 offset:2048
	ds_read_b128 v[204:207], v129 offset:4096
	ds_read_b128 v[212:215], v129 offset:6144
	ds_read_b128 v[208:211], v131 offset:4096
	ds_read_b128 v[216:219], v131 offset:6144
	s_waitcnt vmcnt(6)
	s_waitcnt lgkmcnt(8)
	s_barrier
	s_waitcnt lgkmcnt(0)
	v_cndmask_b32_e32 v188, v148, v140, vcc
	s_setprio 1
	s_waitcnt lgkmcnt(0)
	v_mfma_f32_16x16x128_f8f6f4 v[124:127], v[158:165], v[180:187], v[124:127]
	v_mfma_f32_16x16x128_f8f6f4 v[120:123], v[172:179], v[180:187], v[120:123]
	v_mfma_f32_16x16x128_f8f6f4 v[112:115], v[158:165], v[196:203], v[112:115]
	v_mfma_f32_16x16x128_f8f6f4 v[104:107], v[172:179], v[196:203], v[104:107]
	v_mfma_f32_16x16x128_f8f6f4 v[96:99], v[158:165], v[204:211], v[96:99]
	v_mfma_f32_16x16x128_f8f6f4 v[88:91], v[172:179], v[204:211], v[88:91]
	v_mfma_f32_16x16x128_f8f6f4 v[80:83], v[158:165], v[212:219], v[80:83]
	v_mfma_f32_16x16x128_f8f6f4 v[72:75], v[172:179], v[212:219], v[72:75]
	s_setprio 0
	s_barrier
	ds_read_b128 v[228:231], v167 offset:16384
	ds_read_b128 v[236:239], v167 offset:18432
	ds_read_b128 v[232:235], v168 offset:16384
	ds_read_b128 v[240:243], v168 offset:18432
	v_cndmask_b32_e32 v136, v146, v138, vcc
	s_cselect_b32 s39, s9, s39
	s_cselect_b32 s38, s8, s38
	s_cselect_b32 s37, s31, s71
	s_cselect_b32 s36, s30, s70
	v_cndmask_b32_e32 v139, v150, v142, vcc
	v_lshl_add_u64 v[252:253], v[156:157], 0, s[34:35]
	s_add_i32 m0, s46, 0xc000
	s_nop 0
	global_load_lds_dwordx4 v[252:253], off
	v_lshl_add_u64 v[252:253], v[154:155], 0, s[34:35]
	s_add_i32 m0, s46, 0xe000
	s_nop 0
	global_load_lds_dwordx4 v[252:253], off
	s_barrier
	s_waitcnt lgkmcnt(0)
	s_setprio 1
	s_waitcnt lgkmcnt(0)
	v_mfma_f32_16x16x128_f8f6f4 v[116:119], v[228:235], v[180:187], v[116:119]
	v_mfma_f32_16x16x128_f8f6f4 v[108:111], v[236:243], v[180:187], v[108:111]
	v_mfma_f32_16x16x128_f8f6f4 v[100:103], v[228:235], v[196:203], v[100:103]
	v_mfma_f32_16x16x128_f8f6f4 v[92:95], v[236:243], v[196:203], v[92:95]
	v_mfma_f32_16x16x128_f8f6f4 v[84:87], v[228:235], v[204:211], v[84:87]
	v_mfma_f32_16x16x128_f8f6f4 v[76:79], v[236:243], v[204:211], v[76:79]
	v_mfma_f32_16x16x128_f8f6f4 v[68:71], v[228:235], v[212:219], v[68:71]
	v_mfma_f32_16x16x128_f8f6f4 v[64:67], v[236:243], v[212:219], v[64:67]
	s_setprio 0
	s_barrier
	s_mov_b32 m0, s46
	ds_read_b128 v[196:199], v129 offset:16384
	ds_read_b128 v[204:207], v129 offset:18432
	ds_read_b128 v[200:203], v131 offset:16384
	ds_read_b128 v[208:211], v131 offset:18432
	ds_read_b128 v[212:215], v129 offset:20480
	ds_read_b128 v[220:223], v129 offset:22528
	ds_read_b128 v[216:219], v131 offset:20480
	ds_read_b128 v[224:227], v131 offset:22528
	global_load_lds_dwordx4 v136, s[38:39]
	s_mov_b32 m0, s49
	v_mov_b32_e32 v189, v137
	global_load_lds_dwordx4 v188, s[38:39]
	s_waitcnt lgkmcnt(8)
	s_barrier
	s_waitcnt lgkmcnt(0)
	v_lshl_add_u64 v[246:247], s[38:39], 0, v[136:137]
	v_lshl_add_u64 v[244:245], s[38:39], 0, v[188:189]
	s_setprio 1
	s_waitcnt lgkmcnt(0)
	v_mfma_f32_16x16x128_f8f6f4 v[60:63], v[158:165], v[196:203], v[60:63]
	v_mfma_f32_16x16x128_f8f6f4 v[56:59], v[172:179], v[196:203], v[56:59]
	v_mfma_f32_16x16x128_f8f6f4 v[48:51], v[158:165], v[204:211], v[48:51]
	v_mfma_f32_16x16x128_f8f6f4 v[40:43], v[172:179], v[204:211], v[40:43]
	v_mfma_f32_16x16x128_f8f6f4 v[32:35], v[158:165], v[212:219], v[32:35]
	v_mfma_f32_16x16x128_f8f6f4 v[24:27], v[172:179], v[212:219], v[24:27]
	v_mfma_f32_16x16x128_f8f6f4 v[16:19], v[158:165], v[220:227], v[16:19]
	v_mfma_f32_16x16x128_f8f6f4 v[8:11], v[172:179], v[220:227], v[8:11]
	s_setprio 0
	s_barrier
	s_mov_b32 m0, s47
	v_lshl_add_u64 v[158:159], s[36:37], 0, v[134:135]
	global_load_lds_dwordx4 v[158:159], off
	v_lshl_add_u64 v[160:161], s[36:37], 0, v[132:133]
	s_mov_b32 m0, s48
	s_nop 0
	global_load_lds_dwordx4 v[160:161], off
	s_waitcnt vmcnt(8)
	s_waitcnt lgkmcnt(0)
	s_barrier
	s_setprio 1
	s_waitcnt lgkmcnt(0)
	v_mfma_f32_16x16x128_f8f6f4 v[52:55], v[228:235], v[196:203], v[52:55]
	v_mfma_f32_16x16x128_f8f6f4 v[44:47], v[236:243], v[196:203], v[44:47]
	v_mfma_f32_16x16x128_f8f6f4 v[36:39], v[228:235], v[204:211], v[36:39]
	v_mfma_f32_16x16x128_f8f6f4 v[28:31], v[236:243], v[204:211], v[28:31]
	v_mfma_f32_16x16x128_f8f6f4 v[20:23], v[228:235], v[212:219], v[20:23]
	v_mfma_f32_16x16x128_f8f6f4 v[12:15], v[236:243], v[212:219], v[12:15]
	v_mfma_f32_16x16x128_f8f6f4 v[4:7], v[228:235], v[220:227], v[4:7]
	v_mfma_f32_16x16x128_f8f6f4 v[0:3], v[236:243], v[220:227], v[0:3]
	s_setprio 0
	s_barrier
	ds_read_b128 v[172:175], v167 offset:32768
	ds_read_b128 v[180:183], v167 offset:34816
	ds_read_b128 v[176:179], v168 offset:32768
	ds_read_b128 v[184:187], v168 offset:34816
	s_mov_b32 m0, s52
	ds_read_b128 v[196:199], v129 offset:32768
	ds_read_b128 v[204:207], v129 offset:34816
	ds_read_b128 v[200:203], v131 offset:32768
	ds_read_b128 v[208:211], v131 offset:34816
	ds_read_b128 v[212:215], v129 offset:36864
	ds_read_b128 v[220:223], v129 offset:38912
	ds_read_b128 v[216:219], v131 offset:36864
	ds_read_b128 v[224:227], v131 offset:38912
	v_cndmask_b32_e32 v136, v152, v144, vcc
	global_load_lds_dwordx4 v139, s[38:39]
	s_mov_b32 m0, s53
	s_nop 0
	global_load_lds_dwordx4 v136, s[38:39]
	s_waitcnt vmcnt(8)
	s_waitcnt lgkmcnt(8)
	s_barrier
	s_waitcnt lgkmcnt(0)
	s_setprio 1
	s_waitcnt lgkmcnt(0)
	v_mfma_f32_16x16x128_f8f6f4 v[124:127], v[172:179], v[196:203], v[124:127]
	v_mfma_f32_16x16x128_f8f6f4 v[120:123], v[180:187], v[196:203], v[120:123]
	v_mfma_f32_16x16x128_f8f6f4 v[112:115], v[172:179], v[204:211], v[112:115]
	v_mfma_f32_16x16x128_f8f6f4 v[104:107], v[180:187], v[204:211], v[104:107]
	v_mfma_f32_16x16x128_f8f6f4 v[96:99], v[172:179], v[212:219], v[96:99]
	v_mfma_f32_16x16x128_f8f6f4 v[88:91], v[180:187], v[212:219], v[88:91]
	v_mfma_f32_16x16x128_f8f6f4 v[80:83], v[172:179], v[220:227], v[80:83]
	v_mfma_f32_16x16x128_f8f6f4 v[72:75], v[180:187], v[220:227], v[72:75]
	s_setprio 0
	s_barrier
	ds_read_b128 v[228:231], v167 offset:49152
	ds_read_b128 v[236:239], v167 offset:51200
	ds_read_b128 v[232:235], v168 offset:49152
	ds_read_b128 v[240:243], v168 offset:51200
	s_add_u32 s38, s36, 0x1800
	s_addc_u32 s39, s37, 0
	v_lshl_add_u64 v[188:189], s[38:39], 0, v[134:135]
	s_mov_b32 m0, s50
	s_nop 0
	global_load_lds_dwordx4 v[188:189], off
	v_lshl_add_u64 v[188:189], s[38:39], 0, v[132:133]
	s_mov_b32 m0, s51
	s_nop 0
	global_load_lds_dwordx4 v[188:189], off
	s_waitcnt vmcnt(8)
	s_barrier
	s_waitcnt lgkmcnt(0)
	s_setprio 1
	s_waitcnt lgkmcnt(0)
	v_mfma_f32_16x16x128_f8f6f4 v[116:119], v[228:235], v[196:203], v[116:119]
	v_mfma_f32_16x16x128_f8f6f4 v[108:111], v[236:243], v[196:203], v[108:111]
	v_mfma_f32_16x16x128_f8f6f4 v[100:103], v[228:235], v[204:211], v[100:103]
	v_mfma_f32_16x16x128_f8f6f4 v[92:95], v[236:243], v[204:211], v[92:95]
	v_mfma_f32_16x16x128_f8f6f4 v[84:87], v[228:235], v[212:219], v[84:87]
	v_mfma_f32_16x16x128_f8f6f4 v[76:79], v[236:243], v[212:219], v[76:79]
	v_mfma_f32_16x16x128_f8f6f4 v[68:71], v[228:235], v[220:227], v[68:71]
	v_mfma_f32_16x16x128_f8f6f4 v[64:67], v[236:243], v[220:227], v[64:67]
	s_setprio 0
	s_barrier
	s_mov_b32 m0, s56
	v_lshl_add_u64 v[246:247], v[246:247], 0, s[18:19]
	ds_read_b128 v[196:199], v129 offset:49152
	ds_read_b128 v[204:207], v129 offset:51200
	ds_read_b128 v[200:203], v131 offset:49152
	ds_read_b128 v[208:211], v131 offset:51200
	ds_read_b128 v[212:215], v129 offset:53248
	ds_read_b128 v[220:223], v129 offset:55296
	ds_read_b128 v[216:219], v131 offset:53248
	ds_read_b128 v[224:227], v131 offset:55296
	global_load_lds_dwordx4 v[246:247], off
	v_lshl_add_u64 v[244:245], v[244:245], 0, s[18:19]
	s_mov_b32 m0, s57
	s_nop 0
	global_load_lds_dwordx4 v[244:245], off
	s_waitcnt lgkmcnt(8)
	s_barrier
	s_waitcnt lgkmcnt(0)
	s_setprio 1
	s_waitcnt lgkmcnt(0)
	v_mfma_f32_16x16x128_f8f6f4 v[60:63], v[172:179], v[196:203], v[60:63]
	v_mfma_f32_16x16x128_f8f6f4 v[56:59], v[180:187], v[196:203], v[56:59]
	v_mfma_f32_16x16x128_f8f6f4 v[48:51], v[172:179], v[204:211], v[48:51]
	v_mfma_f32_16x16x128_f8f6f4 v[40:43], v[180:187], v[204:211], v[40:43]
	v_mfma_f32_16x16x128_f8f6f4 v[32:35], v[172:179], v[212:219], v[32:35]
	v_mfma_f32_16x16x128_f8f6f4 v[24:27], v[180:187], v[212:219], v[24:27]
	v_mfma_f32_16x16x128_f8f6f4 v[16:19], v[172:179], v[220:227], v[16:19]
	v_mfma_f32_16x16x128_f8f6f4 v[8:11], v[180:187], v[220:227], v[8:11]
	s_setprio 0
	s_barrier
	s_mov_b32 m0, s54
	v_lshl_add_u64 v[158:159], v[158:159], 0, s[18:19]
	global_load_lds_dwordx4 v[158:159], off
	v_lshl_add_u64 v[158:159], v[160:161], 0, s[18:19]
	s_mov_b32 m0, s55
	s_nop 0
	global_load_lds_dwordx4 v[158:159], off
	s_waitcnt vmcnt(8)
	s_waitcnt lgkmcnt(0)
	s_barrier
	s_setprio 1
	s_waitcnt lgkmcnt(0)
	v_mfma_f32_16x16x128_f8f6f4 v[52:55], v[228:235], v[196:203], v[52:55]
	v_mfma_f32_16x16x128_f8f6f4 v[44:47], v[236:243], v[196:203], v[44:47]
	v_mfma_f32_16x16x128_f8f6f4 v[36:39], v[228:235], v[204:211], v[36:39]
	v_mfma_f32_16x16x128_f8f6f4 v[28:31], v[236:243], v[204:211], v[28:31]
	v_mfma_f32_16x16x128_f8f6f4 v[20:23], v[228:235], v[212:219], v[20:23]
	v_mfma_f32_16x16x128_f8f6f4 v[12:15], v[236:243], v[212:219], v[12:15]
	v_mfma_f32_16x16x128_f8f6f4 v[4:7], v[228:235], v[220:227], v[4:7]
	v_mfma_f32_16x16x128_f8f6f4 v[0:3], v[236:243], v[220:227], v[0:3]
	s_setprio 0
	s_barrier
	s_add_u32 s36, s36, 0x1880
	s_addc_u32 s37, s37, 0
	s_mov_b32 m0, s58
	v_lshl_add_u64 v[158:159], s[36:37], 0, v[134:135]
	global_load_lds_dwordx4 v[158:159], off
	v_lshl_add_u64 v[158:159], s[36:37], 0, v[132:133]
	s_mov_b32 m0, s59
	s_add_i32 s69, s69, 2
	global_load_lds_dwordx4 v[158:159], off
	s_add_u32 s34, s34, 0x100
	s_addc_u32 s35, s35, 0
	s_cmp_gt_u32 s69, 3
	s_cbranch_scc0 .LBB0_313
	s_and_b64 vcc, exec, s[24:25]
	s_cbranch_vccz .LBB0_316
	s_barrier

.LBB0_334:
	v_mov_b32_e32 v161, v137
	v_mov_b32_e32 v163, v137
	s_mov_b64 s[44:45], 0
	s_mov_b64 s[10:11], -1
	s_mov_b64 s[42:43], 0
	s_add_u32 s52, s14, s44
	s_addc_u32 s53, s15, s45
	s_add_u32 s46, s52, 0x100
	s_addc_u32 s47, s53, 0
	s_and_b64 s[0:1], s[42:43], exec
	s_cselect_b32 s46, s14, s46
	s_cselect_b32 s47, s15, s47
	s_add_u32 s0, s40, s44
	s_addc_u32 s1, s41, s45
	s_add_u32 s44, s0, 0x100
	s_addc_u32 s45, s1, 0
	ds_read_b128 v[196:199], v170
	ds_read_b128 v[204:207], v170 offset:2048
	ds_read_b128 v[200:203], v171
	ds_read_b128 v[208:211], v171 offset:2048
	s_and_b64 s[0:1], s[42:43], exec
	s_cselect_b32 s51, s37, s45
	s_cselect_b32 s50, s36, s44
	s_waitcnt lgkmcnt(0)
	ds_read_b128 v[212:215], v129
	ds_read_b128 v[220:223], v129 offset:2048
	ds_read_b128 v[216:219], v133
	ds_read_b128 v[224:227], v133 offset:2048
	ds_read_b128 v[228:231], v129 offset:4096
	ds_read_b128 v[236:239], v129 offset:6144
	ds_read_b128 v[232:235], v133 offset:4096
	ds_read_b128 v[240:243], v133 offset:6144
	s_waitcnt vmcnt(6)
	s_waitcnt lgkmcnt(8)
	s_barrier
	s_waitcnt lgkmcnt(0)
	v_cndmask_b32_e64 v164, v158, v150, s[42:43]
	s_setprio 1
	s_waitcnt lgkmcnt(0)
	v_mfma_f32_16x16x128_f8f6f4 v[124:127], v[196:203], v[212:219], 0
	v_mfma_f32_16x16x128_f8f6f4 v[120:123], v[204:211], v[212:219], 0
	v_mfma_f32_16x16x128_f8f6f4 v[108:111], v[196:203], v[220:227], 0
	v_mfma_f32_16x16x128_f8f6f4 v[104:107], v[204:211], v[220:227], 0
	v_mfma_f32_16x16x128_f8f6f4 v[92:95], v[196:203], v[228:235], 0
	v_mfma_f32_16x16x128_f8f6f4 v[88:91], v[204:211], v[228:235], 0
	v_mfma_f32_16x16x128_f8f6f4 v[76:79], v[196:203], v[236:243], 0
	v_mfma_f32_16x16x128_f8f6f4 v[72:75], v[204:211], v[236:243], 0
	s_setprio 0
	s_barrier
	ds_read_b128 v[196:199], v170 offset:16384
	ds_read_b128 v[204:207], v170 offset:18432
	ds_read_b128 v[200:203], v171 offset:16384
	ds_read_b128 v[208:211], v171 offset:18432
	s_add_i32 m0, s58, 0xc000
	s_add_i32 s0, s58, 0xe000
	s_add_u32 s48, s50, 0x1000
	s_addc_u32 s49, s51, 0
	s_add_u32 s44, s50, 0x1080
	s_addc_u32 s45, s51, 0
	v_cndmask_b32_e64 v136, v156, v148, s[42:43]
	v_cndmask_b32_e64 v149, v160, v152, s[42:43]
	v_lshl_add_u64 v[252:253], s[52:53], 0, v[160:161]
	v_lshl_add_u64 v[252:253], v[252:253], 0, s[26:27]
	global_load_lds_dwordx4 v[252:253], off
	v_lshl_add_u64 v[252:253], s[52:53], 0, v[162:163]
	v_lshl_add_u64 v[252:253], v[252:253], 0, s[26:27]
	s_mov_b32 m0, s0
	s_nop 0
	global_load_lds_dwordx4 v[252:253], off
	s_barrier
	s_waitcnt lgkmcnt(0)
	s_setprio 1
	s_waitcnt lgkmcnt(0)
	v_mfma_f32_16x16x128_f8f6f4 v[116:119], v[196:203], v[212:219], 0
	v_mfma_f32_16x16x128_f8f6f4 v[112:115], v[204:211], v[212:219], 0
	v_mfma_f32_16x16x128_f8f6f4 v[100:103], v[196:203], v[220:227], 0
	v_mfma_f32_16x16x128_f8f6f4 v[96:99], v[204:211], v[220:227], 0
	v_mfma_f32_16x16x128_f8f6f4 v[84:87], v[196:203], v[228:235], 0
	v_mfma_f32_16x16x128_f8f6f4 v[80:83], v[204:211], v[228:235], 0
	v_mfma_f32_16x16x128_f8f6f4 v[68:71], v[196:203], v[236:243], 0
	v_mfma_f32_16x16x128_f8f6f4 v[64:67], v[204:211], v[236:243], 0
	s_setprio 0
	s_barrier
	ds_read_b128 v[196:199], v170
	ds_read_b128 v[204:207], v170 offset:2048
	ds_read_b128 v[200:203], v171
	ds_read_b128 v[208:211], v171 offset:2048
	s_mov_b32 m0, s58
	ds_read_b128 v[212:215], v129 offset:16384
	ds_read_b128 v[220:223], v129 offset:18432
	ds_read_b128 v[216:219], v133 offset:16384
	ds_read_b128 v[224:227], v133 offset:18432
	ds_read_b128 v[228:231], v129 offset:20480
	ds_read_b128 v[236:239], v129 offset:22528
	ds_read_b128 v[232:235], v133 offset:20480
	ds_read_b128 v[240:243], v133 offset:22528
	global_load_lds_dwordx4 v136, s[46:47]
	s_mov_b32 m0, s61
	v_mov_b32_e32 v165, v137
	global_load_lds_dwordx4 v164, s[46:47]
	s_waitcnt lgkmcnt(8)
	s_barrier
	s_waitcnt lgkmcnt(0)
	v_lshl_add_u64 v[168:169], s[46:47], 0, v[136:137]
	v_lshl_add_u64 v[190:191], s[46:47], 0, v[164:165]
	s_setprio 1
	s_waitcnt lgkmcnt(0)
	v_mfma_f32_16x16x128_f8f6f4 v[60:63], v[196:203], v[212:219], 0
	v_mfma_f32_16x16x128_f8f6f4 v[56:59], v[204:211], v[212:219], 0
	v_mfma_f32_16x16x128_f8f6f4 v[44:47], v[196:203], v[220:227], 0
	v_mfma_f32_16x16x128_f8f6f4 v[40:43], v[204:211], v[220:227], 0
	v_mfma_f32_16x16x128_f8f6f4 v[28:31], v[196:203], v[228:235], 0
	v_mfma_f32_16x16x128_f8f6f4 v[24:27], v[204:211], v[228:235], 0
	v_mfma_f32_16x16x128_f8f6f4 v[12:15], v[196:203], v[236:243], 0
	v_mfma_f32_16x16x128_f8f6f4 v[8:11], v[204:211], v[236:243], 0
	s_setprio 0
	s_barrier
	s_mov_b32 m0, s59
	v_lshl_add_u64 v[164:165], s[50:51], 0, v[130:131]
	ds_read_b128 v[196:199], v170 offset:16384
	ds_read_b128 v[204:207], v170 offset:18432
	ds_read_b128 v[200:203], v171 offset:16384
	ds_read_b128 v[208:211], v171 offset:18432
	global_load_lds_dwordx4 v[164:165], off
	v_lshl_add_u64 v[166:167], s[50:51], 0, v[134:135]
	s_mov_b32 m0, s60
	s_nop 0
	global_load_lds_dwordx4 v[166:167], off
	s_waitcnt vmcnt(8)
	s_waitcnt lgkmcnt(0)
	s_barrier
	s_setprio 1
	s_waitcnt lgkmcnt(0)
	v_mfma_f32_16x16x128_f8f6f4 v[52:55], v[196:203], v[212:219], 0
	v_mfma_f32_16x16x128_f8f6f4 v[48:51], v[204:211], v[212:219], 0
	v_mfma_f32_16x16x128_f8f6f4 v[36:39], v[196:203], v[220:227], 0
	v_mfma_f32_16x16x128_f8f6f4 v[32:35], v[204:211], v[220:227], 0
	v_mfma_f32_16x16x128_f8f6f4 v[20:23], v[196:203], v[228:235], 0
	v_mfma_f32_16x16x128_f8f6f4 v[16:19], v[204:211], v[228:235], 0
	v_mfma_f32_16x16x128_f8f6f4 v[4:7], v[196:203], v[236:243], 0
	v_mfma_f32_16x16x128_f8f6f4 v[0:3], v[204:211], v[236:243], 0
	s_setprio 0
	s_barrier
	ds_read_b128 v[196:199], v170 offset:32768
	ds_read_b128 v[204:207], v170 offset:34816
	ds_read_b128 v[200:203], v171 offset:32768
	ds_read_b128 v[208:211], v171 offset:34816
	s_mov_b32 m0, s64
	ds_read_b128 v[212:215], v129 offset:32768
	ds_read_b128 v[220:223], v129 offset:34816
	ds_read_b128 v[216:219], v133 offset:32768
	ds_read_b128 v[224:227], v133 offset:34816
	ds_read_b128 v[228:231], v129 offset:36864
	ds_read_b128 v[236:239], v129 offset:38912
	ds_read_b128 v[232:235], v133 offset:36864
	ds_read_b128 v[240:243], v133 offset:38912
	v_cndmask_b32_e64 v136, v162, v154, s[42:43]
	global_load_lds_dwordx4 v149, s[46:47]
	s_mov_b32 m0, s65
	s_nop 0
	global_load_lds_dwordx4 v136, s[46:47]
	s_waitcnt vmcnt(8)
	s_waitcnt lgkmcnt(8)
	s_barrier
	s_waitcnt lgkmcnt(0)
	s_setprio 1
	s_waitcnt lgkmcnt(0)
	v_mfma_f32_16x16x128_f8f6f4 v[124:127], v[196:203], v[212:219], v[124:127]
	v_mfma_f32_16x16x128_f8f6f4 v[120:123], v[204:211], v[212:219], v[120:123]
	v_mfma_f32_16x16x128_f8f6f4 v[108:111], v[196:203], v[220:227], v[108:111]
	v_mfma_f32_16x16x128_f8f6f4 v[104:107], v[204:211], v[220:227], v[104:107]
	v_mfma_f32_16x16x128_f8f6f4 v[92:95], v[196:203], v[228:235], v[92:95]
	v_mfma_f32_16x16x128_f8f6f4 v[88:91], v[204:211], v[228:235], v[88:91]
	v_mfma_f32_16x16x128_f8f6f4 v[76:79], v[196:203], v[236:243], v[76:79]
	v_mfma_f32_16x16x128_f8f6f4 v[72:75], v[204:211], v[236:243], v[72:75]
	s_setprio 0
	s_barrier
	ds_read_b128 v[196:199], v170 offset:49152
	ds_read_b128 v[204:207], v170 offset:51200
	ds_read_b128 v[200:203], v171 offset:49152
	ds_read_b128 v[208:211], v171 offset:51200
	v_lshl_add_u64 v[192:193], s[48:49], 0, v[130:131]
	s_mov_b32 m0, s62
	s_nop 0
	global_load_lds_dwordx4 v[192:193], off
	v_lshl_add_u64 v[192:193], s[48:49], 0, v[134:135]
	s_mov_b32 m0, s63
	s_nop 0
	global_load_lds_dwordx4 v[192:193], off
	s_waitcnt vmcnt(8)
	s_barrier
	s_waitcnt lgkmcnt(0)
	s_setprio 1
	s_waitcnt lgkmcnt(0)
	v_mfma_f32_16x16x128_f8f6f4 v[116:119], v[196:203], v[212:219], v[116:119]
	v_mfma_f32_16x16x128_f8f6f4 v[112:115], v[204:211], v[212:219], v[112:115]
	v_mfma_f32_16x16x128_f8f6f4 v[100:103], v[196:203], v[220:227], v[100:103]
	v_mfma_f32_16x16x128_f8f6f4 v[96:99], v[204:211], v[220:227], v[96:99]
	v_mfma_f32_16x16x128_f8f6f4 v[84:87], v[196:203], v[228:235], v[84:87]
	v_mfma_f32_16x16x128_f8f6f4 v[80:83], v[204:211], v[228:235], v[80:83]
	v_mfma_f32_16x16x128_f8f6f4 v[68:71], v[196:203], v[236:243], v[68:71]
	v_mfma_f32_16x16x128_f8f6f4 v[64:67], v[204:211], v[236:243], v[64:67]
	s_setprio 0
	s_barrier
	ds_read_b128 v[196:199], v170 offset:32768
	ds_read_b128 v[204:207], v170 offset:34816
	ds_read_b128 v[200:203], v171 offset:32768
	ds_read_b128 v[208:211], v171 offset:34816
	s_mov_b32 m0, s69
	v_lshl_add_u64 v[168:169], v[168:169], 0, s[26:27]
	ds_read_b128 v[212:215], v129 offset:49152
	ds_read_b128 v[220:223], v129 offset:51200
	ds_read_b128 v[216:219], v133 offset:49152
	ds_read_b128 v[224:227], v133 offset:51200
	ds_read_b128 v[228:231], v129 offset:53248
	ds_read_b128 v[236:239], v129 offset:55296
	ds_read_b128 v[232:235], v133 offset:53248
	ds_read_b128 v[240:243], v133 offset:55296
	global_load_lds_dwordx4 v[168:169], off
	v_lshl_add_u64 v[168:169], v[190:191], 0, s[26:27]
	s_mov_b32 m0, s70
	s_nop 0
	global_load_lds_dwordx4 v[168:169], off
	s_waitcnt lgkmcnt(8)
	s_barrier
	s_waitcnt lgkmcnt(0)
	s_setprio 1
	s_waitcnt lgkmcnt(0)
	v_mfma_f32_16x16x128_f8f6f4 v[60:63], v[196:203], v[212:219], v[60:63]
	v_mfma_f32_16x16x128_f8f6f4 v[56:59], v[204:211], v[212:219], v[56:59]
	v_mfma_f32_16x16x128_f8f6f4 v[44:47], v[196:203], v[220:227], v[44:47]
	v_mfma_f32_16x16x128_f8f6f4 v[40:43], v[204:211], v[220:227], v[40:43]
	v_mfma_f32_16x16x128_f8f6f4 v[28:31], v[196:203], v[228:235], v[28:31]
	v_mfma_f32_16x16x128_f8f6f4 v[24:27], v[204:211], v[228:235], v[24:27]
	v_mfma_f32_16x16x128_f8f6f4 v[12:15], v[196:203], v[236:243], v[12:15]
	v_mfma_f32_16x16x128_f8f6f4 v[8:11], v[204:211], v[236:243], v[8:11]
	s_setprio 0
	s_barrier
	s_mov_b32 m0, s67
	v_lshl_add_u64 v[164:165], v[164:165], 0, s[26:27]
	ds_read_b128 v[196:199], v170 offset:49152
	ds_read_b128 v[204:207], v170 offset:51200
	ds_read_b128 v[200:203], v171 offset:49152
	ds_read_b128 v[208:211], v171 offset:51200
	global_load_lds_dwordx4 v[164:165], off
	v_lshl_add_u64 v[164:165], v[166:167], 0, s[26:27]
	s_mov_b32 m0, s68
	s_nop 0
	global_load_lds_dwordx4 v[164:165], off
	s_waitcnt vmcnt(8)
	s_waitcnt lgkmcnt(0)
	s_barrier
	s_setprio 1
	s_waitcnt lgkmcnt(0)
	v_mfma_f32_16x16x128_f8f6f4 v[52:55], v[196:203], v[212:219], v[52:55]
	v_mfma_f32_16x16x128_f8f6f4 v[48:51], v[204:211], v[212:219], v[48:51]
	v_mfma_f32_16x16x128_f8f6f4 v[36:39], v[196:203], v[220:227], v[36:39]
	v_mfma_f32_16x16x128_f8f6f4 v[32:35], v[204:211], v[220:227], v[32:35]
	v_mfma_f32_16x16x128_f8f6f4 v[20:23], v[196:203], v[228:235], v[20:23]
	v_mfma_f32_16x16x128_f8f6f4 v[16:19], v[204:211], v[228:235], v[16:19]
	v_mfma_f32_16x16x128_f8f6f4 v[4:7], v[196:203], v[236:243], v[4:7]
	v_mfma_f32_16x16x128_f8f6f4 v[0:3], v[204:211], v[236:243], v[0:3]
	s_setprio 0
	s_barrier
	s_mov_b32 m0, s71
	v_lshl_add_u64 v[164:165], s[44:45], 0, v[130:131]
	global_load_lds_dwordx4 v[164:165], off
	v_lshl_add_u64 v[164:165], s[44:45], 0, v[134:135]
	s_mov_b32 m0, s72
	s_andn2_b64 vcc, exec, s[10:11]
	global_load_lds_dwordx4 v[164:165], off
	s_mov_b64 s[42:43], -1
	s_mov_b64 s[10:11], 0
	s_mov_b64 s[44:45], 0x100
	s_cbranch_vccz .LBB0_335
	s_branch .Lpeel_after_335
.LBB0_335:
	s_add_u32 s52, s14, s44
	s_addc_u32 s53, s15, s45
	s_add_u32 s46, s52, 0x100
	s_addc_u32 s47, s53, 0
	s_and_b64 s[0:1], s[42:43], exec
	s_cselect_b32 s46, s14, s46
	s_cselect_b32 s47, s15, s47
	s_add_u32 s0, s40, s44
	s_addc_u32 s1, s41, s45
	s_add_u32 s44, s0, 0x100
	s_addc_u32 s45, s1, 0
	ds_read_b128 v[196:199], v170
	ds_read_b128 v[204:207], v170 offset:2048
	ds_read_b128 v[200:203], v171
	ds_read_b128 v[208:211], v171 offset:2048
	s_and_b64 s[0:1], s[42:43], exec
	s_cselect_b32 s51, s37, s45
	s_cselect_b32 s50, s36, s44
	s_waitcnt lgkmcnt(0)
	ds_read_b128 v[212:215], v129
	ds_read_b128 v[220:223], v129 offset:2048
	ds_read_b128 v[216:219], v133
	ds_read_b128 v[224:227], v133 offset:2048
	ds_read_b128 v[228:231], v129 offset:4096
	ds_read_b128 v[236:239], v129 offset:6144
	ds_read_b128 v[232:235], v133 offset:4096
	ds_read_b128 v[240:243], v133 offset:6144
	s_waitcnt vmcnt(6)
	s_waitcnt lgkmcnt(8)
	s_barrier
	s_waitcnt lgkmcnt(0)
	v_cndmask_b32_e64 v164, v158, v150, s[42:43]
	s_setprio 1
	s_waitcnt lgkmcnt(0)
	v_mfma_f32_16x16x128_f8f6f4 v[124:127], v[196:203], v[212:219], v[124:127]
	v_mfma_f32_16x16x128_f8f6f4 v[120:123], v[204:211], v[212:219], v[120:123]
	v_mfma_f32_16x16x128_f8f6f4 v[108:111], v[196:203], v[220:227], v[108:111]
	v_mfma_f32_16x16x128_f8f6f4 v[104:107], v[204:211], v[220:227], v[104:107]
	v_mfma_f32_16x16x128_f8f6f4 v[92:95], v[196:203], v[228:235], v[92:95]
	v_mfma_f32_16x16x128_f8f6f4 v[88:91], v[204:211], v[228:235], v[88:91]
	v_mfma_f32_16x16x128_f8f6f4 v[76:79], v[196:203], v[236:243], v[76:79]
	v_mfma_f32_16x16x128_f8f6f4 v[72:75], v[204:211], v[236:243], v[72:75]
	s_setprio 0
	s_barrier
	ds_read_b128 v[196:199], v170 offset:16384
	ds_read_b128 v[204:207], v170 offset:18432
	ds_read_b128 v[200:203], v171 offset:16384
	ds_read_b128 v[208:211], v171 offset:18432
	s_add_i32 m0, s58, 0xc000
	s_add_i32 s0, s58, 0xe000
	s_add_u32 s48, s50, 0x1000
	s_addc_u32 s49, s51, 0
	s_add_u32 s44, s50, 0x1080
	s_addc_u32 s45, s51, 0
	v_cndmask_b32_e64 v136, v156, v148, s[42:43]
	v_cndmask_b32_e64 v149, v160, v152, s[42:43]
	v_lshl_add_u64 v[252:253], s[52:53], 0, v[160:161]
	v_lshl_add_u64 v[252:253], v[252:253], 0, s[26:27]
	global_load_lds_dwordx4 v[252:253], off
	v_lshl_add_u64 v[252:253], s[52:53], 0, v[162:163]
	v_lshl_add_u64 v[252:253], v[252:253], 0, s[26:27]
	s_mov_b32 m0, s0
	s_nop 0
	global_load_lds_dwordx4 v[252:253], off
	s_barrier
	s_waitcnt lgkmcnt(0)
	s_setprio 1
	s_waitcnt lgkmcnt(0)
	v_mfma_f32_16x16x128_f8f6f4 v[116:119], v[196:203], v[212:219], v[116:119]
	v_mfma_f32_16x16x128_f8f6f4 v[112:115], v[204:211], v[212:219], v[112:115]
	v_mfma_f32_16x16x128_f8f6f4 v[100:103], v[196:203], v[220:227], v[100:103]
	v_mfma_f32_16x16x128_f8f6f4 v[96:99], v[204:211], v[220:227], v[96:99]
	v_mfma_f32_16x16x128_f8f6f4 v[84:87], v[196:203], v[228:235], v[84:87]
	v_mfma_f32_16x16x128_f8f6f4 v[80:83], v[204:211], v[228:235], v[80:83]
	v_mfma_f32_16x16x128_f8f6f4 v[68:71], v[196:203], v[236:243], v[68:71]
	v_mfma_f32_16x16x128_f8f6f4 v[64:67], v[204:211], v[236:243], v[64:67]
	s_setprio 0
	s_barrier
	ds_read_b128 v[196:199], v170
	ds_read_b128 v[204:207], v170 offset:2048
	ds_read_b128 v[200:203], v171
	ds_read_b128 v[208:211], v171 offset:2048
	s_mov_b32 m0, s58
	ds_read_b128 v[212:215], v129 offset:16384
	ds_read_b128 v[220:223], v129 offset:18432
	ds_read_b128 v[216:219], v133 offset:16384
	ds_read_b128 v[224:227], v133 offset:18432
	ds_read_b128 v[228:231], v129 offset:20480
	ds_read_b128 v[236:239], v129 offset:22528
	ds_read_b128 v[232:235], v133 offset:20480
	ds_read_b128 v[240:243], v133 offset:22528
	global_load_lds_dwordx4 v136, s[46:47]
	s_mov_b32 m0, s61
	v_mov_b32_e32 v165, v137
	global_load_lds_dwordx4 v164, s[46:47]
	s_waitcnt lgkmcnt(8)
	s_barrier
	s_waitcnt lgkmcnt(0)
	v_lshl_add_u64 v[168:169], s[46:47], 0, v[136:137]
	v_lshl_add_u64 v[190:191], s[46:47], 0, v[164:165]
	s_setprio 1
	s_waitcnt lgkmcnt(0)
	v_mfma_f32_16x16x128_f8f6f4 v[60:63], v[196:203], v[212:219], v[60:63]
	v_mfma_f32_16x16x128_f8f6f4 v[56:59], v[204:211], v[212:219], v[56:59]
	v_mfma_f32_16x16x128_f8f6f4 v[44:47], v[196:203], v[220:227], v[44:47]
	v_mfma_f32_16x16x128_f8f6f4 v[40:43], v[204:211], v[220:227], v[40:43]
	v_mfma_f32_16x16x128_f8f6f4 v[28:31], v[196:203], v[228:235], v[28:31]
	v_mfma_f32_16x16x128_f8f6f4 v[24:27], v[204:211], v[228:235], v[24:27]
	v_mfma_f32_16x16x128_f8f6f4 v[12:15], v[196:203], v[236:243], v[12:15]
	v_mfma_f32_16x16x128_f8f6f4 v[8:11], v[204:211], v[236:243], v[8:11]
	s_setprio 0
	s_barrier
	s_mov_b32 m0, s59
	v_lshl_add_u64 v[164:165], s[50:51], 0, v[130:131]
	ds_read_b128 v[196:199], v170 offset:16384
	ds_read_b128 v[204:207], v170 offset:18432
	ds_read_b128 v[200:203], v171 offset:16384
	ds_read_b128 v[208:211], v171 offset:18432
	global_load_lds_dwordx4 v[164:165], off
	v_lshl_add_u64 v[166:167], s[50:51], 0, v[134:135]
	s_mov_b32 m0, s60
	s_nop 0
	global_load_lds_dwordx4 v[166:167], off
	s_waitcnt vmcnt(8)
	s_waitcnt lgkmcnt(0)
	s_barrier
	s_setprio 1
	s_waitcnt lgkmcnt(0)
	v_mfma_f32_16x16x128_f8f6f4 v[52:55], v[196:203], v[212:219], v[52:55]
	v_mfma_f32_16x16x128_f8f6f4 v[48:51], v[204:211], v[212:219], v[48:51]
	v_mfma_f32_16x16x128_f8f6f4 v[36:39], v[196:203], v[220:227], v[36:39]
	v_mfma_f32_16x16x128_f8f6f4 v[32:35], v[204:211], v[220:227], v[32:35]
	v_mfma_f32_16x16x128_f8f6f4 v[20:23], v[196:203], v[228:235], v[20:23]
	v_mfma_f32_16x16x128_f8f6f4 v[16:19], v[204:211], v[228:235], v[16:19]
	v_mfma_f32_16x16x128_f8f6f4 v[4:7], v[196:203], v[236:243], v[4:7]
	v_mfma_f32_16x16x128_f8f6f4 v[0:3], v[204:211], v[236:243], v[0:3]
	s_setprio 0
	s_barrier
	ds_read_b128 v[196:199], v170 offset:32768
	ds_read_b128 v[204:207], v170 offset:34816
	ds_read_b128 v[200:203], v171 offset:32768
	ds_read_b128 v[208:211], v171 offset:34816
	s_mov_b32 m0, s64
	ds_read_b128 v[212:215], v129 offset:32768
	ds_read_b128 v[220:223], v129 offset:34816
	ds_read_b128 v[216:219], v133 offset:32768
	ds_read_b128 v[224:227], v133 offset:34816
	ds_read_b128 v[228:231], v129 offset:36864
	ds_read_b128 v[236:239], v129 offset:38912
	ds_read_b128 v[232:235], v133 offset:36864
	ds_read_b128 v[240:243], v133 offset:38912
	v_cndmask_b32_e64 v136, v162, v154, s[42:43]
	global_load_lds_dwordx4 v149, s[46:47]
	s_mov_b32 m0, s65
	s_nop 0
	global_load_lds_dwordx4 v136, s[46:47]
	s_waitcnt vmcnt(8)
	s_waitcnt lgkmcnt(8)
	s_barrier
	s_waitcnt lgkmcnt(0)
	s_setprio 1
	s_waitcnt lgkmcnt(0)
	v_mfma_f32_16x16x128_f8f6f4 v[124:127], v[196:203], v[212:219], v[124:127]
	v_mfma_f32_16x16x128_f8f6f4 v[120:123], v[204:211], v[212:219], v[120:123]
	v_mfma_f32_16x16x128_f8f6f4 v[108:111], v[196:203], v[220:227], v[108:111]
	v_mfma_f32_16x16x128_f8f6f4 v[104:107], v[204:211], v[220:227], v[104:107]
	v_mfma_f32_16x16x128_f8f6f4 v[92:95], v[196:203], v[228:235], v[92:95]
	v_mfma_f32_16x16x128_f8f6f4 v[88:91], v[204:211], v[228:235], v[88:91]
	v_mfma_f32_16x16x128_f8f6f4 v[76:79], v[196:203], v[236:243], v[76:79]
	v_mfma_f32_16x16x128_f8f6f4 v[72:75], v[204:211], v[236:243], v[72:75]
	s_setprio 0
	s_barrier
	ds_read_b128 v[196:199], v170 offset:49152
	ds_read_b128 v[204:207], v170 offset:51200
	ds_read_b128 v[200:203], v171 offset:49152
	ds_read_b128 v[208:211], v171 offset:51200
	v_lshl_add_u64 v[192:193], s[48:49], 0, v[130:131]
	s_mov_b32 m0, s62
	s_nop 0
	global_load_lds_dwordx4 v[192:193], off
	v_lshl_add_u64 v[192:193], s[48:49], 0, v[134:135]
	s_mov_b32 m0, s63
	s_nop 0
	global_load_lds_dwordx4 v[192:193], off
	s_waitcnt vmcnt(8)
	s_barrier
	s_waitcnt lgkmcnt(0)
	s_setprio 1
	s_waitcnt lgkmcnt(0)
	v_mfma_f32_16x16x128_f8f6f4 v[116:119], v[196:203], v[212:219], v[116:119]
	v_mfma_f32_16x16x128_f8f6f4 v[112:115], v[204:211], v[212:219], v[112:115]
	v_mfma_f32_16x16x128_f8f6f4 v[100:103], v[196:203], v[220:227], v[100:103]
	v_mfma_f32_16x16x128_f8f6f4 v[96:99], v[204:211], v[220:227], v[96:99]
	v_mfma_f32_16x16x128_f8f6f4 v[84:87], v[196:203], v[228:235], v[84:87]
	v_mfma_f32_16x16x128_f8f6f4 v[80:83], v[204:211], v[228:235], v[80:83]
	v_mfma_f32_16x16x128_f8f6f4 v[68:71], v[196:203], v[236:243], v[68:71]
	v_mfma_f32_16x16x128_f8f6f4 v[64:67], v[204:211], v[236:243], v[64:67]
	s_setprio 0
	s_barrier
	ds_read_b128 v[196:199], v170 offset:32768
	ds_read_b128 v[204:207], v170 offset:34816
	ds_read_b128 v[200:203], v171 offset:32768
	ds_read_b128 v[208:211], v171 offset:34816
	s_mov_b32 m0, s69
	v_lshl_add_u64 v[168:169], v[168:169], 0, s[26:27]
	ds_read_b128 v[212:215], v129 offset:49152
	ds_read_b128 v[220:223], v129 offset:51200
	ds_read_b128 v[216:219], v133 offset:49152
	ds_read_b128 v[224:227], v133 offset:51200
	ds_read_b128 v[228:231], v129 offset:53248
	ds_read_b128 v[236:239], v129 offset:55296
	ds_read_b128 v[232:235], v133 offset:53248
	ds_read_b128 v[240:243], v133 offset:55296
	global_load_lds_dwordx4 v[168:169], off
	v_lshl_add_u64 v[168:169], v[190:191], 0, s[26:27]
	s_mov_b32 m0, s70
	s_nop 0
	global_load_lds_dwordx4 v[168:169], off
	s_waitcnt lgkmcnt(8)
	s_barrier
	s_waitcnt lgkmcnt(0)
	s_setprio 1
	s_waitcnt lgkmcnt(0)
	v_mfma_f32_16x16x128_f8f6f4 v[60:63], v[196:203], v[212:219], v[60:63]
	v_mfma_f32_16x16x128_f8f6f4 v[56:59], v[204:211], v[212:219], v[56:59]
	v_mfma_f32_16x16x128_f8f6f4 v[44:47], v[196:203], v[220:227], v[44:47]
	v_mfma_f32_16x16x128_f8f6f4 v[40:43], v[204:211], v[220:227], v[40:43]
	v_mfma_f32_16x16x128_f8f6f4 v[28:31], v[196:203], v[228:235], v[28:31]
	v_mfma_f32_16x16x128_f8f6f4 v[24:27], v[204:211], v[228:235], v[24:27]
	v_mfma_f32_16x16x128_f8f6f4 v[12:15], v[196:203], v[236:243], v[12:15]
	v_mfma_f32_16x16x128_f8f6f4 v[8:11], v[204:211], v[236:243], v[8:11]
	s_setprio 0
	s_barrier
	s_mov_b32 m0, s67
	v_lshl_add_u64 v[164:165], v[164:165], 0, s[26:27]
	ds_read_b128 v[196:199], v170 offset:49152
	ds_read_b128 v[204:207], v170 offset:51200
	ds_read_b128 v[200:203], v171 offset:49152
	ds_read_b128 v[208:211], v171 offset:51200
	global_load_lds_dwordx4 v[164:165], off
	v_lshl_add_u64 v[164:165], v[166:167], 0, s[26:27]
	s_mov_b32 m0, s68
	s_nop 0
	global_load_lds_dwordx4 v[164:165], off
	s_waitcnt vmcnt(8)
	s_waitcnt lgkmcnt(0)
	s_barrier
	s_setprio 1
	s_waitcnt lgkmcnt(0)
	v_mfma_f32_16x16x128_f8f6f4 v[52:55], v[196:203], v[212:219], v[52:55]
	v_mfma_f32_16x16x128_f8f6f4 v[48:51], v[204:211], v[212:219], v[48:51]
	v_mfma_f32_16x16x128_f8f6f4 v[36:39], v[196:203], v[220:227], v[36:39]
	v_mfma_f32_16x16x128_f8f6f4 v[32:35], v[204:211], v[220:227], v[32:35]
	v_mfma_f32_16x16x128_f8f6f4 v[20:23], v[196:203], v[228:235], v[20:23]
	v_mfma_f32_16x16x128_f8f6f4 v[16:19], v[204:211], v[228:235], v[16:19]
	v_mfma_f32_16x16x128_f8f6f4 v[4:7], v[196:203], v[236:243], v[4:7]
	v_mfma_f32_16x16x128_f8f6f4 v[0:3], v[204:211], v[236:243], v[0:3]
	s_setprio 0
	s_barrier
	s_mov_b32 m0, s71
	v_lshl_add_u64 v[164:165], s[44:45], 0, v[130:131]
	global_load_lds_dwordx4 v[164:165], off
	v_lshl_add_u64 v[164:165], s[44:45], 0, v[134:135]
	s_mov_b32 m0, s72
	s_andn2_b64 vcc, exec, s[10:11]
	global_load_lds_dwordx4 v[164:165], off
	s_mov_b64 s[42:43], -1
	s_mov_b64 s[10:11], 0
	s_mov_b64 s[44:45], 0x100
	s_cbranch_vccz .LBB0_335

.LBB0_595:
	s_add_u32 s40, s8, s38
	s_addc_u32 s41, s9, s39
	s_add_u32 s42, s40, 0x6ea00100
	ds_read_b128 v[176:179], v188
	ds_read_b128 v[196:199], v188 offset:2048
	ds_read_b128 v[180:183], v189
	ds_read_b128 v[200:203], v189 offset:2048
	s_addc_u32 s43, s41, 0
	s_add_u32 s68, s1, s38
	s_addc_u32 s69, s56, s39
	s_cmpk_eq_i32 s38, 0x700
	s_cselect_b64 vcc, -1, 0
	s_and_b64 s[40:41], vcc, exec
	ds_read_b128 v[204:207], v186
	ds_read_b128 v[212:215], v186 offset:2048
	ds_read_b128 v[208:211], v187
	ds_read_b128 v[216:219], v187 offset:2048
	ds_read_b128 v[220:223], v186 offset:4096
	ds_read_b128 v[228:231], v186 offset:6144
	ds_read_b128 v[224:227], v187 offset:4096
	ds_read_b128 v[232:235], v187 offset:6144
	s_waitcnt vmcnt(6)
	s_waitcnt lgkmcnt(8)
	s_barrier
	s_waitcnt lgkmcnt(0)
	v_cndmask_b32_e32 v184, v166, v139, vcc
	s_setprio 1
	s_waitcnt lgkmcnt(0)
	v_mfma_f32_16x16x128_f8f6f4 v[124:127], v[176:183], v[204:211], v[124:127]
	v_mfma_f32_16x16x128_f8f6f4 v[120:123], v[196:203], v[204:211], v[120:123]
	v_mfma_f32_16x16x128_f8f6f4 v[116:119], v[176:183], v[212:219], v[116:119]
	v_mfma_f32_16x16x128_f8f6f4 v[112:115], v[196:203], v[212:219], v[112:115]
	v_mfma_f32_16x16x128_f8f6f4 v[92:95], v[176:183], v[220:227], v[92:95]
	v_mfma_f32_16x16x128_f8f6f4 v[88:91], v[196:203], v[220:227], v[88:91]
	v_mfma_f32_16x16x128_f8f6f4 v[84:87], v[176:183], v[228:235], v[84:87]
	v_mfma_f32_16x16x128_f8f6f4 v[80:83], v[196:203], v[228:235], v[80:83]
	s_setprio 0
	s_barrier
	ds_read_b128 v[176:179], v188 offset:16384
	ds_read_b128 v[196:199], v188 offset:18432
	ds_read_b128 v[180:183], v189 offset:16384
	ds_read_b128 v[200:203], v189 offset:18432
	v_cndmask_b32_e32 v132, v151, v135, vcc
	s_cselect_b32 s43, s13, s43
	s_cselect_b32 s42, s12, s42
	s_cselect_b32 s41, s37, s69
	s_cselect_b32 s40, s36, s68
	v_cndmask_b32_e32 v155, v168, v143, vcc
	s_mov_b32 m0, s63
	v_lshl_add_u64 v[252:253], v[174:175], 0, s[38:39]
	global_load_lds_dwordx4 v[252:253], off
	v_lshl_add_u64 v[252:253], v[172:173], 0, s[38:39]
	s_mov_b32 m0, s64
	s_nop 0
	global_load_lds_dwordx4 v[252:253], off
	s_barrier
	s_waitcnt lgkmcnt(0)
	s_setprio 1
	s_waitcnt lgkmcnt(0)
	v_mfma_f32_16x16x128_f8f6f4 v[108:111], v[176:183], v[204:211], v[108:111]
	v_mfma_f32_16x16x128_f8f6f4 v[104:107], v[196:203], v[204:211], v[104:107]
	v_mfma_f32_16x16x128_f8f6f4 v[100:103], v[176:183], v[212:219], v[100:103]
	v_mfma_f32_16x16x128_f8f6f4 v[96:99], v[196:203], v[212:219], v[96:99]
	v_mfma_f32_16x16x128_f8f6f4 v[76:79], v[176:183], v[220:227], v[76:79]
	v_mfma_f32_16x16x128_f8f6f4 v[72:75], v[196:203], v[220:227], v[72:75]
	v_mfma_f32_16x16x128_f8f6f4 v[68:71], v[176:183], v[228:235], v[68:71]
	v_mfma_f32_16x16x128_f8f6f4 v[64:67], v[196:203], v[228:235], v[64:67]
	s_setprio 0
	s_barrier
	ds_read_b128 v[196:199], v188
	ds_read_b128 v[204:207], v188 offset:2048
	ds_read_b128 v[200:203], v189
	ds_read_b128 v[208:211], v189 offset:2048
	s_mov_b32 m0, s33
	ds_read_b128 v[212:215], v186 offset:16384
	ds_read_b128 v[220:223], v186 offset:18432
	ds_read_b128 v[216:219], v187 offset:16384
	ds_read_b128 v[224:227], v187 offset:18432
	ds_read_b128 v[228:231], v186 offset:20480
	ds_read_b128 v[236:239], v186 offset:22528
	ds_read_b128 v[232:235], v187 offset:20480
	ds_read_b128 v[240:243], v187 offset:22528
	global_load_lds_dwordx4 v132, s[42:43]
	s_mov_b32 m0, s46
	v_mov_b32_e32 v185, v133
	global_load_lds_dwordx4 v184, s[42:43]
	s_waitcnt lgkmcnt(8)
	s_barrier
	s_waitcnt lgkmcnt(0)
	v_lshl_add_u64 v[182:183], s[42:43], 0, v[132:133]
	v_lshl_add_u64 v[180:181], s[42:43], 0, v[184:185]
	s_setprio 1
	s_waitcnt lgkmcnt(0)
	v_mfma_f32_16x16x128_f8f6f4 v[60:63], v[196:203], v[212:219], v[60:63]
	v_mfma_f32_16x16x128_f8f6f4 v[56:59], v[204:211], v[212:219], v[56:59]
	v_mfma_f32_16x16x128_f8f6f4 v[52:55], v[196:203], v[220:227], v[52:55]
	v_mfma_f32_16x16x128_f8f6f4 v[48:51], v[204:211], v[220:227], v[48:51]
	v_mfma_f32_16x16x128_f8f6f4 v[28:31], v[196:203], v[228:235], v[28:31]
	v_mfma_f32_16x16x128_f8f6f4 v[24:27], v[204:211], v[228:235], v[24:27]
	v_mfma_f32_16x16x128_f8f6f4 v[20:23], v[196:203], v[236:243], v[20:23]
	v_mfma_f32_16x16x128_f8f6f4 v[16:19], v[204:211], v[236:243], v[16:19]
	s_setprio 0
	s_barrier
	s_mov_b32 m0, s44
	v_lshl_add_u64 v[176:177], s[40:41], 0, v[130:131]
	ds_read_b128 v[196:199], v188 offset:16384
	ds_read_b128 v[204:207], v188 offset:18432
	ds_read_b128 v[200:203], v189 offset:16384
	ds_read_b128 v[208:211], v189 offset:18432
	global_load_lds_dwordx4 v[176:177], off
	v_lshl_add_u64 v[178:179], s[40:41], 0, v[128:129]
	s_mov_b32 m0, s45
	s_nop 0
	global_load_lds_dwordx4 v[178:179], off
	s_waitcnt vmcnt(8)
	s_waitcnt lgkmcnt(0)
	s_barrier
	s_setprio 1
	s_waitcnt lgkmcnt(0)
	v_mfma_f32_16x16x128_f8f6f4 v[44:47], v[196:203], v[212:219], v[44:47]
	v_mfma_f32_16x16x128_f8f6f4 v[40:43], v[204:211], v[212:219], v[40:43]
	v_mfma_f32_16x16x128_f8f6f4 v[36:39], v[196:203], v[220:227], v[36:39]
	v_mfma_f32_16x16x128_f8f6f4 v[32:35], v[204:211], v[220:227], v[32:35]
	v_mfma_f32_16x16x128_f8f6f4 v[12:15], v[196:203], v[228:235], v[12:15]
	v_mfma_f32_16x16x128_f8f6f4 v[8:11], v[204:211], v[228:235], v[8:11]
	v_mfma_f32_16x16x128_f8f6f4 v[4:7], v[196:203], v[236:243], v[4:7]
	v_mfma_f32_16x16x128_f8f6f4 v[0:3], v[204:211], v[236:243], v[0:3]
	s_setprio 0
	s_barrier
	ds_read_b128 v[196:199], v188 offset:32768
	ds_read_b128 v[204:207], v188 offset:34816
	ds_read_b128 v[200:203], v189 offset:32768
	ds_read_b128 v[208:211], v189 offset:34816
	s_mov_b32 m0, s49
	ds_read_b128 v[212:215], v186 offset:32768
	ds_read_b128 v[220:223], v186 offset:34816
	ds_read_b128 v[216:219], v187 offset:32768
	ds_read_b128 v[224:227], v187 offset:34816
	ds_read_b128 v[228:231], v186 offset:36864
	ds_read_b128 v[236:239], v186 offset:38912
	ds_read_b128 v[232:235], v187 offset:36864
	ds_read_b128 v[240:243], v187 offset:38912
	v_cndmask_b32_e32 v132, v170, v147, vcc
	global_load_lds_dwordx4 v155, s[42:43]
	s_mov_b32 m0, s50
	s_nop 0
	global_load_lds_dwordx4 v132, s[42:43]
	s_waitcnt vmcnt(8)
	s_waitcnt lgkmcnt(8)
	s_barrier
	s_waitcnt lgkmcnt(0)
	s_setprio 1
	s_waitcnt lgkmcnt(0)
	v_mfma_f32_16x16x128_f8f6f4 v[124:127], v[196:203], v[212:219], v[124:127]
	v_mfma_f32_16x16x128_f8f6f4 v[120:123], v[204:211], v[212:219], v[120:123]
	v_mfma_f32_16x16x128_f8f6f4 v[116:119], v[196:203], v[220:227], v[116:119]
	v_mfma_f32_16x16x128_f8f6f4 v[112:115], v[204:211], v[220:227], v[112:115]
	v_mfma_f32_16x16x128_f8f6f4 v[92:95], v[196:203], v[228:235], v[92:95]
	v_mfma_f32_16x16x128_f8f6f4 v[88:91], v[204:211], v[228:235], v[88:91]
	v_mfma_f32_16x16x128_f8f6f4 v[84:87], v[196:203], v[236:243], v[84:87]
	v_mfma_f32_16x16x128_f8f6f4 v[80:83], v[204:211], v[236:243], v[80:83]
	s_setprio 0
	s_barrier
	ds_read_b128 v[196:199], v188 offset:49152
	ds_read_b128 v[204:207], v188 offset:51200
	ds_read_b128 v[200:203], v189 offset:49152
	ds_read_b128 v[208:211], v189 offset:51200
	s_add_u32 s42, s40, 0x40000
	s_addc_u32 s43, s41, 0
	v_lshl_add_u64 v[184:185], s[42:43], 0, v[130:131]
	s_mov_b32 m0, s47
	s_nop 0
	global_load_lds_dwordx4 v[184:185], off
	v_lshl_add_u64 v[184:185], s[42:43], 0, v[128:129]
	s_mov_b32 m0, s48
	s_nop 0
	global_load_lds_dwordx4 v[184:185], off
	s_waitcnt vmcnt(8)
	s_barrier
	s_waitcnt lgkmcnt(0)
	s_setprio 1
	s_waitcnt lgkmcnt(0)
	v_mfma_f32_16x16x128_f8f6f4 v[108:111], v[196:203], v[212:219], v[108:111]
	v_mfma_f32_16x16x128_f8f6f4 v[104:107], v[204:211], v[212:219], v[104:107]
	v_mfma_f32_16x16x128_f8f6f4 v[100:103], v[196:203], v[220:227], v[100:103]
	v_mfma_f32_16x16x128_f8f6f4 v[96:99], v[204:211], v[220:227], v[96:99]
	v_mfma_f32_16x16x128_f8f6f4 v[76:79], v[196:203], v[228:235], v[76:79]
	v_mfma_f32_16x16x128_f8f6f4 v[72:75], v[204:211], v[228:235], v[72:75]
	v_mfma_f32_16x16x128_f8f6f4 v[68:71], v[196:203], v[236:243], v[68:71]
	v_mfma_f32_16x16x128_f8f6f4 v[64:67], v[204:211], v[236:243], v[64:67]
	s_setprio 0
	s_barrier
	ds_read_b128 v[196:199], v188 offset:32768
	ds_read_b128 v[204:207], v188 offset:34816
	ds_read_b128 v[200:203], v189 offset:32768
	ds_read_b128 v[208:211], v189 offset:34816
	s_mov_b32 m0, s55
	v_lshl_add_u64 v[182:183], v[182:183], 0, s[20:21]
	ds_read_b128 v[212:215], v186 offset:49152
	ds_read_b128 v[220:223], v186 offset:51200
	ds_read_b128 v[216:219], v187 offset:49152
	ds_read_b128 v[224:227], v187 offset:51200
	ds_read_b128 v[228:231], v186 offset:53248
	ds_read_b128 v[236:239], v186 offset:55296
	ds_read_b128 v[232:235], v187 offset:53248
	ds_read_b128 v[240:243], v187 offset:55296
	global_load_lds_dwordx4 v[182:183], off
	v_lshl_add_u64 v[180:181], v[180:181], 0, s[20:21]
	s_mov_b32 m0, s58
	s_nop 0
	global_load_lds_dwordx4 v[180:181], off
	s_waitcnt lgkmcnt(8)
	s_barrier
	s_waitcnt lgkmcnt(0)
	s_setprio 1
	s_waitcnt lgkmcnt(0)
	v_mfma_f32_16x16x128_f8f6f4 v[60:63], v[196:203], v[212:219], v[60:63]
	v_mfma_f32_16x16x128_f8f6f4 v[56:59], v[204:211], v[212:219], v[56:59]
	v_mfma_f32_16x16x128_f8f6f4 v[52:55], v[196:203], v[220:227], v[52:55]
	v_mfma_f32_16x16x128_f8f6f4 v[48:51], v[204:211], v[220:227], v[48:51]
	v_mfma_f32_16x16x128_f8f6f4 v[28:31], v[196:203], v[228:235], v[28:31]
	v_mfma_f32_16x16x128_f8f6f4 v[24:27], v[204:211], v[228:235], v[24:27]
	v_mfma_f32_16x16x128_f8f6f4 v[20:23], v[196:203], v[236:243], v[20:23]
	v_mfma_f32_16x16x128_f8f6f4 v[16:19], v[204:211], v[236:243], v[16:19]
	s_setprio 0
	s_barrier
	s_mov_b32 m0, s53
	v_lshl_add_u64 v[176:177], v[176:177], 0, s[20:21]
	ds_read_b128 v[196:199], v188 offset:49152
	ds_read_b128 v[204:207], v188 offset:51200
	ds_read_b128 v[200:203], v189 offset:49152
	ds_read_b128 v[208:211], v189 offset:51200
	global_load_lds_dwordx4 v[176:177], off
	v_lshl_add_u64 v[176:177], v[178:179], 0, s[20:21]
	s_mov_b32 m0, s54
	s_nop 0
	global_load_lds_dwordx4 v[176:177], off
	s_waitcnt vmcnt(8)
	s_waitcnt lgkmcnt(0)
	s_barrier
	s_setprio 1
	s_waitcnt lgkmcnt(0)
	v_mfma_f32_16x16x128_f8f6f4 v[44:47], v[196:203], v[212:219], v[44:47]
	v_mfma_f32_16x16x128_f8f6f4 v[40:43], v[204:211], v[212:219], v[40:43]
	v_mfma_f32_16x16x128_f8f6f4 v[36:39], v[196:203], v[220:227], v[36:39]
	v_mfma_f32_16x16x128_f8f6f4 v[32:35], v[204:211], v[220:227], v[32:35]
	v_mfma_f32_16x16x128_f8f6f4 v[12:15], v[196:203], v[228:235], v[12:15]
	v_mfma_f32_16x16x128_f8f6f4 v[8:11], v[204:211], v[228:235], v[8:11]
	v_mfma_f32_16x16x128_f8f6f4 v[4:7], v[196:203], v[236:243], v[4:7]
	v_mfma_f32_16x16x128_f8f6f4 v[0:3], v[204:211], v[236:243], v[0:3]
	s_setprio 0
	s_barrier
	s_add_u32 s40, s40, 0x40080
	s_addc_u32 s41, s41, 0
	s_mov_b32 m0, s59
	v_lshl_add_u64 v[176:177], s[40:41], 0, v[130:131]
	global_load_lds_dwordx4 v[176:177], off
	v_lshl_add_u64 v[176:177], s[40:41], 0, v[128:129]
	s_mov_b32 m0, s60
	s_add_i32 s57, s57, 2
	global_load_lds_dwordx4 v[176:177], off
	s_add_u32 s38, s38, 0x100
	s_addc_u32 s39, s39, 0
	s_cmp_gt_u32 s57, 13
	s_cbranch_scc0 .LBB0_595
	s_and_b64 vcc, exec, s[26:27]
	s_cbranch_vccz .LBB0_598
	s_barrier

.LBB0_756:
	s_add_u32 s38, s8, s36
	s_addc_u32 s39, s9, s37
	s_add_u32 s40, s38, 0x14000100
	ds_read_b128 v[144:147], v154
	ds_read_b128 v[168:171], v154 offset:2048
	ds_read_b128 v[148:151], v155
	ds_read_b128 v[172:175], v155 offset:2048
	s_addc_u32 s41, s39, 0
	s_add_u32 s68, s0, s36
	s_addc_u32 s69, s1, s37
	s_cmpk_eq_i32 s36, 0x700
	s_cselect_b64 vcc, -1, 0
	s_and_b64 s[38:39], vcc, exec
	ds_read_b128 v[176:179], v152
	ds_read_b128 v[184:187], v152 offset:2048
	ds_read_b128 v[180:183], v153
	ds_read_b128 v[188:191], v153 offset:2048
	ds_read_b128 v[196:199], v152 offset:4096
	ds_read_b128 v[204:207], v152 offset:6144
	ds_read_b128 v[200:203], v153 offset:4096
	ds_read_b128 v[208:211], v153 offset:6144
	s_waitcnt vmcnt(6)
	s_waitcnt lgkmcnt(8)
	s_barrier
	s_waitcnt lgkmcnt(0)
	v_cndmask_b32_e32 v192, v134, v163, vcc
	s_setprio 1
	s_waitcnt lgkmcnt(0)
	v_mfma_f32_16x16x128_f8f6f4 v[124:127], v[144:151], v[176:183], v[124:127]
	v_mfma_f32_16x16x128_f8f6f4 v[120:123], v[168:175], v[176:183], v[120:123]
	v_mfma_f32_16x16x128_f8f6f4 v[108:111], v[144:151], v[184:191], v[108:111]
	v_mfma_f32_16x16x128_f8f6f4 v[104:107], v[168:175], v[184:191], v[104:107]
	v_mfma_f32_16x16x128_f8f6f4 v[92:95], v[144:151], v[196:203], v[92:95]
	v_mfma_f32_16x16x128_f8f6f4 v[88:91], v[168:175], v[196:203], v[88:91]
	v_mfma_f32_16x16x128_f8f6f4 v[76:79], v[144:151], v[204:211], v[76:79]
	v_mfma_f32_16x16x128_f8f6f4 v[72:75], v[168:175], v[204:211], v[72:75]
	s_setprio 0
	s_barrier
	ds_read_b128 v[234:237], v154 offset:16384
	ds_read_b128 v[242:245], v154 offset:18432
	ds_read_b128 v[238:241], v155 offset:16384
	ds_read_b128 v[246:249], v155 offset:18432
	v_cndmask_b32_e32 v132, v166, v162, vcc
	s_cselect_b32 s41, s11, s41
	s_cselect_b32 s40, s10, s40
	s_cselect_b32 s39, s31, s69
	s_cselect_b32 s38, s30, s68
	v_cndmask_b32_e32 v137, v136, v164, vcc
	s_mov_b32 m0, s66
	v_lshl_add_u64 v[220:221], v[142:143], 0, s[36:37]
	global_load_lds_dwordx4 v[220:221], off
	v_lshl_add_u64 v[220:221], v[140:141], 0, s[36:37]
	s_mov_b32 m0, s67
	s_nop 0
	global_load_lds_dwordx4 v[220:221], off
	s_barrier
	s_waitcnt lgkmcnt(0)
	s_setprio 1
	s_waitcnt lgkmcnt(0)
	v_mfma_f32_16x16x128_f8f6f4 v[116:119], v[234:241], v[176:183], v[116:119]
	v_mfma_f32_16x16x128_f8f6f4 v[112:115], v[242:249], v[176:183], v[112:115]
	v_mfma_f32_16x16x128_f8f6f4 v[100:103], v[234:241], v[184:191], v[100:103]
	v_mfma_f32_16x16x128_f8f6f4 v[96:99], v[242:249], v[184:191], v[96:99]
	v_mfma_f32_16x16x128_f8f6f4 v[84:87], v[234:241], v[196:203], v[84:87]
	v_mfma_f32_16x16x128_f8f6f4 v[80:83], v[242:249], v[196:203], v[80:83]
	v_mfma_f32_16x16x128_f8f6f4 v[68:71], v[234:241], v[204:211], v[68:71]
	v_mfma_f32_16x16x128_f8f6f4 v[64:67], v[242:249], v[204:211], v[64:67]
	s_setprio 0
	s_barrier
	s_mov_b32 m0, s35
	ds_read_b128 v[184:187], v152 offset:16384
	ds_read_b128 v[196:199], v152 offset:18432
	ds_read_b128 v[188:191], v153 offset:16384
	ds_read_b128 v[200:203], v153 offset:18432
	ds_read_b128 v[204:207], v152 offset:20480
	ds_read_b128 v[212:215], v152 offset:22528
	ds_read_b128 v[208:211], v153 offset:20480
	ds_read_b128 v[216:219], v153 offset:22528
	global_load_lds_dwordx4 v132, s[40:41]
	s_mov_b32 m0, s45
	v_mov_b32_e32 v193, v133
	global_load_lds_dwordx4 v192, s[40:41]
	s_waitcnt lgkmcnt(8)
	s_barrier
	s_waitcnt lgkmcnt(0)
	v_lshl_add_u64 v[252:253], s[40:41], 0, v[132:133]
	v_lshl_add_u64 v[250:251], s[40:41], 0, v[192:193]
	s_setprio 1
	s_waitcnt lgkmcnt(0)
	v_mfma_f32_16x16x128_f8f6f4 v[60:63], v[144:151], v[184:191], v[60:63]
	v_mfma_f32_16x16x128_f8f6f4 v[56:59], v[168:175], v[184:191], v[56:59]
	v_mfma_f32_16x16x128_f8f6f4 v[44:47], v[144:151], v[196:203], v[44:47]
	v_mfma_f32_16x16x128_f8f6f4 v[40:43], v[168:175], v[196:203], v[40:43]
	v_mfma_f32_16x16x128_f8f6f4 v[28:31], v[144:151], v[204:211], v[28:31]
	v_mfma_f32_16x16x128_f8f6f4 v[24:27], v[168:175], v[204:211], v[24:27]
	v_mfma_f32_16x16x128_f8f6f4 v[12:15], v[144:151], v[212:219], v[12:15]
	v_mfma_f32_16x16x128_f8f6f4 v[8:11], v[168:175], v[212:219], v[8:11]
	s_setprio 0
	s_barrier
	s_mov_b32 m0, s43
	v_lshl_add_u64 v[144:145], s[38:39], 0, v[130:131]
	global_load_lds_dwordx4 v[144:145], off
	v_lshl_add_u64 v[146:147], s[38:39], 0, v[128:129]
	s_mov_b32 m0, s44
	s_nop 0
	global_load_lds_dwordx4 v[146:147], off
	s_waitcnt vmcnt(8)
	s_waitcnt lgkmcnt(0)
	s_barrier
	s_setprio 1
	s_waitcnt lgkmcnt(0)
	v_mfma_f32_16x16x128_f8f6f4 v[52:55], v[234:241], v[184:191], v[52:55]
	v_mfma_f32_16x16x128_f8f6f4 v[48:51], v[242:249], v[184:191], v[48:51]
	v_mfma_f32_16x16x128_f8f6f4 v[36:39], v[234:241], v[196:203], v[36:39]
	v_mfma_f32_16x16x128_f8f6f4 v[32:35], v[242:249], v[196:203], v[32:35]
	v_mfma_f32_16x16x128_f8f6f4 v[20:23], v[234:241], v[204:211], v[20:23]
	v_mfma_f32_16x16x128_f8f6f4 v[16:19], v[242:249], v[204:211], v[16:19]
	v_mfma_f32_16x16x128_f8f6f4 v[4:7], v[234:241], v[212:219], v[4:7]
	v_mfma_f32_16x16x128_f8f6f4 v[0:3], v[242:249], v[212:219], v[0:3]
	s_setprio 0
	s_barrier
	ds_read_b128 v[168:171], v154 offset:32768
	ds_read_b128 v[176:179], v154 offset:34816
	ds_read_b128 v[172:175], v155 offset:32768
	ds_read_b128 v[180:183], v155 offset:34816
	s_mov_b32 m0, s48
	ds_read_b128 v[184:187], v152 offset:32768
	ds_read_b128 v[196:199], v152 offset:34816
	ds_read_b128 v[188:191], v153 offset:32768
	ds_read_b128 v[200:203], v153 offset:34816
	ds_read_b128 v[204:207], v152 offset:36864
	ds_read_b128 v[212:215], v152 offset:38912
	ds_read_b128 v[208:211], v153 offset:36864
	ds_read_b128 v[216:219], v153 offset:38912
	v_cndmask_b32_e32 v132, v138, v165, vcc
	global_load_lds_dwordx4 v137, s[40:41]
	s_mov_b32 m0, s49
	s_nop 0
	global_load_lds_dwordx4 v132, s[40:41]
	s_waitcnt vmcnt(8)
	s_waitcnt lgkmcnt(8)
	s_barrier
	s_waitcnt lgkmcnt(0)
	s_setprio 1
	s_waitcnt lgkmcnt(0)
	v_mfma_f32_16x16x128_f8f6f4 v[124:127], v[168:175], v[184:191], v[124:127]
	v_mfma_f32_16x16x128_f8f6f4 v[120:123], v[176:183], v[184:191], v[120:123]
	v_mfma_f32_16x16x128_f8f6f4 v[108:111], v[168:175], v[196:203], v[108:111]
	v_mfma_f32_16x16x128_f8f6f4 v[104:107], v[176:183], v[196:203], v[104:107]
	v_mfma_f32_16x16x128_f8f6f4 v[92:95], v[168:175], v[204:211], v[92:95]
	v_mfma_f32_16x16x128_f8f6f4 v[88:91], v[176:183], v[204:211], v[88:91]
	v_mfma_f32_16x16x128_f8f6f4 v[76:79], v[168:175], v[212:219], v[76:79]
	v_mfma_f32_16x16x128_f8f6f4 v[72:75], v[176:183], v[212:219], v[72:75]
	s_setprio 0
	s_barrier
	ds_read_b128 v[234:237], v154 offset:49152
	ds_read_b128 v[242:245], v154 offset:51200
	ds_read_b128 v[238:241], v155 offset:49152
	ds_read_b128 v[246:249], v155 offset:51200
	s_add_u32 s40, s38, 0x4000
	s_addc_u32 s41, s39, 0
	v_lshl_add_u64 v[192:193], s[40:41], 0, v[130:131]
	s_mov_b32 m0, s46
	s_nop 0
	global_load_lds_dwordx4 v[192:193], off
	v_lshl_add_u64 v[192:193], s[40:41], 0, v[128:129]
	s_mov_b32 m0, s47
	s_nop 0
	global_load_lds_dwordx4 v[192:193], off
	s_waitcnt vmcnt(8)
	s_barrier
	s_waitcnt lgkmcnt(0)
	s_setprio 1
	s_waitcnt lgkmcnt(0)
	v_mfma_f32_16x16x128_f8f6f4 v[116:119], v[234:241], v[184:191], v[116:119]
	v_mfma_f32_16x16x128_f8f6f4 v[112:115], v[242:249], v[184:191], v[112:115]
	v_mfma_f32_16x16x128_f8f6f4 v[100:103], v[234:241], v[196:203], v[100:103]
	v_mfma_f32_16x16x128_f8f6f4 v[96:99], v[242:249], v[196:203], v[96:99]
	v_mfma_f32_16x16x128_f8f6f4 v[84:87], v[234:241], v[204:211], v[84:87]
	v_mfma_f32_16x16x128_f8f6f4 v[80:83], v[242:249], v[204:211], v[80:83]
	v_mfma_f32_16x16x128_f8f6f4 v[68:71], v[234:241], v[212:219], v[68:71]
	v_mfma_f32_16x16x128_f8f6f4 v[64:67], v[242:249], v[212:219], v[64:67]
	s_setprio 0
	s_barrier
	s_mov_b32 m0, s60
	v_lshl_add_u64 v[252:253], v[252:253], 0, s[16:17]
	ds_read_b128 v[184:187], v152 offset:49152
	ds_read_b128 v[196:199], v152 offset:51200
	ds_read_b128 v[188:191], v153 offset:49152
	ds_read_b128 v[200:203], v153 offset:51200
	ds_read_b128 v[204:207], v152 offset:53248
	ds_read_b128 v[212:215], v152 offset:55296
	ds_read_b128 v[208:211], v153 offset:53248
	ds_read_b128 v[216:219], v153 offset:55296
	global_load_lds_dwordx4 v[252:253], off
	v_lshl_add_u64 v[250:251], v[250:251], 0, s[16:17]
	s_mov_b32 m0, s61
	s_nop 0
	global_load_lds_dwordx4 v[250:251], off
	s_waitcnt lgkmcnt(8)
	s_barrier
	s_waitcnt lgkmcnt(0)
	s_setprio 1
	s_waitcnt lgkmcnt(0)
	v_mfma_f32_16x16x128_f8f6f4 v[60:63], v[168:175], v[184:191], v[60:63]
	v_mfma_f32_16x16x128_f8f6f4 v[56:59], v[176:183], v[184:191], v[56:59]
	v_mfma_f32_16x16x128_f8f6f4 v[44:47], v[168:175], v[196:203], v[44:47]
	v_mfma_f32_16x16x128_f8f6f4 v[40:43], v[176:183], v[196:203], v[40:43]
	v_mfma_f32_16x16x128_f8f6f4 v[28:31], v[168:175], v[204:211], v[28:31]
	v_mfma_f32_16x16x128_f8f6f4 v[24:27], v[176:183], v[204:211], v[24:27]
	v_mfma_f32_16x16x128_f8f6f4 v[12:15], v[168:175], v[212:219], v[12:15]
	v_mfma_f32_16x16x128_f8f6f4 v[8:11], v[176:183], v[212:219], v[8:11]
	s_setprio 0
	s_barrier
	s_mov_b32 m0, s58
	v_lshl_add_u64 v[144:145], v[144:145], 0, s[16:17]
	global_load_lds_dwordx4 v[144:145], off
	v_lshl_add_u64 v[144:145], v[146:147], 0, s[16:17]
	s_mov_b32 m0, s59
	s_nop 0
	global_load_lds_dwordx4 v[144:145], off
	s_waitcnt vmcnt(8)
	s_waitcnt lgkmcnt(0)
	s_barrier
	s_setprio 1
	s_waitcnt lgkmcnt(0)
	v_mfma_f32_16x16x128_f8f6f4 v[52:55], v[234:241], v[184:191], v[52:55]
	v_mfma_f32_16x16x128_f8f6f4 v[48:51], v[242:249], v[184:191], v[48:51]
	v_mfma_f32_16x16x128_f8f6f4 v[36:39], v[234:241], v[196:203], v[36:39]
	v_mfma_f32_16x16x128_f8f6f4 v[32:35], v[242:249], v[196:203], v[32:35]
	v_mfma_f32_16x16x128_f8f6f4 v[20:23], v[234:241], v[204:211], v[20:23]
	v_mfma_f32_16x16x128_f8f6f4 v[16:19], v[242:249], v[204:211], v[16:19]
	v_mfma_f32_16x16x128_f8f6f4 v[4:7], v[234:241], v[212:219], v[4:7]
	v_mfma_f32_16x16x128_f8f6f4 v[0:3], v[242:249], v[212:219], v[0:3]
	s_setprio 0
	s_barrier
	s_add_u32 s38, s38, 0x4080
	s_addc_u32 s39, s39, 0
	s_mov_b32 m0, s62
	v_lshl_add_u64 v[144:145], s[38:39], 0, v[130:131]
	global_load_lds_dwordx4 v[144:145], off
	v_lshl_add_u64 v[144:145], s[38:39], 0, v[128:129]
	s_mov_b32 m0, s63
	s_add_i32 s57, s57, 2
	global_load_lds_dwordx4 v[144:145], off
	s_add_u32 s36, s36, 0x100
	s_addc_u32 s37, s37, 0
	s_cmp_gt_u32 s57, 13
	s_cbranch_scc0 .LBB0_756
	s_and_b64 vcc, exec, s[20:21]
	s_cbranch_vccz .LBB0_759
	s_barrier

.LBB0_962:
	s_add_u32 s50, s20, s48
	s_addc_u32 s51, s21, s49
	ds_read_b128 v[186:189], v197
	ds_read_b128 v[202:205], v197 offset:2048
	ds_read_b128 v[190:193], v198
	ds_read_b128 v[206:209], v198 offset:2048
	s_add_u32 s52, s50, 0x14000100
	s_addc_u32 s53, s51, 0
	s_and_b64 s[50:51], s[16:17], exec
	s_cselect_b32 s53, s27, s53
	s_cselect_b32 s52, s26, s52
	s_add_u32 s77, s56, s48
	s_addc_u32 s78, s57, s49
	s_and_b64 s[50:51], s[16:17], exec
	s_cselect_b32 s51, s43, s78
	s_cselect_b32 s50, s42, s77
	ds_read_b128 v[210:213], v195
	ds_read_b128 v[218:221], v195 offset:2048
	ds_read_b128 v[214:217], v196
	ds_read_b128 v[222:225], v196 offset:2048
	ds_read_b128 v[226:229], v195 offset:4096
	ds_read_b128 v[234:237], v195 offset:6144
	ds_read_b128 v[230:233], v196 offset:4096
	ds_read_b128 v[238:241], v196 offset:6144
	s_waitcnt vmcnt(6)
	s_waitcnt lgkmcnt(8)
	s_barrier
	s_waitcnt lgkmcnt(0)
	s_setprio 1
	s_waitcnt lgkmcnt(0)
	v_mfma_f32_16x16x128_f8f6f4 v[124:127], v[186:193], v[210:217], v[124:127]
	v_mfma_f32_16x16x128_f8f6f4 v[120:123], v[202:209], v[210:217], v[120:123]
	v_mfma_f32_16x16x128_f8f6f4 v[108:111], v[186:193], v[218:225], v[108:111]
	v_mfma_f32_16x16x128_f8f6f4 v[104:107], v[202:209], v[218:225], v[104:107]
	v_mfma_f32_16x16x128_f8f6f4 v[92:95], v[186:193], v[226:233], v[92:95]
	v_mfma_f32_16x16x128_f8f6f4 v[88:91], v[202:209], v[226:233], v[88:91]
	v_mfma_f32_16x16x128_f8f6f4 v[76:79], v[186:193], v[234:241], v[76:79]
	v_mfma_f32_16x16x128_f8f6f4 v[72:75], v[202:209], v[234:241], v[72:75]
	s_setprio 0
	s_barrier
	ds_read_b128 v[186:189], v197 offset:16384
	ds_read_b128 v[202:205], v197 offset:18432
	ds_read_b128 v[190:193], v198 offset:16384
	ds_read_b128 v[206:209], v198 offset:18432
	v_cndmask_b32_e64 v136, v175, v181, s[16:17]
	v_cndmask_b32_e64 v177, v176, v173, s[16:17]
	v_lshl_add_u64 v[242:243], v[184:185], 0, s[48:49]
	s_add_i32 m0, s45, 0xc000
	s_nop 0
	global_load_lds_dwordx4 v[242:243], off
	v_lshl_add_u64 v[242:243], v[182:183], 0, s[48:49]
	s_add_i32 m0, s45, 0xe000
	v_cndmask_b32_e64 v250, v178, v179, s[16:17]
	global_load_lds_dwordx4 v[242:243], off
	s_barrier
	s_waitcnt lgkmcnt(0)
	s_setprio 1
	s_waitcnt lgkmcnt(0)
	v_mfma_f32_16x16x128_f8f6f4 v[116:119], v[186:193], v[210:217], v[116:119]
	v_mfma_f32_16x16x128_f8f6f4 v[112:115], v[202:209], v[210:217], v[112:115]
	v_mfma_f32_16x16x128_f8f6f4 v[100:103], v[186:193], v[218:225], v[100:103]
	v_mfma_f32_16x16x128_f8f6f4 v[96:99], v[202:209], v[218:225], v[96:99]
	v_mfma_f32_16x16x128_f8f6f4 v[84:87], v[186:193], v[226:233], v[84:87]
	v_mfma_f32_16x16x128_f8f6f4 v[80:83], v[202:209], v[226:233], v[80:83]
	v_mfma_f32_16x16x128_f8f6f4 v[68:71], v[186:193], v[234:241], v[68:71]
	v_mfma_f32_16x16x128_f8f6f4 v[64:67], v[202:209], v[234:241], v[64:67]
	s_setprio 0
	s_barrier
	ds_read_b128 v[202:205], v197
	ds_read_b128 v[210:213], v197 offset:2048
	ds_read_b128 v[206:209], v198
	ds_read_b128 v[214:217], v198 offset:2048
	s_mov_b32 m0, s45
	ds_read_b128 v[218:221], v195 offset:16384
	ds_read_b128 v[226:229], v195 offset:18432
	ds_read_b128 v[222:225], v196 offset:16384
	ds_read_b128 v[230:233], v196 offset:18432
	ds_read_b128 v[234:237], v195 offset:20480
	ds_read_b128 v[242:245], v195 offset:22528
	ds_read_b128 v[238:241], v196 offset:20480
	ds_read_b128 v[246:249], v196 offset:22528
	global_load_lds_dwordx4 v136, s[52:53]
	s_mov_b32 m0, s62
	v_mov_b32_e32 v251, v137
	global_load_lds_dwordx4 v250, s[52:53]
	s_waitcnt lgkmcnt(8)
	s_barrier
	s_waitcnt lgkmcnt(0)
	v_lshl_add_u64 v[192:193], s[52:53], 0, v[136:137]
	v_lshl_add_u64 v[190:191], s[52:53], 0, v[250:251]
	s_setprio 1
	s_waitcnt lgkmcnt(0)
	v_mfma_f32_16x16x128_f8f6f4 v[60:63], v[202:209], v[218:225], v[60:63]
	v_mfma_f32_16x16x128_f8f6f4 v[56:59], v[210:217], v[218:225], v[56:59]
	v_mfma_f32_16x16x128_f8f6f4 v[44:47], v[202:209], v[226:233], v[44:47]
	v_mfma_f32_16x16x128_f8f6f4 v[40:43], v[210:217], v[226:233], v[40:43]
	v_mfma_f32_16x16x128_f8f6f4 v[28:31], v[202:209], v[234:241], v[28:31]
	v_mfma_f32_16x16x128_f8f6f4 v[24:27], v[210:217], v[234:241], v[24:27]
	v_mfma_f32_16x16x128_f8f6f4 v[12:15], v[202:209], v[242:249], v[12:15]
	v_mfma_f32_16x16x128_f8f6f4 v[8:11], v[210:217], v[242:249], v[8:11]
	s_setprio 0
	s_barrier
	s_mov_b32 m0, s60
	v_lshl_add_u64 v[186:187], s[50:51], 0, v[138:139]
	ds_read_b128 v[202:205], v197 offset:16384
	ds_read_b128 v[210:213], v197 offset:18432
	ds_read_b128 v[206:209], v198 offset:16384
	ds_read_b128 v[214:217], v198 offset:18432
	global_load_lds_dwordx4 v[186:187], off
	v_lshl_add_u64 v[188:189], s[50:51], 0, v[140:141]
	s_mov_b32 m0, s61
	s_nop 0
	global_load_lds_dwordx4 v[188:189], off
	s_waitcnt vmcnt(8)
	s_waitcnt lgkmcnt(0)
	s_barrier
	s_setprio 1
	s_waitcnt lgkmcnt(0)
	v_mfma_f32_16x16x128_f8f6f4 v[52:55], v[202:209], v[218:225], v[52:55]
	v_mfma_f32_16x16x128_f8f6f4 v[48:51], v[210:217], v[218:225], v[48:51]
	v_mfma_f32_16x16x128_f8f6f4 v[36:39], v[202:209], v[226:233], v[36:39]
	v_mfma_f32_16x16x128_f8f6f4 v[32:35], v[210:217], v[226:233], v[32:35]
	v_mfma_f32_16x16x128_f8f6f4 v[20:23], v[202:209], v[234:241], v[20:23]
	v_mfma_f32_16x16x128_f8f6f4 v[16:19], v[210:217], v[234:241], v[16:19]
	v_mfma_f32_16x16x128_f8f6f4 v[4:7], v[202:209], v[242:249], v[4:7]
	v_mfma_f32_16x16x128_f8f6f4 v[0:3], v[210:217], v[242:249], v[0:3]
	s_setprio 0
	s_barrier
	ds_read_b128 v[202:205], v197 offset:32768
	ds_read_b128 v[210:213], v197 offset:34816
	ds_read_b128 v[206:209], v198 offset:32768
	ds_read_b128 v[214:217], v198 offset:34816
	s_mov_b32 m0, s65
	v_cndmask_b32_e64 v136, v180, v199, s[16:17]
	s_add_u32 s16, s50, 0x4000
	ds_read_b128 v[218:221], v195 offset:32768
	ds_read_b128 v[226:229], v195 offset:34816
	ds_read_b128 v[222:225], v196 offset:32768
	ds_read_b128 v[230:233], v196 offset:34816
	ds_read_b128 v[234:237], v195 offset:36864
	ds_read_b128 v[242:245], v195 offset:38912
	ds_read_b128 v[238:241], v196 offset:36864
	ds_read_b128 v[246:249], v196 offset:38912
	global_load_lds_dwordx4 v177, s[52:53]
	s_mov_b32 m0, s66
	s_addc_u32 s17, s51, 0
	global_load_lds_dwordx4 v136, s[52:53]
	s_waitcnt vmcnt(8)
	s_waitcnt lgkmcnt(8)
	s_barrier
	s_waitcnt lgkmcnt(0)
	s_setprio 1
	s_waitcnt lgkmcnt(0)
	v_mfma_f32_16x16x128_f8f6f4 v[124:127], v[202:209], v[218:225], v[124:127]
	v_mfma_f32_16x16x128_f8f6f4 v[120:123], v[210:217], v[218:225], v[120:123]
	v_mfma_f32_16x16x128_f8f6f4 v[108:111], v[202:209], v[226:233], v[108:111]
	v_mfma_f32_16x16x128_f8f6f4 v[104:107], v[210:217], v[226:233], v[104:107]
	v_mfma_f32_16x16x128_f8f6f4 v[92:95], v[202:209], v[234:241], v[92:95]
	v_mfma_f32_16x16x128_f8f6f4 v[88:91], v[210:217], v[234:241], v[88:91]
	v_mfma_f32_16x16x128_f8f6f4 v[76:79], v[202:209], v[242:249], v[76:79]
	v_mfma_f32_16x16x128_f8f6f4 v[72:75], v[210:217], v[242:249], v[72:75]
	s_setprio 0
	s_barrier
	ds_read_b128 v[202:205], v197 offset:49152
	ds_read_b128 v[210:213], v197 offset:51200
	ds_read_b128 v[206:209], v198 offset:49152
	ds_read_b128 v[214:217], v198 offset:51200
	v_lshl_add_u64 v[250:251], s[16:17], 0, v[138:139]
	s_mov_b32 m0, s63
	s_nop 0
	global_load_lds_dwordx4 v[250:251], off
	v_lshl_add_u64 v[250:251], s[16:17], 0, v[140:141]
	s_mov_b32 m0, s64
	s_nop 0
	global_load_lds_dwordx4 v[250:251], off
	s_waitcnt vmcnt(8)
	s_barrier
	s_waitcnt lgkmcnt(0)
	s_setprio 1
	s_waitcnt lgkmcnt(0)
	v_mfma_f32_16x16x128_f8f6f4 v[116:119], v[202:209], v[218:225], v[116:119]
	v_mfma_f32_16x16x128_f8f6f4 v[112:115], v[210:217], v[218:225], v[112:115]
	v_mfma_f32_16x16x128_f8f6f4 v[100:103], v[202:209], v[226:233], v[100:103]
	v_mfma_f32_16x16x128_f8f6f4 v[96:99], v[210:217], v[226:233], v[96:99]
	v_mfma_f32_16x16x128_f8f6f4 v[84:87], v[202:209], v[234:241], v[84:87]
	v_mfma_f32_16x16x128_f8f6f4 v[80:83], v[210:217], v[234:241], v[80:83]
	v_mfma_f32_16x16x128_f8f6f4 v[68:71], v[202:209], v[242:249], v[68:71]
	v_mfma_f32_16x16x128_f8f6f4 v[64:67], v[210:217], v[242:249], v[64:67]
	s_setprio 0
	s_barrier
	ds_read_b128 v[202:205], v197 offset:32768
	ds_read_b128 v[210:213], v197 offset:34816
	ds_read_b128 v[206:209], v198 offset:32768
	ds_read_b128 v[214:217], v198 offset:34816
	s_mov_b32 m0, s69
	v_lshl_add_u64 v[192:193], v[192:193], 0, s[34:35]
	ds_read_b128 v[218:221], v195 offset:49152
	ds_read_b128 v[226:229], v195 offset:51200
	ds_read_b128 v[222:225], v196 offset:49152
	ds_read_b128 v[230:233], v196 offset:51200
	ds_read_b128 v[234:237], v195 offset:53248
	ds_read_b128 v[242:245], v195 offset:55296
	ds_read_b128 v[238:241], v196 offset:53248
	ds_read_b128 v[246:249], v196 offset:55296
	global_load_lds_dwordx4 v[192:193], off
	v_lshl_add_u64 v[190:191], v[190:191], 0, s[34:35]
	s_mov_b32 m0, s70
	s_nop 0
	global_load_lds_dwordx4 v[190:191], off
	s_waitcnt lgkmcnt(8)
	s_barrier
	s_waitcnt lgkmcnt(0)
	s_setprio 1
	s_waitcnt lgkmcnt(0)
	v_mfma_f32_16x16x128_f8f6f4 v[60:63], v[202:209], v[218:225], v[60:63]
	v_mfma_f32_16x16x128_f8f6f4 v[56:59], v[210:217], v[218:225], v[56:59]
	v_mfma_f32_16x16x128_f8f6f4 v[44:47], v[202:209], v[226:233], v[44:47]
	v_mfma_f32_16x16x128_f8f6f4 v[40:43], v[210:217], v[226:233], v[40:43]
	v_mfma_f32_16x16x128_f8f6f4 v[28:31], v[202:209], v[234:241], v[28:31]
	v_mfma_f32_16x16x128_f8f6f4 v[24:27], v[210:217], v[234:241], v[24:27]
	v_mfma_f32_16x16x128_f8f6f4 v[12:15], v[202:209], v[242:249], v[12:15]
	v_mfma_f32_16x16x128_f8f6f4 v[8:11], v[210:217], v[242:249], v[8:11]
	s_setprio 0
	s_barrier
	s_mov_b32 m0, s67
	v_lshl_add_u64 v[186:187], v[186:187], 0, s[34:35]
	ds_read_b128 v[202:205], v197 offset:49152
	ds_read_b128 v[210:213], v197 offset:51200
	ds_read_b128 v[206:209], v198 offset:49152
	ds_read_b128 v[214:217], v198 offset:51200
	global_load_lds_dwordx4 v[186:187], off
	v_lshl_add_u64 v[186:187], v[188:189], 0, s[34:35]
	s_mov_b32 m0, s68
	s_nop 0
	global_load_lds_dwordx4 v[186:187], off
	s_waitcnt vmcnt(8)
	s_waitcnt lgkmcnt(0)
	s_barrier
	s_setprio 1
	s_waitcnt lgkmcnt(0)
	v_mfma_f32_16x16x128_f8f6f4 v[52:55], v[202:209], v[218:225], v[52:55]
	v_mfma_f32_16x16x128_f8f6f4 v[48:51], v[210:217], v[218:225], v[48:51]
	v_mfma_f32_16x16x128_f8f6f4 v[36:39], v[202:209], v[226:233], v[36:39]
	v_mfma_f32_16x16x128_f8f6f4 v[32:35], v[210:217], v[226:233], v[32:35]
	v_mfma_f32_16x16x128_f8f6f4 v[20:23], v[202:209], v[234:241], v[20:23]
	v_mfma_f32_16x16x128_f8f6f4 v[16:19], v[210:217], v[234:241], v[16:19]
	v_mfma_f32_16x16x128_f8f6f4 v[4:7], v[202:209], v[242:249], v[4:7]
	v_mfma_f32_16x16x128_f8f6f4 v[0:3], v[210:217], v[242:249], v[0:3]
	s_setprio 0
	s_barrier
	s_add_u32 s16, s50, 0x4080
	s_addc_u32 s17, s51, 0
	s_mov_b32 m0, s71
	v_lshl_add_u64 v[186:187], s[16:17], 0, v[138:139]
	global_load_lds_dwordx4 v[186:187], off
	v_lshl_add_u64 v[186:187], s[16:17], 0, v[140:141]
	s_mov_b32 m0, s72
	s_add_i32 s76, s76, 2
	global_load_lds_dwordx4 v[186:187], off
	s_add_u32 s48, s48, 0x100
	s_addc_u32 s49, s49, 0
	s_cmp_gt_u32 s76, 13
	s_cbranch_scc1 .LBB0_972

.LBB0_1060:
	v_mov_b32_e32 v137, v133
	v_mov_b32_e32 v139, v133
	s_mov_b64 s[44:45], 0
	s_mov_b64 s[40:41], -1
	s_mov_b64 s[42:43], 0
	s_add_u32 s52, s12, s44
	s_addc_u32 s53, s13, s45
	s_add_u32 s29, s52, 0x100
	s_addc_u32 s48, s53, 0
	s_and_b64 s[46:47], s[42:43], exec
	s_cselect_b32 s46, s12, s29
	s_cselect_b32 s47, s13, s48
	s_add_u32 s29, s38, s44
	s_addc_u32 s44, s39, s45
	s_add_u32 s29, s29, 0x100
	s_addc_u32 s48, s44, 0
	ds_read_b128 v[162:165], v147
	ds_read_b128 v[170:173], v147 offset:2048
	ds_read_b128 v[166:169], v148
	ds_read_b128 v[174:177], v148 offset:2048
	s_and_b64 s[44:45], s[42:43], exec
	s_cselect_b32 s51, s35, s48
	s_cselect_b32 s50, s34, s29
	ds_read_b128 v[178:181], v145
	ds_read_b128 v[186:189], v145 offset:2048
	ds_read_b128 v[182:185], v146
	ds_read_b128 v[190:193], v146 offset:2048
	ds_read_b128 v[196:199], v145 offset:4096
	ds_read_b128 v[204:207], v145 offset:6144
	ds_read_b128 v[200:203], v146 offset:4096
	ds_read_b128 v[208:211], v146 offset:6144
	s_waitcnt vmcnt(6)
	s_waitcnt lgkmcnt(8)
	s_barrier
	s_waitcnt lgkmcnt(0)
	v_cndmask_b32_e64 v140, v134, v158, s[42:43]
	s_setprio 1
	s_waitcnt lgkmcnt(0)
	v_mfma_f32_16x16x128_f8f6f4 v[124:127], v[162:169], v[178:185], 0
	v_mfma_f32_16x16x128_f8f6f4 v[120:123], v[170:177], v[178:185], 0
	v_mfma_f32_16x16x128_f8f6f4 v[108:111], v[162:169], v[186:193], 0
	v_mfma_f32_16x16x128_f8f6f4 v[104:107], v[170:177], v[186:193], 0
	v_mfma_f32_16x16x128_f8f6f4 v[92:95], v[162:169], v[196:203], 0
	v_mfma_f32_16x16x128_f8f6f4 v[88:91], v[170:177], v[196:203], 0
	v_mfma_f32_16x16x128_f8f6f4 v[76:79], v[162:169], v[204:211], 0
	v_mfma_f32_16x16x128_f8f6f4 v[72:75], v[170:177], v[204:211], 0
	s_setprio 0
	s_barrier
	ds_read_b128 v[218:221], v147 offset:16384
	ds_read_b128 v[226:229], v147 offset:18432
	ds_read_b128 v[222:225], v148 offset:16384
	ds_read_b128 v[230:233], v148 offset:18432
	s_add_i32 m0, s0, 0xc000
	s_add_i32 s29, s0, 0xe000
	s_add_u32 s48, s50, 0x1000
	s_addc_u32 s49, s51, 0
	s_add_u32 s44, s50, 0x1080
	s_addc_u32 s45, s51, 0
	v_cndmask_b32_e64 v132, v135, v157, s[42:43]
	v_cndmask_b32_e64 v161, v136, v159, s[42:43]
	v_lshl_add_u64 v[252:253], s[52:53], 0, v[136:137]
	v_lshl_add_u64 v[252:253], v[252:253], 0, s[20:21]
	global_load_lds_dwordx4 v[252:253], off
	v_lshl_add_u64 v[252:253], s[52:53], 0, v[138:139]
	v_lshl_add_u64 v[252:253], v[252:253], 0, s[20:21]
	s_mov_b32 m0, s29
	s_nop 0
	global_load_lds_dwordx4 v[252:253], off
	s_barrier
	s_waitcnt lgkmcnt(0)
	s_setprio 1
	s_waitcnt lgkmcnt(0)
	v_mfma_f32_16x16x128_f8f6f4 v[116:119], v[218:225], v[178:185], 0
	v_mfma_f32_16x16x128_f8f6f4 v[112:115], v[226:233], v[178:185], 0
	v_mfma_f32_16x16x128_f8f6f4 v[100:103], v[218:225], v[186:193], 0
	v_mfma_f32_16x16x128_f8f6f4 v[96:99], v[226:233], v[186:193], 0
	v_mfma_f32_16x16x128_f8f6f4 v[84:87], v[218:225], v[196:203], 0
	v_mfma_f32_16x16x128_f8f6f4 v[80:83], v[226:233], v[196:203], 0
	v_mfma_f32_16x16x128_f8f6f4 v[68:71], v[218:225], v[204:211], 0
	v_mfma_f32_16x16x128_f8f6f4 v[64:67], v[226:233], v[204:211], 0
	s_setprio 0
	s_barrier
	s_mov_b32 m0, s0
	ds_read_b128 v[178:181], v145 offset:16384
	ds_read_b128 v[186:189], v145 offset:18432
	ds_read_b128 v[182:185], v146 offset:16384
	ds_read_b128 v[190:193], v146 offset:18432
	ds_read_b128 v[196:199], v145 offset:20480
	ds_read_b128 v[204:207], v145 offset:22528
	ds_read_b128 v[200:203], v146 offset:20480
	ds_read_b128 v[208:211], v146 offset:22528
	global_load_lds_dwordx4 v132, s[46:47]
	s_mov_b32 m0, s56
	v_mov_b32_e32 v141, v133
	global_load_lds_dwordx4 v140, s[46:47]
	s_waitcnt lgkmcnt(8)
	s_barrier
	s_waitcnt lgkmcnt(0)
	v_lshl_add_u64 v[212:213], s[46:47], 0, v[132:133]
	v_lshl_add_u64 v[214:215], s[46:47], 0, v[140:141]
	s_setprio 1
	s_waitcnt lgkmcnt(0)
	v_mfma_f32_16x16x128_f8f6f4 v[60:63], v[162:169], v[178:185], 0
	v_mfma_f32_16x16x128_f8f6f4 v[56:59], v[170:177], v[178:185], 0
	v_mfma_f32_16x16x128_f8f6f4 v[44:47], v[162:169], v[186:193], 0
	v_mfma_f32_16x16x128_f8f6f4 v[40:43], v[170:177], v[186:193], 0
	v_mfma_f32_16x16x128_f8f6f4 v[28:31], v[162:169], v[196:203], 0
	v_mfma_f32_16x16x128_f8f6f4 v[24:27], v[170:177], v[196:203], 0
	v_mfma_f32_16x16x128_f8f6f4 v[12:15], v[162:169], v[204:211], 0
	v_mfma_f32_16x16x128_f8f6f4 v[8:11], v[170:177], v[204:211], 0
	s_setprio 0
	s_barrier
	s_mov_b32 m0, s1
	v_lshl_add_u64 v[140:141], s[50:51], 0, v[128:129]
	global_load_lds_dwordx4 v[140:141], off
	v_lshl_add_u64 v[142:143], s[50:51], 0, v[130:131]
	s_mov_b32 m0, s37
	s_nop 0
	global_load_lds_dwordx4 v[142:143], off
	s_waitcnt vmcnt(8)
	s_waitcnt lgkmcnt(0)
	s_barrier
	s_setprio 1
	s_waitcnt lgkmcnt(0)
	v_mfma_f32_16x16x128_f8f6f4 v[52:55], v[218:225], v[178:185], 0
	v_mfma_f32_16x16x128_f8f6f4 v[48:51], v[226:233], v[178:185], 0
	v_mfma_f32_16x16x128_f8f6f4 v[36:39], v[218:225], v[186:193], 0
	v_mfma_f32_16x16x128_f8f6f4 v[32:35], v[226:233], v[186:193], 0
	v_mfma_f32_16x16x128_f8f6f4 v[20:23], v[218:225], v[196:203], 0
	v_mfma_f32_16x16x128_f8f6f4 v[16:19], v[226:233], v[196:203], 0
	v_mfma_f32_16x16x128_f8f6f4 v[4:7], v[218:225], v[204:211], 0
	v_mfma_f32_16x16x128_f8f6f4 v[0:3], v[226:233], v[204:211], 0
	s_setprio 0
	s_barrier
	ds_read_b128 v[162:165], v147 offset:32768
	ds_read_b128 v[170:173], v147 offset:34816
	ds_read_b128 v[166:169], v148 offset:32768
	ds_read_b128 v[174:177], v148 offset:34816
	s_mov_b32 m0, s63
	ds_read_b128 v[178:181], v145 offset:32768
	ds_read_b128 v[186:189], v145 offset:34816
	ds_read_b128 v[182:185], v146 offset:32768
	ds_read_b128 v[190:193], v146 offset:34816
	ds_read_b128 v[196:199], v145 offset:36864
	ds_read_b128 v[204:207], v145 offset:38912
	ds_read_b128 v[200:203], v146 offset:36864
	ds_read_b128 v[208:211], v146 offset:38912
	v_cndmask_b32_e64 v132, v138, v160, s[42:43]
	global_load_lds_dwordx4 v161, s[46:47]
	s_mov_b32 m0, s64
	s_nop 0
	global_load_lds_dwordx4 v132, s[46:47]
	s_waitcnt vmcnt(8)
	s_waitcnt lgkmcnt(8)
	s_barrier
	s_waitcnt lgkmcnt(0)
	s_setprio 1
	s_waitcnt lgkmcnt(0)
	v_mfma_f32_16x16x128_f8f6f4 v[124:127], v[162:169], v[178:185], v[124:127]
	v_mfma_f32_16x16x128_f8f6f4 v[120:123], v[170:177], v[178:185], v[120:123]
	v_mfma_f32_16x16x128_f8f6f4 v[108:111], v[162:169], v[186:193], v[108:111]
	v_mfma_f32_16x16x128_f8f6f4 v[104:107], v[170:177], v[186:193], v[104:107]
	v_mfma_f32_16x16x128_f8f6f4 v[92:95], v[162:169], v[196:203], v[92:95]
	v_mfma_f32_16x16x128_f8f6f4 v[88:91], v[170:177], v[196:203], v[88:91]
	v_mfma_f32_16x16x128_f8f6f4 v[76:79], v[162:169], v[204:211], v[76:79]
	v_mfma_f32_16x16x128_f8f6f4 v[72:75], v[170:177], v[204:211], v[72:75]
	s_setprio 0
	s_barrier
	ds_read_b128 v[218:221], v147 offset:49152
	ds_read_b128 v[226:229], v147 offset:51200
	ds_read_b128 v[222:225], v148 offset:49152
	ds_read_b128 v[230:233], v148 offset:51200
	v_lshl_add_u64 v[216:217], s[48:49], 0, v[128:129]
	s_mov_b32 m0, s57
	s_nop 0
	global_load_lds_dwordx4 v[216:217], off
	v_lshl_add_u64 v[216:217], s[48:49], 0, v[130:131]
	s_mov_b32 m0, s62
	s_nop 0
	global_load_lds_dwordx4 v[216:217], off
	s_waitcnt vmcnt(8)
	s_barrier
	s_waitcnt lgkmcnt(0)
	s_setprio 1
	s_waitcnt lgkmcnt(0)
	v_mfma_f32_16x16x128_f8f6f4 v[116:119], v[218:225], v[178:185], v[116:119]
	v_mfma_f32_16x16x128_f8f6f4 v[112:115], v[226:233], v[178:185], v[112:115]
	v_mfma_f32_16x16x128_f8f6f4 v[100:103], v[218:225], v[186:193], v[100:103]
	v_mfma_f32_16x16x128_f8f6f4 v[96:99], v[226:233], v[186:193], v[96:99]
	v_mfma_f32_16x16x128_f8f6f4 v[84:87], v[218:225], v[196:203], v[84:87]
	v_mfma_f32_16x16x128_f8f6f4 v[80:83], v[226:233], v[196:203], v[80:83]
	v_mfma_f32_16x16x128_f8f6f4 v[68:71], v[218:225], v[204:211], v[68:71]
	v_mfma_f32_16x16x128_f8f6f4 v[64:67], v[226:233], v[204:211], v[64:67]
	s_setprio 0
	s_barrier
	s_mov_b32 m0, s67
	v_lshl_add_u64 v[212:213], v[212:213], 0, s[20:21]
	ds_read_b128 v[178:181], v145 offset:49152
	ds_read_b128 v[186:189], v145 offset:51200
	ds_read_b128 v[182:185], v146 offset:49152
	ds_read_b128 v[190:193], v146 offset:51200
	ds_read_b128 v[196:199], v145 offset:53248
	ds_read_b128 v[204:207], v145 offset:55296
	ds_read_b128 v[200:203], v146 offset:53248
	ds_read_b128 v[208:211], v146 offset:55296
	global_load_lds_dwordx4 v[212:213], off
	v_lshl_add_u64 v[212:213], v[214:215], 0, s[20:21]
	s_mov_b32 m0, s68
	s_nop 0
	global_load_lds_dwordx4 v[212:213], off
	s_waitcnt lgkmcnt(8)
	s_barrier
	s_waitcnt lgkmcnt(0)
	s_setprio 1
	s_waitcnt lgkmcnt(0)
	v_mfma_f32_16x16x128_f8f6f4 v[60:63], v[162:169], v[178:185], v[60:63]
	v_mfma_f32_16x16x128_f8f6f4 v[56:59], v[170:177], v[178:185], v[56:59]
	v_mfma_f32_16x16x128_f8f6f4 v[44:47], v[162:169], v[186:193], v[44:47]
	v_mfma_f32_16x16x128_f8f6f4 v[40:43], v[170:177], v[186:193], v[40:43]
	v_mfma_f32_16x16x128_f8f6f4 v[28:31], v[162:169], v[196:203], v[28:31]
	v_mfma_f32_16x16x128_f8f6f4 v[24:27], v[170:177], v[196:203], v[24:27]
	v_mfma_f32_16x16x128_f8f6f4 v[12:15], v[162:169], v[204:211], v[12:15]
	v_mfma_f32_16x16x128_f8f6f4 v[8:11], v[170:177], v[204:211], v[8:11]
	s_setprio 0
	s_barrier
	s_mov_b32 m0, s65
	v_lshl_add_u64 v[140:141], v[140:141], 0, s[20:21]
	global_load_lds_dwordx4 v[140:141], off
	v_lshl_add_u64 v[140:141], v[142:143], 0, s[20:21]
	s_mov_b32 m0, s66
	s_nop 0
	global_load_lds_dwordx4 v[140:141], off
	s_waitcnt vmcnt(8)
	s_waitcnt lgkmcnt(0)
	s_barrier
	s_setprio 1
	s_waitcnt lgkmcnt(0)
	v_mfma_f32_16x16x128_f8f6f4 v[52:55], v[218:225], v[178:185], v[52:55]
	v_mfma_f32_16x16x128_f8f6f4 v[48:51], v[226:233], v[178:185], v[48:51]
	v_mfma_f32_16x16x128_f8f6f4 v[36:39], v[218:225], v[186:193], v[36:39]
	v_mfma_f32_16x16x128_f8f6f4 v[32:35], v[226:233], v[186:193], v[32:35]
	v_mfma_f32_16x16x128_f8f6f4 v[20:23], v[218:225], v[196:203], v[20:23]
	v_mfma_f32_16x16x128_f8f6f4 v[16:19], v[226:233], v[196:203], v[16:19]
	v_mfma_f32_16x16x128_f8f6f4 v[4:7], v[218:225], v[204:211], v[4:7]
	v_mfma_f32_16x16x128_f8f6f4 v[0:3], v[226:233], v[204:211], v[0:3]
	s_setprio 0
	s_barrier
	s_mov_b32 m0, s69
	v_lshl_add_u64 v[140:141], s[44:45], 0, v[128:129]
	global_load_lds_dwordx4 v[140:141], off
	v_lshl_add_u64 v[140:141], s[44:45], 0, v[130:131]
	s_mov_b32 m0, s70
	s_andn2_b64 vcc, exec, s[40:41]
	global_load_lds_dwordx4 v[140:141], off
	s_mov_b64 s[42:43], -1
	s_mov_b64 s[40:41], 0
	s_mov_b64 s[44:45], 0x100
	s_cbranch_vccz .LBB0_1061
	s_branch .Lpeel_after_1061
.LBB0_1061:
	s_add_u32 s52, s12, s44
	s_addc_u32 s53, s13, s45
	s_add_u32 s29, s52, 0x100
	s_addc_u32 s48, s53, 0
	s_and_b64 s[46:47], s[42:43], exec
	s_cselect_b32 s46, s12, s29
	s_cselect_b32 s47, s13, s48
	s_add_u32 s29, s38, s44
	s_addc_u32 s44, s39, s45
	s_add_u32 s29, s29, 0x100
	s_addc_u32 s48, s44, 0
	ds_read_b128 v[162:165], v147
	ds_read_b128 v[170:173], v147 offset:2048
	ds_read_b128 v[166:169], v148
	ds_read_b128 v[174:177], v148 offset:2048
	s_and_b64 s[44:45], s[42:43], exec
	s_cselect_b32 s51, s35, s48
	s_cselect_b32 s50, s34, s29
	ds_read_b128 v[178:181], v145
	ds_read_b128 v[186:189], v145 offset:2048
	ds_read_b128 v[182:185], v146
	ds_read_b128 v[190:193], v146 offset:2048
	ds_read_b128 v[196:199], v145 offset:4096
	ds_read_b128 v[204:207], v145 offset:6144
	ds_read_b128 v[200:203], v146 offset:4096
	ds_read_b128 v[208:211], v146 offset:6144
	s_waitcnt vmcnt(6)
	s_waitcnt lgkmcnt(8)
	s_barrier
	s_waitcnt lgkmcnt(0)
	v_cndmask_b32_e64 v140, v134, v158, s[42:43]
	s_setprio 1
	s_waitcnt lgkmcnt(0)
	v_mfma_f32_16x16x128_f8f6f4 v[124:127], v[162:169], v[178:185], v[124:127]
	v_mfma_f32_16x16x128_f8f6f4 v[120:123], v[170:177], v[178:185], v[120:123]
	v_mfma_f32_16x16x128_f8f6f4 v[108:111], v[162:169], v[186:193], v[108:111]
	v_mfma_f32_16x16x128_f8f6f4 v[104:107], v[170:177], v[186:193], v[104:107]
	v_mfma_f32_16x16x128_f8f6f4 v[92:95], v[162:169], v[196:203], v[92:95]
	v_mfma_f32_16x16x128_f8f6f4 v[88:91], v[170:177], v[196:203], v[88:91]
	v_mfma_f32_16x16x128_f8f6f4 v[76:79], v[162:169], v[204:211], v[76:79]
	v_mfma_f32_16x16x128_f8f6f4 v[72:75], v[170:177], v[204:211], v[72:75]
	s_setprio 0
	s_barrier
	ds_read_b128 v[218:221], v147 offset:16384
	ds_read_b128 v[226:229], v147 offset:18432
	ds_read_b128 v[222:225], v148 offset:16384
	ds_read_b128 v[230:233], v148 offset:18432
	s_add_i32 m0, s0, 0xc000
	s_add_i32 s29, s0, 0xe000
	s_add_u32 s48, s50, 0x1000
	s_addc_u32 s49, s51, 0
	s_add_u32 s44, s50, 0x1080
	s_addc_u32 s45, s51, 0
	v_cndmask_b32_e64 v132, v135, v157, s[42:43]
	v_cndmask_b32_e64 v161, v136, v159, s[42:43]
	v_lshl_add_u64 v[252:253], s[52:53], 0, v[136:137]
	v_lshl_add_u64 v[252:253], v[252:253], 0, s[20:21]
	global_load_lds_dwordx4 v[252:253], off
	v_lshl_add_u64 v[252:253], s[52:53], 0, v[138:139]
	v_lshl_add_u64 v[252:253], v[252:253], 0, s[20:21]
	s_mov_b32 m0, s29
	s_nop 0
	global_load_lds_dwordx4 v[252:253], off
	s_barrier
	s_waitcnt lgkmcnt(0)
	s_setprio 1
	s_waitcnt lgkmcnt(0)
	v_mfma_f32_16x16x128_f8f6f4 v[116:119], v[218:225], v[178:185], v[116:119]
	v_mfma_f32_16x16x128_f8f6f4 v[112:115], v[226:233], v[178:185], v[112:115]
	v_mfma_f32_16x16x128_f8f6f4 v[100:103], v[218:225], v[186:193], v[100:103]
	v_mfma_f32_16x16x128_f8f6f4 v[96:99], v[226:233], v[186:193], v[96:99]
	v_mfma_f32_16x16x128_f8f6f4 v[84:87], v[218:225], v[196:203], v[84:87]
	v_mfma_f32_16x16x128_f8f6f4 v[80:83], v[226:233], v[196:203], v[80:83]
	v_mfma_f32_16x16x128_f8f6f4 v[68:71], v[218:225], v[204:211], v[68:71]
	v_mfma_f32_16x16x128_f8f6f4 v[64:67], v[226:233], v[204:211], v[64:67]
	s_setprio 0
	s_barrier
	s_mov_b32 m0, s0
	ds_read_b128 v[178:181], v145 offset:16384
	ds_read_b128 v[186:189], v145 offset:18432
	ds_read_b128 v[182:185], v146 offset:16384
	ds_read_b128 v[190:193], v146 offset:18432
	ds_read_b128 v[196:199], v145 offset:20480
	ds_read_b128 v[204:207], v145 offset:22528
	ds_read_b128 v[200:203], v146 offset:20480
	ds_read_b128 v[208:211], v146 offset:22528
	global_load_lds_dwordx4 v132, s[46:47]
	s_mov_b32 m0, s56
	v_mov_b32_e32 v141, v133
	global_load_lds_dwordx4 v140, s[46:47]
	s_waitcnt lgkmcnt(8)
	s_barrier
	s_waitcnt lgkmcnt(0)
	v_lshl_add_u64 v[212:213], s[46:47], 0, v[132:133]
	v_lshl_add_u64 v[214:215], s[46:47], 0, v[140:141]
	s_setprio 1
	s_waitcnt lgkmcnt(0)
	v_mfma_f32_16x16x128_f8f6f4 v[60:63], v[162:169], v[178:185], v[60:63]
	v_mfma_f32_16x16x128_f8f6f4 v[56:59], v[170:177], v[178:185], v[56:59]
	v_mfma_f32_16x16x128_f8f6f4 v[44:47], v[162:169], v[186:193], v[44:47]
	v_mfma_f32_16x16x128_f8f6f4 v[40:43], v[170:177], v[186:193], v[40:43]
	v_mfma_f32_16x16x128_f8f6f4 v[28:31], v[162:169], v[196:203], v[28:31]
	v_mfma_f32_16x16x128_f8f6f4 v[24:27], v[170:177], v[196:203], v[24:27]
	v_mfma_f32_16x16x128_f8f6f4 v[12:15], v[162:169], v[204:211], v[12:15]
	v_mfma_f32_16x16x128_f8f6f4 v[8:11], v[170:177], v[204:211], v[8:11]
	s_setprio 0
	s_barrier
	s_mov_b32 m0, s1
	v_lshl_add_u64 v[140:141], s[50:51], 0, v[128:129]
	global_load_lds_dwordx4 v[140:141], off
	v_lshl_add_u64 v[142:143], s[50:51], 0, v[130:131]
	s_mov_b32 m0, s37
	s_nop 0
	global_load_lds_dwordx4 v[142:143], off
	s_waitcnt vmcnt(8)
	s_waitcnt lgkmcnt(0)
	s_barrier
	s_setprio 1
	s_waitcnt lgkmcnt(0)
	v_mfma_f32_16x16x128_f8f6f4 v[52:55], v[218:225], v[178:185], v[52:55]
	v_mfma_f32_16x16x128_f8f6f4 v[48:51], v[226:233], v[178:185], v[48:51]
	v_mfma_f32_16x16x128_f8f6f4 v[36:39], v[218:225], v[186:193], v[36:39]
	v_mfma_f32_16x16x128_f8f6f4 v[32:35], v[226:233], v[186:193], v[32:35]
	v_mfma_f32_16x16x128_f8f6f4 v[20:23], v[218:225], v[196:203], v[20:23]
	v_mfma_f32_16x16x128_f8f6f4 v[16:19], v[226:233], v[196:203], v[16:19]
	v_mfma_f32_16x16x128_f8f6f4 v[4:7], v[218:225], v[204:211], v[4:7]
	v_mfma_f32_16x16x128_f8f6f4 v[0:3], v[226:233], v[204:211], v[0:3]
	s_setprio 0
	s_barrier
	ds_read_b128 v[162:165], v147 offset:32768
	ds_read_b128 v[170:173], v147 offset:34816
	ds_read_b128 v[166:169], v148 offset:32768
	ds_read_b128 v[174:177], v148 offset:34816
	s_mov_b32 m0, s63
	ds_read_b128 v[178:181], v145 offset:32768
	ds_read_b128 v[186:189], v145 offset:34816
	ds_read_b128 v[182:185], v146 offset:32768
	ds_read_b128 v[190:193], v146 offset:34816
	ds_read_b128 v[196:199], v145 offset:36864
	ds_read_b128 v[204:207], v145 offset:38912
	ds_read_b128 v[200:203], v146 offset:36864
	ds_read_b128 v[208:211], v146 offset:38912
	v_cndmask_b32_e64 v132, v138, v160, s[42:43]
	global_load_lds_dwordx4 v161, s[46:47]
	s_mov_b32 m0, s64
	s_nop 0
	global_load_lds_dwordx4 v132, s[46:47]
	s_waitcnt vmcnt(8)
	s_waitcnt lgkmcnt(8)
	s_barrier
	s_waitcnt lgkmcnt(0)
	s_setprio 1
	s_waitcnt lgkmcnt(0)
	v_mfma_f32_16x16x128_f8f6f4 v[124:127], v[162:169], v[178:185], v[124:127]
	v_mfma_f32_16x16x128_f8f6f4 v[120:123], v[170:177], v[178:185], v[120:123]
	v_mfma_f32_16x16x128_f8f6f4 v[108:111], v[162:169], v[186:193], v[108:111]
	v_mfma_f32_16x16x128_f8f6f4 v[104:107], v[170:177], v[186:193], v[104:107]
	v_mfma_f32_16x16x128_f8f6f4 v[92:95], v[162:169], v[196:203], v[92:95]
	v_mfma_f32_16x16x128_f8f6f4 v[88:91], v[170:177], v[196:203], v[88:91]
	v_mfma_f32_16x16x128_f8f6f4 v[76:79], v[162:169], v[204:211], v[76:79]
	v_mfma_f32_16x16x128_f8f6f4 v[72:75], v[170:177], v[204:211], v[72:75]
	s_setprio 0
	s_barrier
	ds_read_b128 v[218:221], v147 offset:49152
	ds_read_b128 v[226:229], v147 offset:51200
	ds_read_b128 v[222:225], v148 offset:49152
	ds_read_b128 v[230:233], v148 offset:51200
	v_lshl_add_u64 v[216:217], s[48:49], 0, v[128:129]
	s_mov_b32 m0, s57
	s_nop 0
	global_load_lds_dwordx4 v[216:217], off
	v_lshl_add_u64 v[216:217], s[48:49], 0, v[130:131]
	s_mov_b32 m0, s62
	s_nop 0
	global_load_lds_dwordx4 v[216:217], off
	s_waitcnt vmcnt(8)
	s_barrier
	s_waitcnt lgkmcnt(0)
	s_setprio 1
	s_waitcnt lgkmcnt(0)
	v_mfma_f32_16x16x128_f8f6f4 v[116:119], v[218:225], v[178:185], v[116:119]
	v_mfma_f32_16x16x128_f8f6f4 v[112:115], v[226:233], v[178:185], v[112:115]
	v_mfma_f32_16x16x128_f8f6f4 v[100:103], v[218:225], v[186:193], v[100:103]
	v_mfma_f32_16x16x128_f8f6f4 v[96:99], v[226:233], v[186:193], v[96:99]
	v_mfma_f32_16x16x128_f8f6f4 v[84:87], v[218:225], v[196:203], v[84:87]
	v_mfma_f32_16x16x128_f8f6f4 v[80:83], v[226:233], v[196:203], v[80:83]
	v_mfma_f32_16x16x128_f8f6f4 v[68:71], v[218:225], v[204:211], v[68:71]
	v_mfma_f32_16x16x128_f8f6f4 v[64:67], v[226:233], v[204:211], v[64:67]
	s_setprio 0
	s_barrier
	s_mov_b32 m0, s67
	v_lshl_add_u64 v[212:213], v[212:213], 0, s[20:21]
	ds_read_b128 v[178:181], v145 offset:49152
	ds_read_b128 v[186:189], v145 offset:51200
	ds_read_b128 v[182:185], v146 offset:49152
	ds_read_b128 v[190:193], v146 offset:51200
	ds_read_b128 v[196:199], v145 offset:53248
	ds_read_b128 v[204:207], v145 offset:55296
	ds_read_b128 v[200:203], v146 offset:53248
	ds_read_b128 v[208:211], v146 offset:55296
	global_load_lds_dwordx4 v[212:213], off
	v_lshl_add_u64 v[212:213], v[214:215], 0, s[20:21]
	s_mov_b32 m0, s68
	s_nop 0
	global_load_lds_dwordx4 v[212:213], off
	s_waitcnt lgkmcnt(8)
	s_barrier
	s_waitcnt lgkmcnt(0)
	s_setprio 1
	s_waitcnt lgkmcnt(0)
	v_mfma_f32_16x16x128_f8f6f4 v[60:63], v[162:169], v[178:185], v[60:63]
	v_mfma_f32_16x16x128_f8f6f4 v[56:59], v[170:177], v[178:185], v[56:59]
	v_mfma_f32_16x16x128_f8f6f4 v[44:47], v[162:169], v[186:193], v[44:47]
	v_mfma_f32_16x16x128_f8f6f4 v[40:43], v[170:177], v[186:193], v[40:43]
	v_mfma_f32_16x16x128_f8f6f4 v[28:31], v[162:169], v[196:203], v[28:31]
	v_mfma_f32_16x16x128_f8f6f4 v[24:27], v[170:177], v[196:203], v[24:27]
	v_mfma_f32_16x16x128_f8f6f4 v[12:15], v[162:169], v[204:211], v[12:15]
	v_mfma_f32_16x16x128_f8f6f4 v[8:11], v[170:177], v[204:211], v[8:11]
	s_setprio 0
	s_barrier
	s_mov_b32 m0, s65
	v_lshl_add_u64 v[140:141], v[140:141], 0, s[20:21]
	global_load_lds_dwordx4 v[140:141], off
	v_lshl_add_u64 v[140:141], v[142:143], 0, s[20:21]
	s_mov_b32 m0, s66
	s_nop 0
	global_load_lds_dwordx4 v[140:141], off
	s_waitcnt vmcnt(8)
	s_waitcnt lgkmcnt(0)
	s_barrier
	s_setprio 1
	s_waitcnt lgkmcnt(0)
	v_mfma_f32_16x16x128_f8f6f4 v[52:55], v[218:225], v[178:185], v[52:55]
	v_mfma_f32_16x16x128_f8f6f4 v[48:51], v[226:233], v[178:185], v[48:51]
	v_mfma_f32_16x16x128_f8f6f4 v[36:39], v[218:225], v[186:193], v[36:39]
	v_mfma_f32_16x16x128_f8f6f4 v[32:35], v[226:233], v[186:193], v[32:35]
	v_mfma_f32_16x16x128_f8f6f4 v[20:23], v[218:225], v[196:203], v[20:23]
	v_mfma_f32_16x16x128_f8f6f4 v[16:19], v[226:233], v[196:203], v[16:19]
	v_mfma_f32_16x16x128_f8f6f4 v[4:7], v[218:225], v[204:211], v[4:7]
	v_mfma_f32_16x16x128_f8f6f4 v[0:3], v[226:233], v[204:211], v[0:3]
	s_setprio 0
	s_barrier
	s_mov_b32 m0, s69
	v_lshl_add_u64 v[140:141], s[44:45], 0, v[128:129]
	global_load_lds_dwordx4 v[140:141], off
	v_lshl_add_u64 v[140:141], s[44:45], 0, v[130:131]
	s_mov_b32 m0, s70
	s_andn2_b64 vcc, exec, s[40:41]
	global_load_lds_dwordx4 v[140:141], off
	s_mov_b64 s[42:43], -1
	s_mov_b64 s[40:41], 0
	s_mov_b64 s[44:45], 0x100
	s_cbranch_vccz .LBB0_1061

.LBB0_1080:
	v_mov_b32_e32 v137, v133
	v_mov_b32_e32 v139, v133
	s_mov_b64 s[34:35], 0
	s_mov_b64 s[28:29], -1
	s_mov_b64 s[30:31], 0
	s_add_u32 s42, s10, s34
	s_addc_u32 s43, s11, s35
	s_add_u32 s38, s42, 0x100
	s_addc_u32 s39, s43, 0
	s_and_b64 s[36:37], s[30:31], exec
	s_cselect_b32 s36, s10, s38
	s_cselect_b32 s37, s11, s39
	s_add_u32 s34, s26, s34
	s_addc_u32 s35, s27, s35
	s_add_u32 s38, s34, 0x100
	s_addc_u32 s39, s35, 0
	ds_read_b128 v[160:163], v147
	ds_read_b128 v[168:171], v147 offset:2048
	ds_read_b128 v[164:167], v148
	ds_read_b128 v[172:175], v148 offset:2048
	s_and_b64 s[34:35], s[30:31], exec
	s_cselect_b32 s41, s25, s39
	s_cselect_b32 s40, s24, s38
	ds_read_b128 v[176:179], v145
	ds_read_b128 v[184:187], v145 offset:2048
	ds_read_b128 v[180:183], v146
	ds_read_b128 v[188:191], v146 offset:2048
	ds_read_b128 v[196:199], v145 offset:4096
	ds_read_b128 v[204:207], v145 offset:6144
	ds_read_b128 v[200:203], v146 offset:4096
	ds_read_b128 v[208:211], v146 offset:6144
	s_waitcnt vmcnt(6)
	s_waitcnt lgkmcnt(8)
	s_barrier
	s_waitcnt lgkmcnt(0)
	v_cndmask_b32_e64 v140, v134, v156, s[30:31]
	s_setprio 1
	s_waitcnt lgkmcnt(0)
	v_mfma_f32_16x16x128_f8f6f4 v[124:127], v[160:167], v[176:183], 0
	v_mfma_f32_16x16x128_f8f6f4 v[120:123], v[168:175], v[176:183], 0
	v_mfma_f32_16x16x128_f8f6f4 v[108:111], v[160:167], v[184:191], 0
	v_mfma_f32_16x16x128_f8f6f4 v[104:107], v[168:175], v[184:191], 0
	v_mfma_f32_16x16x128_f8f6f4 v[92:95], v[160:167], v[196:203], 0
	v_mfma_f32_16x16x128_f8f6f4 v[88:91], v[168:175], v[196:203], 0
	v_mfma_f32_16x16x128_f8f6f4 v[76:79], v[160:167], v[204:211], 0
	v_mfma_f32_16x16x128_f8f6f4 v[72:75], v[168:175], v[204:211], 0
	s_setprio 0
	s_barrier
	ds_read_b128 v[218:221], v147 offset:16384
	ds_read_b128 v[226:229], v147 offset:18432
	ds_read_b128 v[222:225], v148 offset:16384
	ds_read_b128 v[230:233], v148 offset:18432
	s_add_i32 m0, s1, 0xc000
	s_add_i32 s64, s1, 0xe000
	s_add_u32 s38, s40, 0x1000
	s_addc_u32 s39, s41, 0
	s_add_u32 s34, s40, 0x1080
	s_addc_u32 s35, s41, 0
	v_cndmask_b32_e64 v132, v135, v155, s[30:31]
	v_cndmask_b32_e64 v159, v136, v157, s[30:31]
	v_lshl_add_u64 v[252:253], s[42:43], 0, v[136:137]
	v_lshl_add_u64 v[252:253], v[252:253], 0, s[16:17]
	global_load_lds_dwordx4 v[252:253], off
	v_lshl_add_u64 v[252:253], s[42:43], 0, v[138:139]
	v_lshl_add_u64 v[252:253], v[252:253], 0, s[16:17]
	s_mov_b32 m0, s64
	s_nop 0
	global_load_lds_dwordx4 v[252:253], off
	s_barrier
	s_waitcnt lgkmcnt(0)
	s_setprio 1
	s_waitcnt lgkmcnt(0)
	v_mfma_f32_16x16x128_f8f6f4 v[116:119], v[218:225], v[176:183], 0
	v_mfma_f32_16x16x128_f8f6f4 v[112:115], v[226:233], v[176:183], 0
	v_mfma_f32_16x16x128_f8f6f4 v[100:103], v[218:225], v[184:191], 0
	v_mfma_f32_16x16x128_f8f6f4 v[96:99], v[226:233], v[184:191], 0
	v_mfma_f32_16x16x128_f8f6f4 v[84:87], v[218:225], v[196:203], 0
	v_mfma_f32_16x16x128_f8f6f4 v[80:83], v[226:233], v[196:203], 0
	v_mfma_f32_16x16x128_f8f6f4 v[68:71], v[218:225], v[204:211], 0
	v_mfma_f32_16x16x128_f8f6f4 v[64:67], v[226:233], v[204:211], 0
	s_setprio 0
	s_barrier
	s_mov_b32 m0, s1
	ds_read_b128 v[176:179], v145 offset:16384
	ds_read_b128 v[184:187], v145 offset:18432
	ds_read_b128 v[180:183], v146 offset:16384
	ds_read_b128 v[188:191], v146 offset:18432
	ds_read_b128 v[196:199], v145 offset:20480
	ds_read_b128 v[204:207], v145 offset:22528
	ds_read_b128 v[200:203], v146 offset:20480
	ds_read_b128 v[208:211], v146 offset:22528
	global_load_lds_dwordx4 v132, s[36:37]
	s_mov_b32 m0, s48
	v_mov_b32_e32 v141, v133
	global_load_lds_dwordx4 v140, s[36:37]
	s_waitcnt lgkmcnt(8)
	s_barrier
	s_waitcnt lgkmcnt(0)
	v_lshl_add_u64 v[192:193], s[36:37], 0, v[132:133]
	v_lshl_add_u64 v[212:213], s[36:37], 0, v[140:141]
	s_setprio 1
	s_waitcnt lgkmcnt(0)
	v_mfma_f32_16x16x128_f8f6f4 v[60:63], v[160:167], v[176:183], 0
	v_mfma_f32_16x16x128_f8f6f4 v[56:59], v[168:175], v[176:183], 0
	v_mfma_f32_16x16x128_f8f6f4 v[44:47], v[160:167], v[184:191], 0
	v_mfma_f32_16x16x128_f8f6f4 v[40:43], v[168:175], v[184:191], 0
	v_mfma_f32_16x16x128_f8f6f4 v[28:31], v[160:167], v[196:203], 0
	v_mfma_f32_16x16x128_f8f6f4 v[24:27], v[168:175], v[196:203], 0
	v_mfma_f32_16x16x128_f8f6f4 v[12:15], v[160:167], v[204:211], 0
	v_mfma_f32_16x16x128_f8f6f4 v[8:11], v[168:175], v[204:211], 0
	s_setprio 0
	s_barrier
	s_mov_b32 m0, s46
	v_lshl_add_u64 v[140:141], s[40:41], 0, v[130:131]
	global_load_lds_dwordx4 v[140:141], off
	v_lshl_add_u64 v[142:143], s[40:41], 0, v[128:129]
	s_mov_b32 m0, s47
	s_nop 0
	global_load_lds_dwordx4 v[142:143], off
	s_waitcnt vmcnt(8)
	s_waitcnt lgkmcnt(0)
	s_barrier
	s_setprio 1
	s_waitcnt lgkmcnt(0)
	v_mfma_f32_16x16x128_f8f6f4 v[52:55], v[218:225], v[176:183], 0
	v_mfma_f32_16x16x128_f8f6f4 v[48:51], v[226:233], v[176:183], 0
	v_mfma_f32_16x16x128_f8f6f4 v[36:39], v[218:225], v[184:191], 0
	v_mfma_f32_16x16x128_f8f6f4 v[32:35], v[226:233], v[184:191], 0
	v_mfma_f32_16x16x128_f8f6f4 v[20:23], v[218:225], v[196:203], 0
	v_mfma_f32_16x16x128_f8f6f4 v[16:19], v[226:233], v[196:203], 0
	v_mfma_f32_16x16x128_f8f6f4 v[4:7], v[218:225], v[204:211], 0
	v_mfma_f32_16x16x128_f8f6f4 v[0:3], v[226:233], v[204:211], 0
	s_setprio 0
	s_barrier
	ds_read_b128 v[160:163], v147 offset:32768
	ds_read_b128 v[168:171], v147 offset:34816
	ds_read_b128 v[164:167], v148 offset:32768
	ds_read_b128 v[172:175], v148 offset:34816
	s_mov_b32 m0, s51
	ds_read_b128 v[176:179], v145 offset:32768
	ds_read_b128 v[184:187], v145 offset:34816
	ds_read_b128 v[180:183], v146 offset:32768
	ds_read_b128 v[188:191], v146 offset:34816
	ds_read_b128 v[196:199], v145 offset:36864
	ds_read_b128 v[204:207], v145 offset:38912
	ds_read_b128 v[200:203], v146 offset:36864
	ds_read_b128 v[208:211], v146 offset:38912
	v_cndmask_b32_e64 v132, v138, v158, s[30:31]
	global_load_lds_dwordx4 v159, s[36:37]
	s_mov_b32 m0, s52
	s_nop 0
	global_load_lds_dwordx4 v132, s[36:37]
	s_waitcnt vmcnt(8)
	s_waitcnt lgkmcnt(8)
	s_barrier
	s_waitcnt lgkmcnt(0)
	s_setprio 1
	s_waitcnt lgkmcnt(0)
	v_mfma_f32_16x16x128_f8f6f4 v[124:127], v[160:167], v[176:183], v[124:127]
	v_mfma_f32_16x16x128_f8f6f4 v[120:123], v[168:175], v[176:183], v[120:123]
	v_mfma_f32_16x16x128_f8f6f4 v[108:111], v[160:167], v[184:191], v[108:111]
	v_mfma_f32_16x16x128_f8f6f4 v[104:107], v[168:175], v[184:191], v[104:107]
	v_mfma_f32_16x16x128_f8f6f4 v[92:95], v[160:167], v[196:203], v[92:95]
	v_mfma_f32_16x16x128_f8f6f4 v[88:91], v[168:175], v[196:203], v[88:91]
	v_mfma_f32_16x16x128_f8f6f4 v[76:79], v[160:167], v[204:211], v[76:79]
	v_mfma_f32_16x16x128_f8f6f4 v[72:75], v[168:175], v[204:211], v[72:75]
	s_setprio 0
	s_barrier
	ds_read_b128 v[218:221], v147 offset:49152
	ds_read_b128 v[226:229], v147 offset:51200
	ds_read_b128 v[222:225], v148 offset:49152
	ds_read_b128 v[230:233], v148 offset:51200
	v_lshl_add_u64 v[214:215], s[38:39], 0, v[130:131]
	s_mov_b32 m0, s49
	s_nop 0
	global_load_lds_dwordx4 v[214:215], off
	v_lshl_add_u64 v[214:215], s[38:39], 0, v[128:129]
	s_mov_b32 m0, s50
	s_nop 0
	global_load_lds_dwordx4 v[214:215], off
	s_waitcnt vmcnt(8)
	s_barrier
	s_waitcnt lgkmcnt(0)
	s_setprio 1
	s_waitcnt lgkmcnt(0)
	v_mfma_f32_16x16x128_f8f6f4 v[116:119], v[218:225], v[176:183], v[116:119]
	v_mfma_f32_16x16x128_f8f6f4 v[112:115], v[226:233], v[176:183], v[112:115]
	v_mfma_f32_16x16x128_f8f6f4 v[100:103], v[218:225], v[184:191], v[100:103]
	v_mfma_f32_16x16x128_f8f6f4 v[96:99], v[226:233], v[184:191], v[96:99]
	v_mfma_f32_16x16x128_f8f6f4 v[84:87], v[218:225], v[196:203], v[84:87]
	v_mfma_f32_16x16x128_f8f6f4 v[80:83], v[226:233], v[196:203], v[80:83]
	v_mfma_f32_16x16x128_f8f6f4 v[68:71], v[218:225], v[204:211], v[68:71]
	v_mfma_f32_16x16x128_f8f6f4 v[64:67], v[226:233], v[204:211], v[64:67]
	s_setprio 0
	s_barrier
	s_mov_b32 m0, s56
	v_lshl_add_u64 v[192:193], v[192:193], 0, s[16:17]
	ds_read_b128 v[176:179], v145 offset:49152
	ds_read_b128 v[184:187], v145 offset:51200
	ds_read_b128 v[180:183], v146 offset:49152
	ds_read_b128 v[188:191], v146 offset:51200
	ds_read_b128 v[196:199], v145 offset:53248
	ds_read_b128 v[204:207], v145 offset:55296
	ds_read_b128 v[200:203], v146 offset:53248
	ds_read_b128 v[208:211], v146 offset:55296
	global_load_lds_dwordx4 v[192:193], off
	v_lshl_add_u64 v[192:193], v[212:213], 0, s[16:17]
	s_mov_b32 m0, s57
	s_nop 0
	global_load_lds_dwordx4 v[192:193], off
	s_waitcnt lgkmcnt(8)
	s_barrier
	s_waitcnt lgkmcnt(0)
	s_setprio 1
	s_waitcnt lgkmcnt(0)
	v_mfma_f32_16x16x128_f8f6f4 v[60:63], v[160:167], v[176:183], v[60:63]
	v_mfma_f32_16x16x128_f8f6f4 v[56:59], v[168:175], v[176:183], v[56:59]
	v_mfma_f32_16x16x128_f8f6f4 v[44:47], v[160:167], v[184:191], v[44:47]
	v_mfma_f32_16x16x128_f8f6f4 v[40:43], v[168:175], v[184:191], v[40:43]
	v_mfma_f32_16x16x128_f8f6f4 v[28:31], v[160:167], v[196:203], v[28:31]
	v_mfma_f32_16x16x128_f8f6f4 v[24:27], v[168:175], v[196:203], v[24:27]
	v_mfma_f32_16x16x128_f8f6f4 v[12:15], v[160:167], v[204:211], v[12:15]
	v_mfma_f32_16x16x128_f8f6f4 v[8:11], v[168:175], v[204:211], v[8:11]
	s_setprio 0
	s_barrier
	s_mov_b32 m0, s54
	v_lshl_add_u64 v[140:141], v[140:141], 0, s[16:17]
	global_load_lds_dwordx4 v[140:141], off
	v_lshl_add_u64 v[140:141], v[142:143], 0, s[16:17]
	s_mov_b32 m0, s55
	s_nop 0
	global_load_lds_dwordx4 v[140:141], off
	s_waitcnt vmcnt(8)
	s_waitcnt lgkmcnt(0)
	s_barrier
	s_setprio 1
	s_waitcnt lgkmcnt(0)
	v_mfma_f32_16x16x128_f8f6f4 v[52:55], v[218:225], v[176:183], v[52:55]
	v_mfma_f32_16x16x128_f8f6f4 v[48:51], v[226:233], v[176:183], v[48:51]
	v_mfma_f32_16x16x128_f8f6f4 v[36:39], v[218:225], v[184:191], v[36:39]
	v_mfma_f32_16x16x128_f8f6f4 v[32:35], v[226:233], v[184:191], v[32:35]
	v_mfma_f32_16x16x128_f8f6f4 v[20:23], v[218:225], v[196:203], v[20:23]
	v_mfma_f32_16x16x128_f8f6f4 v[16:19], v[226:233], v[196:203], v[16:19]
	v_mfma_f32_16x16x128_f8f6f4 v[4:7], v[218:225], v[204:211], v[4:7]
	v_mfma_f32_16x16x128_f8f6f4 v[0:3], v[226:233], v[204:211], v[0:3]
	s_setprio 0
	s_barrier
	s_mov_b32 m0, s58
	v_lshl_add_u64 v[140:141], s[34:35], 0, v[130:131]
	global_load_lds_dwordx4 v[140:141], off
	v_lshl_add_u64 v[140:141], s[34:35], 0, v[128:129]
	s_mov_b32 m0, s59
	s_andn2_b64 vcc, exec, s[28:29]
	global_load_lds_dwordx4 v[140:141], off
	s_mov_b64 s[30:31], -1
	s_mov_b64 s[28:29], 0
	s_mov_b64 s[34:35], 0x100
	s_cbranch_vccz .LBB0_1081
	s_branch .Lpeel_after_1081
.LBB0_1081:
	s_add_u32 s42, s10, s34
	s_addc_u32 s43, s11, s35
	s_add_u32 s38, s42, 0x100
	s_addc_u32 s39, s43, 0
	s_and_b64 s[36:37], s[30:31], exec
	s_cselect_b32 s36, s10, s38
	s_cselect_b32 s37, s11, s39
	s_add_u32 s34, s26, s34
	s_addc_u32 s35, s27, s35
	s_add_u32 s38, s34, 0x100
	s_addc_u32 s39, s35, 0
	ds_read_b128 v[160:163], v147
	ds_read_b128 v[168:171], v147 offset:2048
	ds_read_b128 v[164:167], v148
	ds_read_b128 v[172:175], v148 offset:2048
	s_and_b64 s[34:35], s[30:31], exec
	s_cselect_b32 s41, s25, s39
	s_cselect_b32 s40, s24, s38
	ds_read_b128 v[176:179], v145
	ds_read_b128 v[184:187], v145 offset:2048
	ds_read_b128 v[180:183], v146
	ds_read_b128 v[188:191], v146 offset:2048
	ds_read_b128 v[196:199], v145 offset:4096
	ds_read_b128 v[204:207], v145 offset:6144
	ds_read_b128 v[200:203], v146 offset:4096
	ds_read_b128 v[208:211], v146 offset:6144
	s_waitcnt vmcnt(6)
	s_waitcnt lgkmcnt(8)
	s_barrier
	s_waitcnt lgkmcnt(0)
	v_cndmask_b32_e64 v140, v134, v156, s[30:31]
	s_setprio 1
	s_waitcnt lgkmcnt(0)
	v_mfma_f32_16x16x128_f8f6f4 v[124:127], v[160:167], v[176:183], v[124:127]
	v_mfma_f32_16x16x128_f8f6f4 v[120:123], v[168:175], v[176:183], v[120:123]
	v_mfma_f32_16x16x128_f8f6f4 v[108:111], v[160:167], v[184:191], v[108:111]
	v_mfma_f32_16x16x128_f8f6f4 v[104:107], v[168:175], v[184:191], v[104:107]
	v_mfma_f32_16x16x128_f8f6f4 v[92:95], v[160:167], v[196:203], v[92:95]
	v_mfma_f32_16x16x128_f8f6f4 v[88:91], v[168:175], v[196:203], v[88:91]
	v_mfma_f32_16x16x128_f8f6f4 v[76:79], v[160:167], v[204:211], v[76:79]
	v_mfma_f32_16x16x128_f8f6f4 v[72:75], v[168:175], v[204:211], v[72:75]
	s_setprio 0
	s_barrier
	ds_read_b128 v[218:221], v147 offset:16384
	ds_read_b128 v[226:229], v147 offset:18432
	ds_read_b128 v[222:225], v148 offset:16384
	ds_read_b128 v[230:233], v148 offset:18432
	s_add_i32 m0, s1, 0xc000
	s_add_i32 s64, s1, 0xe000
	s_add_u32 s38, s40, 0x1000
	s_addc_u32 s39, s41, 0
	s_add_u32 s34, s40, 0x1080
	s_addc_u32 s35, s41, 0
	v_cndmask_b32_e64 v132, v135, v155, s[30:31]
	v_cndmask_b32_e64 v159, v136, v157, s[30:31]
	v_lshl_add_u64 v[252:253], s[42:43], 0, v[136:137]
	v_lshl_add_u64 v[252:253], v[252:253], 0, s[16:17]
	global_load_lds_dwordx4 v[252:253], off
	v_lshl_add_u64 v[252:253], s[42:43], 0, v[138:139]
	v_lshl_add_u64 v[252:253], v[252:253], 0, s[16:17]
	s_mov_b32 m0, s64
	s_nop 0
	global_load_lds_dwordx4 v[252:253], off
	s_barrier
	s_waitcnt lgkmcnt(0)
	s_setprio 1
	s_waitcnt lgkmcnt(0)
	v_mfma_f32_16x16x128_f8f6f4 v[116:119], v[218:225], v[176:183], v[116:119]
	v_mfma_f32_16x16x128_f8f6f4 v[112:115], v[226:233], v[176:183], v[112:115]
	v_mfma_f32_16x16x128_f8f6f4 v[100:103], v[218:225], v[184:191], v[100:103]
	v_mfma_f32_16x16x128_f8f6f4 v[96:99], v[226:233], v[184:191], v[96:99]
	v_mfma_f32_16x16x128_f8f6f4 v[84:87], v[218:225], v[196:203], v[84:87]
	v_mfma_f32_16x16x128_f8f6f4 v[80:83], v[226:233], v[196:203], v[80:83]
	v_mfma_f32_16x16x128_f8f6f4 v[68:71], v[218:225], v[204:211], v[68:71]
	v_mfma_f32_16x16x128_f8f6f4 v[64:67], v[226:233], v[204:211], v[64:67]
	s_setprio 0
	s_barrier
	s_mov_b32 m0, s1
	ds_read_b128 v[176:179], v145 offset:16384
	ds_read_b128 v[184:187], v145 offset:18432
	ds_read_b128 v[180:183], v146 offset:16384
	ds_read_b128 v[188:191], v146 offset:18432
	ds_read_b128 v[196:199], v145 offset:20480
	ds_read_b128 v[204:207], v145 offset:22528
	ds_read_b128 v[200:203], v146 offset:20480
	ds_read_b128 v[208:211], v146 offset:22528
	global_load_lds_dwordx4 v132, s[36:37]
	s_mov_b32 m0, s48
	v_mov_b32_e32 v141, v133
	global_load_lds_dwordx4 v140, s[36:37]
	s_waitcnt lgkmcnt(8)
	s_barrier
	s_waitcnt lgkmcnt(0)
	v_lshl_add_u64 v[192:193], s[36:37], 0, v[132:133]
	v_lshl_add_u64 v[212:213], s[36:37], 0, v[140:141]
	s_setprio 1
	s_waitcnt lgkmcnt(0)
	v_mfma_f32_16x16x128_f8f6f4 v[60:63], v[160:167], v[176:183], v[60:63]
	v_mfma_f32_16x16x128_f8f6f4 v[56:59], v[168:175], v[176:183], v[56:59]
	v_mfma_f32_16x16x128_f8f6f4 v[44:47], v[160:167], v[184:191], v[44:47]
	v_mfma_f32_16x16x128_f8f6f4 v[40:43], v[168:175], v[184:191], v[40:43]
	v_mfma_f32_16x16x128_f8f6f4 v[28:31], v[160:167], v[196:203], v[28:31]
	v_mfma_f32_16x16x128_f8f6f4 v[24:27], v[168:175], v[196:203], v[24:27]
	v_mfma_f32_16x16x128_f8f6f4 v[12:15], v[160:167], v[204:211], v[12:15]
	v_mfma_f32_16x16x128_f8f6f4 v[8:11], v[168:175], v[204:211], v[8:11]
	s_setprio 0
	s_barrier
	s_mov_b32 m0, s46
	v_lshl_add_u64 v[140:141], s[40:41], 0, v[130:131]
	global_load_lds_dwordx4 v[140:141], off
	v_lshl_add_u64 v[142:143], s[40:41], 0, v[128:129]
	s_mov_b32 m0, s47
	s_nop 0
	global_load_lds_dwordx4 v[142:143], off
	s_waitcnt vmcnt(8)
	s_waitcnt lgkmcnt(0)
	s_barrier
	s_setprio 1
	s_waitcnt lgkmcnt(0)
	v_mfma_f32_16x16x128_f8f6f4 v[52:55], v[218:225], v[176:183], v[52:55]
	v_mfma_f32_16x16x128_f8f6f4 v[48:51], v[226:233], v[176:183], v[48:51]
	v_mfma_f32_16x16x128_f8f6f4 v[36:39], v[218:225], v[184:191], v[36:39]
	v_mfma_f32_16x16x128_f8f6f4 v[32:35], v[226:233], v[184:191], v[32:35]
	v_mfma_f32_16x16x128_f8f6f4 v[20:23], v[218:225], v[196:203], v[20:23]
	v_mfma_f32_16x16x128_f8f6f4 v[16:19], v[226:233], v[196:203], v[16:19]
	v_mfma_f32_16x16x128_f8f6f4 v[4:7], v[218:225], v[204:211], v[4:7]
	v_mfma_f32_16x16x128_f8f6f4 v[0:3], v[226:233], v[204:211], v[0:3]
	s_setprio 0
	s_barrier
	ds_read_b128 v[160:163], v147 offset:32768
	ds_read_b128 v[168:171], v147 offset:34816
	ds_read_b128 v[164:167], v148 offset:32768
	ds_read_b128 v[172:175], v148 offset:34816
	s_mov_b32 m0, s51
	ds_read_b128 v[176:179], v145 offset:32768
	ds_read_b128 v[184:187], v145 offset:34816
	ds_read_b128 v[180:183], v146 offset:32768
	ds_read_b128 v[188:191], v146 offset:34816
	ds_read_b128 v[196:199], v145 offset:36864
	ds_read_b128 v[204:207], v145 offset:38912
	ds_read_b128 v[200:203], v146 offset:36864
	ds_read_b128 v[208:211], v146 offset:38912
	v_cndmask_b32_e64 v132, v138, v158, s[30:31]
	global_load_lds_dwordx4 v159, s[36:37]
	s_mov_b32 m0, s52
	s_nop 0
	global_load_lds_dwordx4 v132, s[36:37]
	s_waitcnt vmcnt(8)
	s_waitcnt lgkmcnt(8)
	s_barrier
	s_waitcnt lgkmcnt(0)
	s_setprio 1
	s_waitcnt lgkmcnt(0)
	v_mfma_f32_16x16x128_f8f6f4 v[124:127], v[160:167], v[176:183], v[124:127]
	v_mfma_f32_16x16x128_f8f6f4 v[120:123], v[168:175], v[176:183], v[120:123]
	v_mfma_f32_16x16x128_f8f6f4 v[108:111], v[160:167], v[184:191], v[108:111]
	v_mfma_f32_16x16x128_f8f6f4 v[104:107], v[168:175], v[184:191], v[104:107]
	v_mfma_f32_16x16x128_f8f6f4 v[92:95], v[160:167], v[196:203], v[92:95]
	v_mfma_f32_16x16x128_f8f6f4 v[88:91], v[168:175], v[196:203], v[88:91]
	v_mfma_f32_16x16x128_f8f6f4 v[76:79], v[160:167], v[204:211], v[76:79]
	v_mfma_f32_16x16x128_f8f6f4 v[72:75], v[168:175], v[204:211], v[72:75]
	s_setprio 0
	s_barrier
	ds_read_b128 v[218:221], v147 offset:49152
	ds_read_b128 v[226:229], v147 offset:51200
	ds_read_b128 v[222:225], v148 offset:49152
	ds_read_b128 v[230:233], v148 offset:51200
	v_lshl_add_u64 v[214:215], s[38:39], 0, v[130:131]
	s_mov_b32 m0, s49
	s_nop 0
	global_load_lds_dwordx4 v[214:215], off
	v_lshl_add_u64 v[214:215], s[38:39], 0, v[128:129]
	s_mov_b32 m0, s50
	s_nop 0
	global_load_lds_dwordx4 v[214:215], off
	s_waitcnt vmcnt(8)
	s_barrier
	s_waitcnt lgkmcnt(0)
	s_setprio 1
	s_waitcnt lgkmcnt(0)
	v_mfma_f32_16x16x128_f8f6f4 v[116:119], v[218:225], v[176:183], v[116:119]
	v_mfma_f32_16x16x128_f8f6f4 v[112:115], v[226:233], v[176:183], v[112:115]
	v_mfma_f32_16x16x128_f8f6f4 v[100:103], v[218:225], v[184:191], v[100:103]
	v_mfma_f32_16x16x128_f8f6f4 v[96:99], v[226:233], v[184:191], v[96:99]
	v_mfma_f32_16x16x128_f8f6f4 v[84:87], v[218:225], v[196:203], v[84:87]
	v_mfma_f32_16x16x128_f8f6f4 v[80:83], v[226:233], v[196:203], v[80:83]
	v_mfma_f32_16x16x128_f8f6f4 v[68:71], v[218:225], v[204:211], v[68:71]
	v_mfma_f32_16x16x128_f8f6f4 v[64:67], v[226:233], v[204:211], v[64:67]
	s_setprio 0
	s_barrier
	s_mov_b32 m0, s56
	v_lshl_add_u64 v[192:193], v[192:193], 0, s[16:17]
	ds_read_b128 v[176:179], v145 offset:49152
	ds_read_b128 v[184:187], v145 offset:51200
	ds_read_b128 v[180:183], v146 offset:49152
	ds_read_b128 v[188:191], v146 offset:51200
	ds_read_b128 v[196:199], v145 offset:53248
	ds_read_b128 v[204:207], v145 offset:55296
	ds_read_b128 v[200:203], v146 offset:53248
	ds_read_b128 v[208:211], v146 offset:55296
	global_load_lds_dwordx4 v[192:193], off
	v_lshl_add_u64 v[192:193], v[212:213], 0, s[16:17]
	s_mov_b32 m0, s57
	s_nop 0
	global_load_lds_dwordx4 v[192:193], off
	s_waitcnt lgkmcnt(8)
	s_barrier
	s_waitcnt lgkmcnt(0)
	s_setprio 1
	s_waitcnt lgkmcnt(0)
	v_mfma_f32_16x16x128_f8f6f4 v[60:63], v[160:167], v[176:183], v[60:63]
	v_mfma_f32_16x16x128_f8f6f4 v[56:59], v[168:175], v[176:183], v[56:59]
	v_mfma_f32_16x16x128_f8f6f4 v[44:47], v[160:167], v[184:191], v[44:47]
	v_mfma_f32_16x16x128_f8f6f4 v[40:43], v[168:175], v[184:191], v[40:43]
	v_mfma_f32_16x16x128_f8f6f4 v[28:31], v[160:167], v[196:203], v[28:31]
	v_mfma_f32_16x16x128_f8f6f4 v[24:27], v[168:175], v[196:203], v[24:27]
	v_mfma_f32_16x16x128_f8f6f4 v[12:15], v[160:167], v[204:211], v[12:15]
	v_mfma_f32_16x16x128_f8f6f4 v[8:11], v[168:175], v[204:211], v[8:11]
	s_setprio 0
	s_barrier
	s_mov_b32 m0, s54
	v_lshl_add_u64 v[140:141], v[140:141], 0, s[16:17]
	global_load_lds_dwordx4 v[140:141], off
	v_lshl_add_u64 v[140:141], v[142:143], 0, s[16:17]
	s_mov_b32 m0, s55
	s_nop 0
	global_load_lds_dwordx4 v[140:141], off
	s_waitcnt vmcnt(8)
	s_waitcnt lgkmcnt(0)
	s_barrier
	s_setprio 1
	s_waitcnt lgkmcnt(0)
	v_mfma_f32_16x16x128_f8f6f4 v[52:55], v[218:225], v[176:183], v[52:55]
	v_mfma_f32_16x16x128_f8f6f4 v[48:51], v[226:233], v[176:183], v[48:51]
	v_mfma_f32_16x16x128_f8f6f4 v[36:39], v[218:225], v[184:191], v[36:39]
	v_mfma_f32_16x16x128_f8f6f4 v[32:35], v[226:233], v[184:191], v[32:35]
	v_mfma_f32_16x16x128_f8f6f4 v[20:23], v[218:225], v[196:203], v[20:23]
	v_mfma_f32_16x16x128_f8f6f4 v[16:19], v[226:233], v[196:203], v[16:19]
	v_mfma_f32_16x16x128_f8f6f4 v[4:7], v[218:225], v[204:211], v[4:7]
	v_mfma_f32_16x16x128_f8f6f4 v[0:3], v[226:233], v[204:211], v[0:3]
	s_setprio 0
	s_barrier
	s_mov_b32 m0, s58
	v_lshl_add_u64 v[140:141], s[34:35], 0, v[130:131]
	global_load_lds_dwordx4 v[140:141], off
	v_lshl_add_u64 v[140:141], s[34:35], 0, v[128:129]
	s_mov_b32 m0, s59
	s_andn2_b64 vcc, exec, s[28:29]
	global_load_lds_dwordx4 v[140:141], off
	s_mov_b64 s[30:31], -1
	s_mov_b64 s[28:29], 0
	s_mov_b64 s[34:35], 0x100
	s_cbranch_vccz .LBB0_1081

.LBB0_1248:
	s_add_u32 s33, s16, s46
	s_addc_u32 s48, s17, s47
	s_add_u32 s33, s33, 0x3d000100
	ds_read_b128 v[148:151], v164
	ds_read_b128 v[204:207], v164 offset:2048
	ds_read_b128 v[152:155], v165
	ds_read_b128 v[208:211], v165 offset:2048
	s_addc_u32 s50, s48, 0
	s_add_u32 s56, s0, s46
	s_addc_u32 s57, s1, s47
	s_cmpk_eq_i32 s46, 0x700
	s_cselect_b64 vcc, -1, 0
	s_and_b64 s[48:49], vcc, exec
	ds_read_b128 v[212:215], v162
	ds_read_b128 v[220:223], v162 offset:2048
	ds_read_b128 v[216:219], v163
	ds_read_b128 v[224:227], v163 offset:2048
	ds_read_b128 v[228:231], v162 offset:4096
	ds_read_b128 v[236:239], v162 offset:6144
	ds_read_b128 v[232:235], v163 offset:4096
	ds_read_b128 v[240:243], v163 offset:6144
	s_waitcnt vmcnt(6)
	s_waitcnt lgkmcnt(8)
	s_barrier
	s_waitcnt lgkmcnt(0)
	v_cndmask_b32_e32 v156, v138, v201, vcc
	s_setprio 1
	s_waitcnt lgkmcnt(0)
	v_mfma_f32_16x16x128_f8f6f4 v[124:127], v[148:155], v[212:219], v[124:127]
	v_mfma_f32_16x16x128_f8f6f4 v[120:123], v[204:211], v[212:219], v[120:123]
	v_mfma_f32_16x16x128_f8f6f4 v[108:111], v[148:155], v[220:227], v[108:111]
	v_mfma_f32_16x16x128_f8f6f4 v[104:107], v[204:211], v[220:227], v[104:107]
	v_mfma_f32_16x16x128_f8f6f4 v[92:95], v[148:155], v[228:235], v[92:95]
	v_mfma_f32_16x16x128_f8f6f4 v[88:91], v[204:211], v[228:235], v[88:91]
	v_mfma_f32_16x16x128_f8f6f4 v[76:79], v[148:155], v[236:243], v[76:79]
	v_mfma_f32_16x16x128_f8f6f4 v[72:75], v[204:211], v[236:243], v[72:75]
	s_setprio 0
	s_barrier
	ds_read_b128 v[148:151], v164 offset:16384
	ds_read_b128 v[204:207], v164 offset:18432
	ds_read_b128 v[152:155], v165 offset:16384
	ds_read_b128 v[208:211], v165 offset:18432
	v_cndmask_b32_e32 v132, v139, v200, vcc
	s_cselect_b32 s51, s19, s50
	s_cselect_b32 s50, s18, s33
	s_cselect_b32 s49, s45, s57
	s_cselect_b32 s48, s44, s56
	v_cndmask_b32_e32 v141, v140, v202, vcc
	v_lshl_add_u64 v[252:253], v[146:147], 0, s[46:47]
	s_add_i32 m0, s39, 0xc000
	s_nop 0
	global_load_lds_dwordx4 v[252:253], off
	v_lshl_add_u64 v[252:253], v[144:145], 0, s[46:47]
	s_add_i32 m0, s39, 0xe000
	s_nop 0
	global_load_lds_dwordx4 v[252:253], off
	s_barrier
	s_waitcnt lgkmcnt(0)
	s_setprio 1
	s_waitcnt lgkmcnt(0)
	v_mfma_f32_16x16x128_f8f6f4 v[116:119], v[148:155], v[212:219], v[116:119]
	v_mfma_f32_16x16x128_f8f6f4 v[112:115], v[204:211], v[212:219], v[112:115]
	v_mfma_f32_16x16x128_f8f6f4 v[100:103], v[148:155], v[220:227], v[100:103]
	v_mfma_f32_16x16x128_f8f6f4 v[96:99], v[204:211], v[220:227], v[96:99]
	v_mfma_f32_16x16x128_f8f6f4 v[84:87], v[148:155], v[228:235], v[84:87]
	v_mfma_f32_16x16x128_f8f6f4 v[80:83], v[204:211], v[228:235], v[80:83]
	v_mfma_f32_16x16x128_f8f6f4 v[68:71], v[148:155], v[236:243], v[68:71]
	v_mfma_f32_16x16x128_f8f6f4 v[64:67], v[204:211], v[236:243], v[64:67]
	s_setprio 0
	s_barrier
	ds_read_b128 v[204:207], v164
	ds_read_b128 v[212:215], v164 offset:2048
	ds_read_b128 v[208:211], v165
	ds_read_b128 v[216:219], v165 offset:2048
	s_mov_b32 m0, s39
	ds_read_b128 v[220:223], v162 offset:16384
	ds_read_b128 v[228:231], v162 offset:18432
	ds_read_b128 v[224:227], v163 offset:16384
	ds_read_b128 v[232:235], v163 offset:18432
	ds_read_b128 v[236:239], v162 offset:20480
	ds_read_b128 v[244:247], v162 offset:22528
	ds_read_b128 v[240:243], v163 offset:20480
	ds_read_b128 v[248:251], v163 offset:22528
	global_load_lds_dwordx4 v132, s[50:51]
	s_mov_b32 m0, s54
	v_mov_b32_e32 v157, v133
	global_load_lds_dwordx4 v156, s[50:51]
	s_waitcnt lgkmcnt(8)
	s_barrier
	s_waitcnt lgkmcnt(0)
	v_lshl_add_u64 v[154:155], s[50:51], 0, v[132:133]
	v_lshl_add_u64 v[152:153], s[50:51], 0, v[156:157]
	s_setprio 1
	s_waitcnt lgkmcnt(0)
	v_mfma_f32_16x16x128_f8f6f4 v[60:63], v[204:211], v[220:227], v[60:63]
	v_mfma_f32_16x16x128_f8f6f4 v[56:59], v[212:219], v[220:227], v[56:59]
	v_mfma_f32_16x16x128_f8f6f4 v[44:47], v[204:211], v[228:235], v[44:47]
	v_mfma_f32_16x16x128_f8f6f4 v[40:43], v[212:219], v[228:235], v[40:43]
	v_mfma_f32_16x16x128_f8f6f4 v[28:31], v[204:211], v[236:243], v[28:31]
	v_mfma_f32_16x16x128_f8f6f4 v[24:27], v[212:219], v[236:243], v[24:27]
	v_mfma_f32_16x16x128_f8f6f4 v[12:15], v[204:211], v[244:251], v[12:15]
	v_mfma_f32_16x16x128_f8f6f4 v[8:11], v[212:219], v[244:251], v[8:11]
	s_setprio 0
	s_barrier
	s_mov_b32 m0, s52
	v_lshl_add_u64 v[148:149], s[48:49], 0, v[128:129]
	ds_read_b128 v[204:207], v164 offset:16384
	ds_read_b128 v[212:215], v164 offset:18432
	ds_read_b128 v[208:211], v165 offset:16384
	ds_read_b128 v[216:219], v165 offset:18432
	global_load_lds_dwordx4 v[148:149], off
	v_lshl_add_u64 v[150:151], s[48:49], 0, v[130:131]
	s_mov_b32 m0, s53
	s_nop 0
	global_load_lds_dwordx4 v[150:151], off
	s_waitcnt vmcnt(8)
	s_waitcnt lgkmcnt(0)
	s_barrier
	s_setprio 1
	s_waitcnt lgkmcnt(0)
	v_mfma_f32_16x16x128_f8f6f4 v[52:55], v[204:211], v[220:227], v[52:55]
	v_mfma_f32_16x16x128_f8f6f4 v[48:51], v[212:219], v[220:227], v[48:51]
	v_mfma_f32_16x16x128_f8f6f4 v[36:39], v[204:211], v[228:235], v[36:39]
	v_mfma_f32_16x16x128_f8f6f4 v[32:35], v[212:219], v[228:235], v[32:35]
	v_mfma_f32_16x16x128_f8f6f4 v[20:23], v[204:211], v[236:243], v[20:23]
	v_mfma_f32_16x16x128_f8f6f4 v[16:19], v[212:219], v[236:243], v[16:19]
	v_mfma_f32_16x16x128_f8f6f4 v[4:7], v[204:211], v[244:251], v[4:7]
	v_mfma_f32_16x16x128_f8f6f4 v[0:3], v[212:219], v[244:251], v[0:3]
	s_setprio 0
	s_barrier
	ds_read_b128 v[204:207], v164 offset:32768
	ds_read_b128 v[212:215], v164 offset:34816
	ds_read_b128 v[208:211], v165 offset:32768
	ds_read_b128 v[216:219], v165 offset:34816
	s_mov_b32 m0, s59
	ds_read_b128 v[220:223], v162 offset:32768
	ds_read_b128 v[228:231], v162 offset:34816
	ds_read_b128 v[224:227], v163 offset:32768
	ds_read_b128 v[232:235], v163 offset:34816
	ds_read_b128 v[236:239], v162 offset:36864
	ds_read_b128 v[244:247], v162 offset:38912
	ds_read_b128 v[240:243], v163 offset:36864
	ds_read_b128 v[248:251], v163 offset:38912
	v_cndmask_b32_e32 v132, v142, v203, vcc
	global_load_lds_dwordx4 v141, s[50:51]
	s_mov_b32 m0, s60
	s_nop 0
	global_load_lds_dwordx4 v132, s[50:51]
	s_waitcnt vmcnt(8)
	s_waitcnt lgkmcnt(8)
	s_barrier
	s_waitcnt lgkmcnt(0)
	s_setprio 1
	s_waitcnt lgkmcnt(0)
	v_mfma_f32_16x16x128_f8f6f4 v[124:127], v[204:211], v[220:227], v[124:127]
	v_mfma_f32_16x16x128_f8f6f4 v[120:123], v[212:219], v[220:227], v[120:123]
	v_mfma_f32_16x16x128_f8f6f4 v[108:111], v[204:211], v[228:235], v[108:111]
	v_mfma_f32_16x16x128_f8f6f4 v[104:107], v[212:219], v[228:235], v[104:107]
	v_mfma_f32_16x16x128_f8f6f4 v[92:95], v[204:211], v[236:243], v[92:95]
	v_mfma_f32_16x16x128_f8f6f4 v[88:91], v[212:219], v[236:243], v[88:91]
	v_mfma_f32_16x16x128_f8f6f4 v[76:79], v[204:211], v[244:251], v[76:79]
	v_mfma_f32_16x16x128_f8f6f4 v[72:75], v[212:219], v[244:251], v[72:75]
	s_setprio 0
	s_barrier
	ds_read_b128 v[204:207], v164 offset:49152
	ds_read_b128 v[212:215], v164 offset:51200
	ds_read_b128 v[208:211], v165 offset:49152
	ds_read_b128 v[216:219], v165 offset:51200
	s_add_u32 s50, s48, 0x4000
	s_addc_u32 s51, s49, 0
	v_lshl_add_u64 v[156:157], s[50:51], 0, v[128:129]
	s_mov_b32 m0, s55
	s_nop 0
	global_load_lds_dwordx4 v[156:157], off
	v_lshl_add_u64 v[156:157], s[50:51], 0, v[130:131]
	s_mov_b32 m0, s58
	s_nop 0
	global_load_lds_dwordx4 v[156:157], off
	s_waitcnt vmcnt(8)
	s_barrier
	s_waitcnt lgkmcnt(0)
	s_setprio 1
	s_waitcnt lgkmcnt(0)
	v_mfma_f32_16x16x128_f8f6f4 v[116:119], v[204:211], v[220:227], v[116:119]
	v_mfma_f32_16x16x128_f8f6f4 v[112:115], v[212:219], v[220:227], v[112:115]
	v_mfma_f32_16x16x128_f8f6f4 v[100:103], v[204:211], v[228:235], v[100:103]
	v_mfma_f32_16x16x128_f8f6f4 v[96:99], v[212:219], v[228:235], v[96:99]
	v_mfma_f32_16x16x128_f8f6f4 v[84:87], v[204:211], v[236:243], v[84:87]
	v_mfma_f32_16x16x128_f8f6f4 v[80:83], v[212:219], v[236:243], v[80:83]
	v_mfma_f32_16x16x128_f8f6f4 v[68:71], v[204:211], v[244:251], v[68:71]
	v_mfma_f32_16x16x128_f8f6f4 v[64:67], v[212:219], v[244:251], v[64:67]
	s_setprio 0
	s_barrier
	ds_read_b128 v[204:207], v164 offset:32768
	ds_read_b128 v[212:215], v164 offset:34816
	ds_read_b128 v[208:211], v165 offset:32768
	ds_read_b128 v[216:219], v165 offset:34816
	s_mov_b32 m0, s64
	v_lshl_add_u64 v[154:155], v[154:155], 0, s[30:31]
	ds_read_b128 v[220:223], v162 offset:49152
	ds_read_b128 v[228:231], v162 offset:51200
	ds_read_b128 v[224:227], v163 offset:49152
	ds_read_b128 v[232:235], v163 offset:51200
	ds_read_b128 v[236:239], v162 offset:53248
	ds_read_b128 v[244:247], v162 offset:55296
	ds_read_b128 v[240:243], v163 offset:53248
	ds_read_b128 v[248:251], v163 offset:55296
	global_load_lds_dwordx4 v[154:155], off
	v_lshl_add_u64 v[152:153], v[152:153], 0, s[30:31]
	s_mov_b32 m0, s65
	s_nop 0
	global_load_lds_dwordx4 v[152:153], off
	s_waitcnt lgkmcnt(8)
	s_barrier
	s_waitcnt lgkmcnt(0)
	s_setprio 1
	s_waitcnt lgkmcnt(0)
	v_mfma_f32_16x16x128_f8f6f4 v[60:63], v[204:211], v[220:227], v[60:63]
	v_mfma_f32_16x16x128_f8f6f4 v[56:59], v[212:219], v[220:227], v[56:59]
	v_mfma_f32_16x16x128_f8f6f4 v[44:47], v[204:211], v[228:235], v[44:47]
	v_mfma_f32_16x16x128_f8f6f4 v[40:43], v[212:219], v[228:235], v[40:43]
	v_mfma_f32_16x16x128_f8f6f4 v[28:31], v[204:211], v[236:243], v[28:31]
	v_mfma_f32_16x16x128_f8f6f4 v[24:27], v[212:219], v[236:243], v[24:27]
	v_mfma_f32_16x16x128_f8f6f4 v[12:15], v[204:211], v[244:251], v[12:15]
	v_mfma_f32_16x16x128_f8f6f4 v[8:11], v[212:219], v[244:251], v[8:11]
	s_setprio 0
	s_barrier
	s_mov_b32 m0, s62
	v_lshl_add_u64 v[148:149], v[148:149], 0, s[30:31]
	ds_read_b128 v[152:155], v164 offset:49152
	ds_read_b128 v[204:207], v164 offset:51200
	ds_read_b128 v[156:159], v165 offset:49152
	ds_read_b128 v[208:211], v165 offset:51200
	global_load_lds_dwordx4 v[148:149], off
	v_lshl_add_u64 v[148:149], v[150:151], 0, s[30:31]
	s_mov_b32 m0, s63
	s_nop 0
	global_load_lds_dwordx4 v[148:149], off
	s_waitcnt vmcnt(8)
	s_waitcnt lgkmcnt(0)
	s_barrier
	s_setprio 1
	s_waitcnt lgkmcnt(0)
	v_mfma_f32_16x16x128_f8f6f4 v[52:55], v[152:159], v[220:227], v[52:55]
	v_mfma_f32_16x16x128_f8f6f4 v[48:51], v[204:211], v[220:227], v[48:51]
	v_mfma_f32_16x16x128_f8f6f4 v[36:39], v[152:159], v[228:235], v[36:39]
	v_mfma_f32_16x16x128_f8f6f4 v[32:35], v[204:211], v[228:235], v[32:35]
	v_mfma_f32_16x16x128_f8f6f4 v[20:23], v[152:159], v[236:243], v[20:23]
	v_mfma_f32_16x16x128_f8f6f4 v[16:19], v[204:211], v[236:243], v[16:19]
	v_mfma_f32_16x16x128_f8f6f4 v[4:7], v[152:159], v[244:251], v[4:7]
	v_mfma_f32_16x16x128_f8f6f4 v[0:3], v[204:211], v[244:251], v[0:3]
	s_setprio 0
	s_barrier
	s_add_u32 s48, s48, 0x4080
	s_addc_u32 s49, s49, 0
	s_mov_b32 m0, s66
	v_lshl_add_u64 v[148:149], s[48:49], 0, v[128:129]
	global_load_lds_dwordx4 v[148:149], off
	v_lshl_add_u64 v[148:149], s[48:49], 0, v[130:131]
	s_mov_b32 m0, s67
	s_add_i32 s20, s20, 2
	global_load_lds_dwordx4 v[148:149], off
	s_add_u32 s46, s46, 0x100
	s_addc_u32 s47, s47, 0
	s_cmp_gt_u32 s20, 13
	s_cbranch_scc0 .LBB0_1248
	s_and_b64 vcc, exec, s[36:37]
	s_cbranch_vccz .LBB0_1251
	s_barrier

.LBB0_1503:
	s_add_u32 s36, s8, s34
	s_addc_u32 s37, s9, s35
	s_add_u32 s38, s36, 0x6ea00100
	ds_read_b128 v[144:147], v168
	ds_read_b128 v[152:155], v168 offset:2048
	ds_read_b128 v[148:151], v169
	ds_read_b128 v[156:159], v169 offset:2048
	s_addc_u32 s39, s37, 0
	s_add_u32 s60, s56, s34
	s_addc_u32 s61, s57, s35
	s_cmpk_eq_i32 s34, 0x700
	s_cselect_b64 vcc, -1, 0
	s_and_b64 s[36:37], vcc, exec
	ds_read_b128 v[184:187], v166
	ds_read_b128 v[196:199], v166 offset:2048
	ds_read_b128 v[188:191], v167
	ds_read_b128 v[200:203], v167 offset:2048
	ds_read_b128 v[204:207], v166 offset:4096
	ds_read_b128 v[212:215], v166 offset:6144
	ds_read_b128 v[208:211], v167 offset:4096
	ds_read_b128 v[216:219], v167 offset:6144
	s_waitcnt vmcnt(6)
	s_waitcnt lgkmcnt(8)
	s_barrier
	s_waitcnt lgkmcnt(0)
	v_cndmask_b32_e32 v160, v134, v180, vcc
	s_setprio 1
	s_waitcnt lgkmcnt(0)
	v_mfma_f32_16x16x128_f8f6f4 v[124:127], v[144:151], v[184:191], v[124:127]
	v_mfma_f32_16x16x128_f8f6f4 v[120:123], v[152:159], v[184:191], v[120:123]
	v_mfma_f32_16x16x128_f8f6f4 v[112:115], v[144:151], v[196:203], v[112:115]
	v_mfma_f32_16x16x128_f8f6f4 v[104:107], v[152:159], v[196:203], v[104:107]
	v_mfma_f32_16x16x128_f8f6f4 v[96:99], v[144:151], v[204:211], v[96:99]
	v_mfma_f32_16x16x128_f8f6f4 v[88:91], v[152:159], v[204:211], v[88:91]
	v_mfma_f32_16x16x128_f8f6f4 v[80:83], v[144:151], v[212:219], v[80:83]
	v_mfma_f32_16x16x128_f8f6f4 v[72:75], v[152:159], v[212:219], v[72:75]
	s_setprio 0
	s_barrier
	ds_read_b128 v[228:231], v168 offset:16384
	ds_read_b128 v[236:239], v168 offset:18432
	ds_read_b128 v[232:235], v169 offset:16384
	ds_read_b128 v[240:243], v169 offset:18432
	v_cndmask_b32_e32 v132, v135, v179, vcc
	s_cselect_b32 s39, s11, s39
	s_cselect_b32 s38, s10, s38
	s_cselect_b32 s37, s31, s61
	s_cselect_b32 s36, s30, s60
	v_cndmask_b32_e32 v137, v136, v181, vcc
	v_lshl_add_u64 v[252:253], v[142:143], 0, s[34:35]
	s_add_i32 m0, s27, 0xc000
	s_nop 0
	global_load_lds_dwordx4 v[252:253], off
	v_lshl_add_u64 v[252:253], v[140:141], 0, s[34:35]
	s_add_i32 m0, s27, 0xe000
	s_nop 0
	global_load_lds_dwordx4 v[252:253], off
	s_barrier
	s_waitcnt lgkmcnt(0)
	s_setprio 1
	s_waitcnt lgkmcnt(0)
	v_mfma_f32_16x16x128_f8f6f4 v[116:119], v[228:235], v[184:191], v[116:119]
	v_mfma_f32_16x16x128_f8f6f4 v[108:111], v[236:243], v[184:191], v[108:111]
	v_mfma_f32_16x16x128_f8f6f4 v[100:103], v[228:235], v[196:203], v[100:103]
	v_mfma_f32_16x16x128_f8f6f4 v[92:95], v[236:243], v[196:203], v[92:95]
	v_mfma_f32_16x16x128_f8f6f4 v[84:87], v[228:235], v[204:211], v[84:87]
	v_mfma_f32_16x16x128_f8f6f4 v[76:79], v[236:243], v[204:211], v[76:79]
	v_mfma_f32_16x16x128_f8f6f4 v[68:71], v[228:235], v[212:219], v[68:71]
	v_mfma_f32_16x16x128_f8f6f4 v[64:67], v[236:243], v[212:219], v[64:67]
	s_setprio 0
	s_barrier
	s_mov_b32 m0, s27
	ds_read_b128 v[196:199], v166 offset:16384
	ds_read_b128 v[204:207], v166 offset:18432
	ds_read_b128 v[200:203], v167 offset:16384
	ds_read_b128 v[208:211], v167 offset:18432
	ds_read_b128 v[212:215], v166 offset:20480
	ds_read_b128 v[220:223], v166 offset:22528
	ds_read_b128 v[216:219], v167 offset:20480
	ds_read_b128 v[224:227], v167 offset:22528
	global_load_lds_dwordx4 v132, s[38:39]
	s_mov_b32 m0, s41
	v_mov_b32_e32 v161, v133
	global_load_lds_dwordx4 v160, s[38:39]
	s_waitcnt lgkmcnt(8)
	s_barrier
	s_waitcnt lgkmcnt(0)
	v_lshl_add_u64 v[246:247], s[38:39], 0, v[132:133]
	v_lshl_add_u64 v[244:245], s[38:39], 0, v[160:161]
	s_setprio 1
	s_waitcnt lgkmcnt(0)
	v_mfma_f32_16x16x128_f8f6f4 v[60:63], v[144:151], v[196:203], v[60:63]
	v_mfma_f32_16x16x128_f8f6f4 v[56:59], v[152:159], v[196:203], v[56:59]
	v_mfma_f32_16x16x128_f8f6f4 v[48:51], v[144:151], v[204:211], v[48:51]
	v_mfma_f32_16x16x128_f8f6f4 v[40:43], v[152:159], v[204:211], v[40:43]
	v_mfma_f32_16x16x128_f8f6f4 v[32:35], v[144:151], v[212:219], v[32:35]
	v_mfma_f32_16x16x128_f8f6f4 v[24:27], v[152:159], v[212:219], v[24:27]
	v_mfma_f32_16x16x128_f8f6f4 v[16:19], v[144:151], v[220:227], v[16:19]
	v_mfma_f32_16x16x128_f8f6f4 v[8:11], v[152:159], v[220:227], v[8:11]
	s_setprio 0
	s_barrier
	s_mov_b32 m0, s33
	v_lshl_add_u64 v[144:145], s[36:37], 0, v[128:129]
	global_load_lds_dwordx4 v[144:145], off
	v_lshl_add_u64 v[146:147], s[36:37], 0, v[130:131]
	s_mov_b32 m0, s40
	s_nop 0
	global_load_lds_dwordx4 v[146:147], off
	s_waitcnt vmcnt(8)
	s_waitcnt lgkmcnt(0)
	s_barrier
	s_setprio 1
	s_waitcnt lgkmcnt(0)
	v_mfma_f32_16x16x128_f8f6f4 v[52:55], v[228:235], v[196:203], v[52:55]
	v_mfma_f32_16x16x128_f8f6f4 v[44:47], v[236:243], v[196:203], v[44:47]
	v_mfma_f32_16x16x128_f8f6f4 v[36:39], v[228:235], v[204:211], v[36:39]
	v_mfma_f32_16x16x128_f8f6f4 v[28:31], v[236:243], v[204:211], v[28:31]
	v_mfma_f32_16x16x128_f8f6f4 v[20:23], v[228:235], v[212:219], v[20:23]
	v_mfma_f32_16x16x128_f8f6f4 v[12:15], v[236:243], v[212:219], v[12:15]
	v_mfma_f32_16x16x128_f8f6f4 v[4:7], v[228:235], v[220:227], v[4:7]
	v_mfma_f32_16x16x128_f8f6f4 v[0:3], v[236:243], v[220:227], v[0:3]
	s_setprio 0
	s_barrier
	ds_read_b128 v[152:155], v168 offset:32768
	ds_read_b128 v[184:187], v168 offset:34816
	ds_read_b128 v[156:159], v169 offset:32768
	ds_read_b128 v[188:191], v169 offset:34816
	s_mov_b32 m0, s44
	ds_read_b128 v[196:199], v166 offset:32768
	ds_read_b128 v[204:207], v166 offset:34816
	ds_read_b128 v[200:203], v167 offset:32768
	ds_read_b128 v[208:211], v167 offset:34816
	ds_read_b128 v[212:215], v166 offset:36864
	ds_read_b128 v[220:223], v166 offset:38912
	ds_read_b128 v[216:219], v167 offset:36864
	ds_read_b128 v[224:227], v167 offset:38912
	v_cndmask_b32_e32 v132, v138, v182, vcc
	global_load_lds_dwordx4 v137, s[38:39]
	s_mov_b32 m0, s45
	s_nop 0
	global_load_lds_dwordx4 v132, s[38:39]
	s_waitcnt vmcnt(8)
	s_waitcnt lgkmcnt(8)
	s_barrier
	s_waitcnt lgkmcnt(0)
	s_setprio 1
	s_waitcnt lgkmcnt(0)
	v_mfma_f32_16x16x128_f8f6f4 v[124:127], v[152:159], v[196:203], v[124:127]
	v_mfma_f32_16x16x128_f8f6f4 v[120:123], v[184:191], v[196:203], v[120:123]
	v_mfma_f32_16x16x128_f8f6f4 v[112:115], v[152:159], v[204:211], v[112:115]
	v_mfma_f32_16x16x128_f8f6f4 v[104:107], v[184:191], v[204:211], v[104:107]
	v_mfma_f32_16x16x128_f8f6f4 v[96:99], v[152:159], v[212:219], v[96:99]
	v_mfma_f32_16x16x128_f8f6f4 v[88:91], v[184:191], v[212:219], v[88:91]
	v_mfma_f32_16x16x128_f8f6f4 v[80:83], v[152:159], v[220:227], v[80:83]
	v_mfma_f32_16x16x128_f8f6f4 v[72:75], v[184:191], v[220:227], v[72:75]
	s_setprio 0
	s_barrier
	ds_read_b128 v[228:231], v168 offset:49152
	ds_read_b128 v[236:239], v168 offset:51200
	ds_read_b128 v[232:235], v169 offset:49152
	ds_read_b128 v[240:243], v169 offset:51200
	s_add_u32 s38, s36, 0x40000
	s_addc_u32 s39, s37, 0
	v_lshl_add_u64 v[160:161], s[38:39], 0, v[128:129]
	s_mov_b32 m0, s42
	s_nop 0
	global_load_lds_dwordx4 v[160:161], off
	v_lshl_add_u64 v[160:161], s[38:39], 0, v[130:131]
	s_mov_b32 m0, s43
	s_nop 0
	global_load_lds_dwordx4 v[160:161], off
	s_waitcnt vmcnt(8)
	s_barrier
	s_waitcnt lgkmcnt(0)
	s_setprio 1
	s_waitcnt lgkmcnt(0)
	v_mfma_f32_16x16x128_f8f6f4 v[116:119], v[228:235], v[196:203], v[116:119]
	v_mfma_f32_16x16x128_f8f6f4 v[108:111], v[236:243], v[196:203], v[108:111]
	v_mfma_f32_16x16x128_f8f6f4 v[100:103], v[228:235], v[204:211], v[100:103]
	v_mfma_f32_16x16x128_f8f6f4 v[92:95], v[236:243], v[204:211], v[92:95]
	v_mfma_f32_16x16x128_f8f6f4 v[84:87], v[228:235], v[212:219], v[84:87]
	v_mfma_f32_16x16x128_f8f6f4 v[76:79], v[236:243], v[212:219], v[76:79]
	v_mfma_f32_16x16x128_f8f6f4 v[68:71], v[228:235], v[220:227], v[68:71]
	v_mfma_f32_16x16x128_f8f6f4 v[64:67], v[236:243], v[220:227], v[64:67]
	s_setprio 0
	s_barrier
	s_mov_b32 m0, s50
	v_lshl_add_u64 v[246:247], v[246:247], 0, s[16:17]
	ds_read_b128 v[196:199], v166 offset:49152
	ds_read_b128 v[204:207], v166 offset:51200
	ds_read_b128 v[200:203], v167 offset:49152
	ds_read_b128 v[208:211], v167 offset:51200
	ds_read_b128 v[212:215], v166 offset:53248
	ds_read_b128 v[220:223], v166 offset:55296
	ds_read_b128 v[216:219], v167 offset:53248
	ds_read_b128 v[224:227], v167 offset:55296
	global_load_lds_dwordx4 v[246:247], off
	v_lshl_add_u64 v[244:245], v[244:245], 0, s[16:17]
	s_mov_b32 m0, s51
	s_nop 0
	global_load_lds_dwordx4 v[244:245], off
	s_waitcnt lgkmcnt(8)
	s_barrier
	s_waitcnt lgkmcnt(0)
	s_setprio 1
	s_waitcnt lgkmcnt(0)
	v_mfma_f32_16x16x128_f8f6f4 v[60:63], v[152:159], v[196:203], v[60:63]
	v_mfma_f32_16x16x128_f8f6f4 v[56:59], v[184:191], v[196:203], v[56:59]
	v_mfma_f32_16x16x128_f8f6f4 v[48:51], v[152:159], v[204:211], v[48:51]
	v_mfma_f32_16x16x128_f8f6f4 v[40:43], v[184:191], v[204:211], v[40:43]
	v_mfma_f32_16x16x128_f8f6f4 v[32:35], v[152:159], v[212:219], v[32:35]
	v_mfma_f32_16x16x128_f8f6f4 v[24:27], v[184:191], v[212:219], v[24:27]
	v_mfma_f32_16x16x128_f8f6f4 v[16:19], v[152:159], v[220:227], v[16:19]
	v_mfma_f32_16x16x128_f8f6f4 v[8:11], v[184:191], v[220:227], v[8:11]
	s_setprio 0
	s_barrier
	s_mov_b32 m0, s48
	v_lshl_add_u64 v[144:145], v[144:145], 0, s[16:17]
	global_load_lds_dwordx4 v[144:145], off
	v_lshl_add_u64 v[144:145], v[146:147], 0, s[16:17]
	s_mov_b32 m0, s49
	s_nop 0
	global_load_lds_dwordx4 v[144:145], off
	s_waitcnt vmcnt(8)
	s_waitcnt lgkmcnt(0)
	s_barrier
	s_setprio 1
	s_waitcnt lgkmcnt(0)
	v_mfma_f32_16x16x128_f8f6f4 v[52:55], v[228:235], v[196:203], v[52:55]
	v_mfma_f32_16x16x128_f8f6f4 v[44:47], v[236:243], v[196:203], v[44:47]
	v_mfma_f32_16x16x128_f8f6f4 v[36:39], v[228:235], v[204:211], v[36:39]
	v_mfma_f32_16x16x128_f8f6f4 v[28:31], v[236:243], v[204:211], v[28:31]
	v_mfma_f32_16x16x128_f8f6f4 v[20:23], v[228:235], v[212:219], v[20:23]
	v_mfma_f32_16x16x128_f8f6f4 v[12:15], v[236:243], v[212:219], v[12:15]
	v_mfma_f32_16x16x128_f8f6f4 v[4:7], v[228:235], v[220:227], v[4:7]
	v_mfma_f32_16x16x128_f8f6f4 v[0:3], v[236:243], v[220:227], v[0:3]
	s_setprio 0
	s_barrier
	s_add_u32 s36, s36, 0x40080
	s_addc_u32 s37, s37, 0
	s_mov_b32 m0, s52
	v_lshl_add_u64 v[144:145], s[36:37], 0, v[128:129]
	global_load_lds_dwordx4 v[144:145], off
	v_lshl_add_u64 v[144:145], s[36:37], 0, v[130:131]
	s_mov_b32 m0, s53
	s_add_i32 s59, s59, 2
	global_load_lds_dwordx4 v[144:145], off
	s_add_u32 s34, s34, 0x100
	s_addc_u32 s35, s35, 0
	s_cmp_gt_u32 s59, 13
	s_cbranch_scc0 .LBB0_1503
	s_and_b64 vcc, exec, s[20:21]
	s_cbranch_vccz .LBB0_1506
	s_barrier

.LBB0_1862:
	s_add_u32 s50, s20, s48
	s_addc_u32 s51, s21, s49
	ds_read_b128 v[186:189], v197
	ds_read_b128 v[202:205], v197 offset:2048
	ds_read_b128 v[190:193], v198
	ds_read_b128 v[206:209], v198 offset:2048
	s_add_u32 s52, s50, 0x14000100
	s_addc_u32 s53, s51, 0
	s_and_b64 s[50:51], s[16:17], exec
	s_cselect_b32 s53, s27, s53
	s_cselect_b32 s52, s26, s52
	s_add_u32 s79, s56, s48
	s_addc_u32 s80, s57, s49
	s_and_b64 s[50:51], s[16:17], exec
	s_cselect_b32 s51, s43, s80
	s_cselect_b32 s50, s42, s79
	ds_read_b128 v[210:213], v195
	ds_read_b128 v[218:221], v195 offset:2048
	ds_read_b128 v[214:217], v196
	ds_read_b128 v[222:225], v196 offset:2048
	ds_read_b128 v[226:229], v195 offset:4096
	ds_read_b128 v[234:237], v195 offset:6144
	ds_read_b128 v[230:233], v196 offset:4096
	ds_read_b128 v[238:241], v196 offset:6144
	s_waitcnt vmcnt(6)
	s_waitcnt lgkmcnt(8)
	s_barrier
	s_waitcnt lgkmcnt(0)
	s_setprio 1
	s_waitcnt lgkmcnt(0)
	v_mfma_f32_16x16x128_f8f6f4 v[124:127], v[186:193], v[210:217], v[124:127]
	v_mfma_f32_16x16x128_f8f6f4 v[120:123], v[202:209], v[210:217], v[120:123]
	v_mfma_f32_16x16x128_f8f6f4 v[108:111], v[186:193], v[218:225], v[108:111]
	v_mfma_f32_16x16x128_f8f6f4 v[104:107], v[202:209], v[218:225], v[104:107]
	v_mfma_f32_16x16x128_f8f6f4 v[92:95], v[186:193], v[226:233], v[92:95]
	v_mfma_f32_16x16x128_f8f6f4 v[88:91], v[202:209], v[226:233], v[88:91]
	v_mfma_f32_16x16x128_f8f6f4 v[76:79], v[186:193], v[234:241], v[76:79]
	v_mfma_f32_16x16x128_f8f6f4 v[72:75], v[202:209], v[234:241], v[72:75]
	s_setprio 0
	s_barrier
	ds_read_b128 v[186:189], v197 offset:16384
	ds_read_b128 v[202:205], v197 offset:18432
	ds_read_b128 v[190:193], v198 offset:16384
	ds_read_b128 v[206:209], v198 offset:18432
	v_cndmask_b32_e64 v136, v175, v173, s[16:17]
	v_cndmask_b32_e64 v177, v176, v151, s[16:17]
	v_lshl_add_u64 v[242:243], v[184:185], 0, s[48:49]
	s_add_i32 m0, s45, 0xc000
	s_nop 0
	global_load_lds_dwordx4 v[242:243], off
	v_lshl_add_u64 v[242:243], v[182:183], 0, s[48:49]
	s_add_i32 m0, s45, 0xe000
	v_cndmask_b32_e64 v250, v178, v155, s[16:17]
	global_load_lds_dwordx4 v[242:243], off
	s_barrier
	s_waitcnt lgkmcnt(0)
	s_setprio 1
	s_waitcnt lgkmcnt(0)
	v_mfma_f32_16x16x128_f8f6f4 v[116:119], v[186:193], v[210:217], v[116:119]
	v_mfma_f32_16x16x128_f8f6f4 v[112:115], v[202:209], v[210:217], v[112:115]
	v_mfma_f32_16x16x128_f8f6f4 v[100:103], v[186:193], v[218:225], v[100:103]
	v_mfma_f32_16x16x128_f8f6f4 v[96:99], v[202:209], v[218:225], v[96:99]
	v_mfma_f32_16x16x128_f8f6f4 v[84:87], v[186:193], v[226:233], v[84:87]
	v_mfma_f32_16x16x128_f8f6f4 v[80:83], v[202:209], v[226:233], v[80:83]
	v_mfma_f32_16x16x128_f8f6f4 v[68:71], v[186:193], v[234:241], v[68:71]
	v_mfma_f32_16x16x128_f8f6f4 v[64:67], v[202:209], v[234:241], v[64:67]
	s_setprio 0
	s_barrier
	ds_read_b128 v[202:205], v197
	ds_read_b128 v[210:213], v197 offset:2048
	ds_read_b128 v[206:209], v198
	ds_read_b128 v[214:217], v198 offset:2048
	s_mov_b32 m0, s45
	ds_read_b128 v[218:221], v195 offset:16384
	ds_read_b128 v[226:229], v195 offset:18432
	ds_read_b128 v[222:225], v196 offset:16384
	ds_read_b128 v[230:233], v196 offset:18432
	ds_read_b128 v[234:237], v195 offset:20480
	ds_read_b128 v[242:245], v195 offset:22528
	ds_read_b128 v[238:241], v196 offset:20480
	ds_read_b128 v[246:249], v196 offset:22528
	global_load_lds_dwordx4 v136, s[52:53]
	s_mov_b32 m0, s62
	v_mov_b32_e32 v251, v137
	global_load_lds_dwordx4 v250, s[52:53]
	s_waitcnt lgkmcnt(8)
	s_barrier
	s_waitcnt lgkmcnt(0)
	v_lshl_add_u64 v[192:193], s[52:53], 0, v[136:137]
	v_lshl_add_u64 v[190:191], s[52:53], 0, v[250:251]
	s_setprio 1
	s_waitcnt lgkmcnt(0)
	v_mfma_f32_16x16x128_f8f6f4 v[60:63], v[202:209], v[218:225], v[60:63]
	v_mfma_f32_16x16x128_f8f6f4 v[56:59], v[210:217], v[218:225], v[56:59]
	v_mfma_f32_16x16x128_f8f6f4 v[44:47], v[202:209], v[226:233], v[44:47]
	v_mfma_f32_16x16x128_f8f6f4 v[40:43], v[210:217], v[226:233], v[40:43]
	v_mfma_f32_16x16x128_f8f6f4 v[28:31], v[202:209], v[234:241], v[28:31]
	v_mfma_f32_16x16x128_f8f6f4 v[24:27], v[210:217], v[234:241], v[24:27]
	v_mfma_f32_16x16x128_f8f6f4 v[12:15], v[202:209], v[242:249], v[12:15]
	v_mfma_f32_16x16x128_f8f6f4 v[8:11], v[210:217], v[242:249], v[8:11]
	s_setprio 0
	s_barrier
	s_mov_b32 m0, s60
	v_lshl_add_u64 v[186:187], s[50:51], 0, v[138:139]
	ds_read_b128 v[202:205], v197 offset:16384
	ds_read_b128 v[210:213], v197 offset:18432
	ds_read_b128 v[206:209], v198 offset:16384
	ds_read_b128 v[214:217], v198 offset:18432
	global_load_lds_dwordx4 v[186:187], off
	v_lshl_add_u64 v[188:189], s[50:51], 0, v[140:141]
	s_mov_b32 m0, s61
	s_nop 0
	global_load_lds_dwordx4 v[188:189], off
	s_waitcnt vmcnt(8)
	s_waitcnt lgkmcnt(0)
	s_barrier
	s_setprio 1
	s_waitcnt lgkmcnt(0)
	v_mfma_f32_16x16x128_f8f6f4 v[52:55], v[202:209], v[218:225], v[52:55]
	v_mfma_f32_16x16x128_f8f6f4 v[48:51], v[210:217], v[218:225], v[48:51]
	v_mfma_f32_16x16x128_f8f6f4 v[36:39], v[202:209], v[226:233], v[36:39]
	v_mfma_f32_16x16x128_f8f6f4 v[32:35], v[210:217], v[226:233], v[32:35]
	v_mfma_f32_16x16x128_f8f6f4 v[20:23], v[202:209], v[234:241], v[20:23]
	v_mfma_f32_16x16x128_f8f6f4 v[16:19], v[210:217], v[234:241], v[16:19]
	v_mfma_f32_16x16x128_f8f6f4 v[4:7], v[202:209], v[242:249], v[4:7]
	v_mfma_f32_16x16x128_f8f6f4 v[0:3], v[210:217], v[242:249], v[0:3]
	s_setprio 0
	s_barrier
	ds_read_b128 v[202:205], v197 offset:32768
	ds_read_b128 v[210:213], v197 offset:34816
	ds_read_b128 v[206:209], v198 offset:32768
	ds_read_b128 v[214:217], v198 offset:34816
	s_mov_b32 m0, s65
	v_cndmask_b32_e64 v136, v180, v179, s[16:17]
	s_add_u32 s16, s50, 0x4000
	ds_read_b128 v[218:221], v195 offset:32768
	ds_read_b128 v[226:229], v195 offset:34816
	ds_read_b128 v[222:225], v196 offset:32768
	ds_read_b128 v[230:233], v196 offset:34816
	ds_read_b128 v[234:237], v195 offset:36864
	ds_read_b128 v[242:245], v195 offset:38912
	ds_read_b128 v[238:241], v196 offset:36864
	ds_read_b128 v[246:249], v196 offset:38912
	global_load_lds_dwordx4 v177, s[52:53]
	s_mov_b32 m0, s66
	s_addc_u32 s17, s51, 0
	global_load_lds_dwordx4 v136, s[52:53]
	s_waitcnt vmcnt(8)
	s_waitcnt lgkmcnt(8)
	s_barrier
	s_waitcnt lgkmcnt(0)
	s_setprio 1
	s_waitcnt lgkmcnt(0)
	v_mfma_f32_16x16x128_f8f6f4 v[124:127], v[202:209], v[218:225], v[124:127]
	v_mfma_f32_16x16x128_f8f6f4 v[120:123], v[210:217], v[218:225], v[120:123]
	v_mfma_f32_16x16x128_f8f6f4 v[108:111], v[202:209], v[226:233], v[108:111]
	v_mfma_f32_16x16x128_f8f6f4 v[104:107], v[210:217], v[226:233], v[104:107]
	v_mfma_f32_16x16x128_f8f6f4 v[92:95], v[202:209], v[234:241], v[92:95]
	v_mfma_f32_16x16x128_f8f6f4 v[88:91], v[210:217], v[234:241], v[88:91]
	v_mfma_f32_16x16x128_f8f6f4 v[76:79], v[202:209], v[242:249], v[76:79]
	v_mfma_f32_16x16x128_f8f6f4 v[72:75], v[210:217], v[242:249], v[72:75]
	s_setprio 0
	s_barrier
	ds_read_b128 v[202:205], v197 offset:49152
	ds_read_b128 v[210:213], v197 offset:51200
	ds_read_b128 v[206:209], v198 offset:49152
	ds_read_b128 v[214:217], v198 offset:51200
	v_lshl_add_u64 v[250:251], s[16:17], 0, v[138:139]
	s_mov_b32 m0, s63
	s_nop 0
	global_load_lds_dwordx4 v[250:251], off
	v_lshl_add_u64 v[250:251], s[16:17], 0, v[140:141]
	s_mov_b32 m0, s64
	s_nop 0
	global_load_lds_dwordx4 v[250:251], off
	s_waitcnt vmcnt(8)
	s_barrier
	s_waitcnt lgkmcnt(0)
	s_setprio 1
	s_waitcnt lgkmcnt(0)
	v_mfma_f32_16x16x128_f8f6f4 v[116:119], v[202:209], v[218:225], v[116:119]
	v_mfma_f32_16x16x128_f8f6f4 v[112:115], v[210:217], v[218:225], v[112:115]
	v_mfma_f32_16x16x128_f8f6f4 v[100:103], v[202:209], v[226:233], v[100:103]
	v_mfma_f32_16x16x128_f8f6f4 v[96:99], v[210:217], v[226:233], v[96:99]
	v_mfma_f32_16x16x128_f8f6f4 v[84:87], v[202:209], v[234:241], v[84:87]
	v_mfma_f32_16x16x128_f8f6f4 v[80:83], v[210:217], v[234:241], v[80:83]
	v_mfma_f32_16x16x128_f8f6f4 v[68:71], v[202:209], v[242:249], v[68:71]
	v_mfma_f32_16x16x128_f8f6f4 v[64:67], v[210:217], v[242:249], v[64:67]
	s_setprio 0
	s_barrier
	ds_read_b128 v[202:205], v197 offset:32768
	ds_read_b128 v[210:213], v197 offset:34816
	ds_read_b128 v[206:209], v198 offset:32768
	ds_read_b128 v[214:217], v198 offset:34816
	s_mov_b32 m0, s71
	v_lshl_add_u64 v[192:193], v[192:193], 0, s[34:35]
	ds_read_b128 v[218:221], v195 offset:49152
	ds_read_b128 v[226:229], v195 offset:51200
	ds_read_b128 v[222:225], v196 offset:49152
	ds_read_b128 v[230:233], v196 offset:51200
	ds_read_b128 v[234:237], v195 offset:53248
	ds_read_b128 v[242:245], v195 offset:55296
	ds_read_b128 v[238:241], v196 offset:53248
	ds_read_b128 v[246:249], v196 offset:55296
	global_load_lds_dwordx4 v[192:193], off
	v_lshl_add_u64 v[190:191], v[190:191], 0, s[34:35]
	s_mov_b32 m0, s72
	s_nop 0
	global_load_lds_dwordx4 v[190:191], off
	s_waitcnt lgkmcnt(8)
	s_barrier
	s_waitcnt lgkmcnt(0)
	s_setprio 1
	s_waitcnt lgkmcnt(0)
	v_mfma_f32_16x16x128_f8f6f4 v[60:63], v[202:209], v[218:225], v[60:63]
	v_mfma_f32_16x16x128_f8f6f4 v[56:59], v[210:217], v[218:225], v[56:59]
	v_mfma_f32_16x16x128_f8f6f4 v[44:47], v[202:209], v[226:233], v[44:47]
	v_mfma_f32_16x16x128_f8f6f4 v[40:43], v[210:217], v[226:233], v[40:43]
	v_mfma_f32_16x16x128_f8f6f4 v[28:31], v[202:209], v[234:241], v[28:31]
	v_mfma_f32_16x16x128_f8f6f4 v[24:27], v[210:217], v[234:241], v[24:27]
	v_mfma_f32_16x16x128_f8f6f4 v[12:15], v[202:209], v[242:249], v[12:15]
	v_mfma_f32_16x16x128_f8f6f4 v[8:11], v[210:217], v[242:249], v[8:11]
	s_setprio 0
	s_barrier
	s_mov_b32 m0, s69
	v_lshl_add_u64 v[186:187], v[186:187], 0, s[34:35]
	ds_read_b128 v[202:205], v197 offset:49152
	ds_read_b128 v[210:213], v197 offset:51200
	ds_read_b128 v[206:209], v198 offset:49152
	ds_read_b128 v[214:217], v198 offset:51200
	global_load_lds_dwordx4 v[186:187], off
	v_lshl_add_u64 v[186:187], v[188:189], 0, s[34:35]
	s_mov_b32 m0, s70
	s_nop 0
	global_load_lds_dwordx4 v[186:187], off
	s_waitcnt vmcnt(8)
	s_waitcnt lgkmcnt(0)
	s_barrier
	s_setprio 1
	s_waitcnt lgkmcnt(0)
	v_mfma_f32_16x16x128_f8f6f4 v[52:55], v[202:209], v[218:225], v[52:55]
	v_mfma_f32_16x16x128_f8f6f4 v[48:51], v[210:217], v[218:225], v[48:51]
	v_mfma_f32_16x16x128_f8f6f4 v[36:39], v[202:209], v[226:233], v[36:39]
	v_mfma_f32_16x16x128_f8f6f4 v[32:35], v[210:217], v[226:233], v[32:35]
	v_mfma_f32_16x16x128_f8f6f4 v[20:23], v[202:209], v[234:241], v[20:23]
	v_mfma_f32_16x16x128_f8f6f4 v[16:19], v[210:217], v[234:241], v[16:19]
	v_mfma_f32_16x16x128_f8f6f4 v[4:7], v[202:209], v[242:249], v[4:7]
	v_mfma_f32_16x16x128_f8f6f4 v[0:3], v[210:217], v[242:249], v[0:3]
	s_setprio 0
	s_barrier
	s_add_u32 s16, s50, 0x4080
	s_addc_u32 s17, s51, 0
	s_mov_b32 m0, s73
	v_lshl_add_u64 v[186:187], s[16:17], 0, v[138:139]
	global_load_lds_dwordx4 v[186:187], off
	v_lshl_add_u64 v[186:187], s[16:17], 0, v[140:141]
	s_mov_b32 m0, s74
	s_add_i32 s78, s78, 2
	global_load_lds_dwordx4 v[186:187], off
	s_add_u32 s48, s48, 0x100
	s_addc_u32 s49, s49, 0
	s_cmp_gt_u32 s78, 13
	s_cbranch_scc1 .LBB0_1872

.LBB0_1960:
	v_mov_b32_e32 v137, v133
	v_mov_b32_e32 v139, v133
	s_mov_b64 s[44:45], 0
	s_mov_b64 s[40:41], -1
	s_mov_b64 s[42:43], 0
	s_add_u32 s52, s12, s44
	s_addc_u32 s53, s13, s45
	s_add_u32 s29, s52, 0x100
	s_addc_u32 s48, s53, 0
	s_and_b64 s[46:47], s[42:43], exec
	s_cselect_b32 s46, s12, s29
	s_cselect_b32 s47, s13, s48
	s_add_u32 s29, s38, s44
	s_addc_u32 s44, s39, s45
	s_add_u32 s29, s29, 0x100
	s_addc_u32 s48, s44, 0
	ds_read_b128 v[162:165], v147
	ds_read_b128 v[170:173], v147 offset:2048
	ds_read_b128 v[166:169], v148
	ds_read_b128 v[174:177], v148 offset:2048
	s_and_b64 s[44:45], s[42:43], exec
	s_cselect_b32 s51, s35, s48
	s_cselect_b32 s50, s34, s29
	ds_read_b128 v[178:181], v145
	ds_read_b128 v[186:189], v145 offset:2048
	ds_read_b128 v[182:185], v146
	ds_read_b128 v[190:193], v146 offset:2048
	ds_read_b128 v[196:199], v145 offset:4096
	ds_read_b128 v[204:207], v145 offset:6144
	ds_read_b128 v[200:203], v146 offset:4096
	ds_read_b128 v[208:211], v146 offset:6144
	s_waitcnt vmcnt(6)
	s_waitcnt lgkmcnt(8)
	s_barrier
	s_waitcnt lgkmcnt(0)
	v_cndmask_b32_e64 v140, v134, v158, s[42:43]
	s_setprio 1
	s_waitcnt lgkmcnt(0)
	v_mfma_f32_16x16x128_f8f6f4 v[124:127], v[162:169], v[178:185], 0
	v_mfma_f32_16x16x128_f8f6f4 v[120:123], v[170:177], v[178:185], 0
	v_mfma_f32_16x16x128_f8f6f4 v[108:111], v[162:169], v[186:193], 0
	v_mfma_f32_16x16x128_f8f6f4 v[104:107], v[170:177], v[186:193], 0
	v_mfma_f32_16x16x128_f8f6f4 v[92:95], v[162:169], v[196:203], 0
	v_mfma_f32_16x16x128_f8f6f4 v[88:91], v[170:177], v[196:203], 0
	v_mfma_f32_16x16x128_f8f6f4 v[76:79], v[162:169], v[204:211], 0
	v_mfma_f32_16x16x128_f8f6f4 v[72:75], v[170:177], v[204:211], 0
	s_setprio 0
	s_barrier
	ds_read_b128 v[218:221], v147 offset:16384
	ds_read_b128 v[226:229], v147 offset:18432
	ds_read_b128 v[222:225], v148 offset:16384
	ds_read_b128 v[230:233], v148 offset:18432
	s_add_i32 m0, s0, 0xc000
	s_add_i32 s29, s0, 0xe000
	s_add_u32 s48, s50, 0x1000
	s_addc_u32 s49, s51, 0
	s_add_u32 s44, s50, 0x1080
	s_addc_u32 s45, s51, 0
	v_cndmask_b32_e64 v132, v135, v157, s[42:43]
	v_cndmask_b32_e64 v161, v136, v159, s[42:43]
	v_lshl_add_u64 v[252:253], s[52:53], 0, v[136:137]
	v_lshl_add_u64 v[252:253], v[252:253], 0, s[20:21]
	global_load_lds_dwordx4 v[252:253], off
	v_lshl_add_u64 v[252:253], s[52:53], 0, v[138:139]
	v_lshl_add_u64 v[252:253], v[252:253], 0, s[20:21]
	s_mov_b32 m0, s29
	s_nop 0
	global_load_lds_dwordx4 v[252:253], off
	s_barrier
	s_waitcnt lgkmcnt(0)
	s_setprio 1
	s_waitcnt lgkmcnt(0)
	v_mfma_f32_16x16x128_f8f6f4 v[116:119], v[218:225], v[178:185], 0
	v_mfma_f32_16x16x128_f8f6f4 v[112:115], v[226:233], v[178:185], 0
	v_mfma_f32_16x16x128_f8f6f4 v[100:103], v[218:225], v[186:193], 0
	v_mfma_f32_16x16x128_f8f6f4 v[96:99], v[226:233], v[186:193], 0
	v_mfma_f32_16x16x128_f8f6f4 v[84:87], v[218:225], v[196:203], 0
	v_mfma_f32_16x16x128_f8f6f4 v[80:83], v[226:233], v[196:203], 0
	v_mfma_f32_16x16x128_f8f6f4 v[68:71], v[218:225], v[204:211], 0
	v_mfma_f32_16x16x128_f8f6f4 v[64:67], v[226:233], v[204:211], 0
	s_setprio 0
	s_barrier
	s_mov_b32 m0, s0
	ds_read_b128 v[178:181], v145 offset:16384
	ds_read_b128 v[186:189], v145 offset:18432
	ds_read_b128 v[182:185], v146 offset:16384
	ds_read_b128 v[190:193], v146 offset:18432
	ds_read_b128 v[196:199], v145 offset:20480
	ds_read_b128 v[204:207], v145 offset:22528
	ds_read_b128 v[200:203], v146 offset:20480
	ds_read_b128 v[208:211], v146 offset:22528
	global_load_lds_dwordx4 v132, s[46:47]
	s_mov_b32 m0, s56
	v_mov_b32_e32 v141, v133
	global_load_lds_dwordx4 v140, s[46:47]
	s_waitcnt lgkmcnt(8)
	s_barrier
	s_waitcnt lgkmcnt(0)
	v_lshl_add_u64 v[212:213], s[46:47], 0, v[132:133]
	v_lshl_add_u64 v[214:215], s[46:47], 0, v[140:141]
	s_setprio 1
	s_waitcnt lgkmcnt(0)
	v_mfma_f32_16x16x128_f8f6f4 v[60:63], v[162:169], v[178:185], 0
	v_mfma_f32_16x16x128_f8f6f4 v[56:59], v[170:177], v[178:185], 0
	v_mfma_f32_16x16x128_f8f6f4 v[44:47], v[162:169], v[186:193], 0
	v_mfma_f32_16x16x128_f8f6f4 v[40:43], v[170:177], v[186:193], 0
	v_mfma_f32_16x16x128_f8f6f4 v[28:31], v[162:169], v[196:203], 0
	v_mfma_f32_16x16x128_f8f6f4 v[24:27], v[170:177], v[196:203], 0
	v_mfma_f32_16x16x128_f8f6f4 v[12:15], v[162:169], v[204:211], 0
	v_mfma_f32_16x16x128_f8f6f4 v[8:11], v[170:177], v[204:211], 0
	s_setprio 0
	s_barrier
	s_mov_b32 m0, s1
	v_lshl_add_u64 v[140:141], s[50:51], 0, v[128:129]
	global_load_lds_dwordx4 v[140:141], off
	v_lshl_add_u64 v[142:143], s[50:51], 0, v[130:131]
	s_mov_b32 m0, s37
	s_nop 0
	global_load_lds_dwordx4 v[142:143], off
	s_waitcnt vmcnt(8)
	s_waitcnt lgkmcnt(0)
	s_barrier
	s_setprio 1
	s_waitcnt lgkmcnt(0)
	v_mfma_f32_16x16x128_f8f6f4 v[52:55], v[218:225], v[178:185], 0
	v_mfma_f32_16x16x128_f8f6f4 v[48:51], v[226:233], v[178:185], 0
	v_mfma_f32_16x16x128_f8f6f4 v[36:39], v[218:225], v[186:193], 0
	v_mfma_f32_16x16x128_f8f6f4 v[32:35], v[226:233], v[186:193], 0
	v_mfma_f32_16x16x128_f8f6f4 v[20:23], v[218:225], v[196:203], 0
	v_mfma_f32_16x16x128_f8f6f4 v[16:19], v[226:233], v[196:203], 0
	v_mfma_f32_16x16x128_f8f6f4 v[4:7], v[218:225], v[204:211], 0
	v_mfma_f32_16x16x128_f8f6f4 v[0:3], v[226:233], v[204:211], 0
	s_setprio 0
	s_barrier
	ds_read_b128 v[162:165], v147 offset:32768
	ds_read_b128 v[170:173], v147 offset:34816
	ds_read_b128 v[166:169], v148 offset:32768
	ds_read_b128 v[174:177], v148 offset:34816
	s_mov_b32 m0, s65
	ds_read_b128 v[178:181], v145 offset:32768
	ds_read_b128 v[186:189], v145 offset:34816
	ds_read_b128 v[182:185], v146 offset:32768
	ds_read_b128 v[190:193], v146 offset:34816
	ds_read_b128 v[196:199], v145 offset:36864
	ds_read_b128 v[204:207], v145 offset:38912
	ds_read_b128 v[200:203], v146 offset:36864
	ds_read_b128 v[208:211], v146 offset:38912
	v_cndmask_b32_e64 v132, v138, v160, s[42:43]
	global_load_lds_dwordx4 v161, s[46:47]
	s_mov_b32 m0, s66
	s_nop 0
	global_load_lds_dwordx4 v132, s[46:47]
	s_waitcnt vmcnt(8)
	s_waitcnt lgkmcnt(8)
	s_barrier
	s_waitcnt lgkmcnt(0)
	s_setprio 1
	s_waitcnt lgkmcnt(0)
	v_mfma_f32_16x16x128_f8f6f4 v[124:127], v[162:169], v[178:185], v[124:127]
	v_mfma_f32_16x16x128_f8f6f4 v[120:123], v[170:177], v[178:185], v[120:123]
	v_mfma_f32_16x16x128_f8f6f4 v[108:111], v[162:169], v[186:193], v[108:111]
	v_mfma_f32_16x16x128_f8f6f4 v[104:107], v[170:177], v[186:193], v[104:107]
	v_mfma_f32_16x16x128_f8f6f4 v[92:95], v[162:169], v[196:203], v[92:95]
	v_mfma_f32_16x16x128_f8f6f4 v[88:91], v[170:177], v[196:203], v[88:91]
	v_mfma_f32_16x16x128_f8f6f4 v[76:79], v[162:169], v[204:211], v[76:79]
	v_mfma_f32_16x16x128_f8f6f4 v[72:75], v[170:177], v[204:211], v[72:75]
	s_setprio 0
	s_barrier
	ds_read_b128 v[218:221], v147 offset:49152
	ds_read_b128 v[226:229], v147 offset:51200
	ds_read_b128 v[222:225], v148 offset:49152
	ds_read_b128 v[230:233], v148 offset:51200
	v_lshl_add_u64 v[216:217], s[48:49], 0, v[128:129]
	s_mov_b32 m0, s57
	s_nop 0
	global_load_lds_dwordx4 v[216:217], off
	v_lshl_add_u64 v[216:217], s[48:49], 0, v[130:131]
	s_mov_b32 m0, s64
	s_nop 0
	global_load_lds_dwordx4 v[216:217], off
	s_waitcnt vmcnt(8)
	s_barrier
	s_waitcnt lgkmcnt(0)
	s_setprio 1
	s_waitcnt lgkmcnt(0)
	v_mfma_f32_16x16x128_f8f6f4 v[116:119], v[218:225], v[178:185], v[116:119]
	v_mfma_f32_16x16x128_f8f6f4 v[112:115], v[226:233], v[178:185], v[112:115]
	v_mfma_f32_16x16x128_f8f6f4 v[100:103], v[218:225], v[186:193], v[100:103]
	v_mfma_f32_16x16x128_f8f6f4 v[96:99], v[226:233], v[186:193], v[96:99]
	v_mfma_f32_16x16x128_f8f6f4 v[84:87], v[218:225], v[196:203], v[84:87]
	v_mfma_f32_16x16x128_f8f6f4 v[80:83], v[226:233], v[196:203], v[80:83]
	v_mfma_f32_16x16x128_f8f6f4 v[68:71], v[218:225], v[204:211], v[68:71]
	v_mfma_f32_16x16x128_f8f6f4 v[64:67], v[226:233], v[204:211], v[64:67]
	s_setprio 0
	s_barrier
	s_mov_b32 m0, s69
	v_lshl_add_u64 v[212:213], v[212:213], 0, s[20:21]
	ds_read_b128 v[178:181], v145 offset:49152
	ds_read_b128 v[186:189], v145 offset:51200
	ds_read_b128 v[182:185], v146 offset:49152
	ds_read_b128 v[190:193], v146 offset:51200
	ds_read_b128 v[196:199], v145 offset:53248
	ds_read_b128 v[204:207], v145 offset:55296
	ds_read_b128 v[200:203], v146 offset:53248
	ds_read_b128 v[208:211], v146 offset:55296
	global_load_lds_dwordx4 v[212:213], off
	v_lshl_add_u64 v[212:213], v[214:215], 0, s[20:21]
	s_mov_b32 m0, s70
	s_nop 0
	global_load_lds_dwordx4 v[212:213], off
	s_waitcnt lgkmcnt(8)
	s_barrier
	s_waitcnt lgkmcnt(0)
	s_setprio 1
	s_waitcnt lgkmcnt(0)
	v_mfma_f32_16x16x128_f8f6f4 v[60:63], v[162:169], v[178:185], v[60:63]
	v_mfma_f32_16x16x128_f8f6f4 v[56:59], v[170:177], v[178:185], v[56:59]
	v_mfma_f32_16x16x128_f8f6f4 v[44:47], v[162:169], v[186:193], v[44:47]
	v_mfma_f32_16x16x128_f8f6f4 v[40:43], v[170:177], v[186:193], v[40:43]
	v_mfma_f32_16x16x128_f8f6f4 v[28:31], v[162:169], v[196:203], v[28:31]
	v_mfma_f32_16x16x128_f8f6f4 v[24:27], v[170:177], v[196:203], v[24:27]
	v_mfma_f32_16x16x128_f8f6f4 v[12:15], v[162:169], v[204:211], v[12:15]
	v_mfma_f32_16x16x128_f8f6f4 v[8:11], v[170:177], v[204:211], v[8:11]
	s_setprio 0
	s_barrier
	s_mov_b32 m0, s67
	v_lshl_add_u64 v[140:141], v[140:141], 0, s[20:21]
	global_load_lds_dwordx4 v[140:141], off
	v_lshl_add_u64 v[140:141], v[142:143], 0, s[20:21]
	s_mov_b32 m0, s68
	s_nop 0
	global_load_lds_dwordx4 v[140:141], off
	s_waitcnt vmcnt(8)
	s_waitcnt lgkmcnt(0)
	s_barrier
	s_setprio 1
	s_waitcnt lgkmcnt(0)
	v_mfma_f32_16x16x128_f8f6f4 v[52:55], v[218:225], v[178:185], v[52:55]
	v_mfma_f32_16x16x128_f8f6f4 v[48:51], v[226:233], v[178:185], v[48:51]
	v_mfma_f32_16x16x128_f8f6f4 v[36:39], v[218:225], v[186:193], v[36:39]
	v_mfma_f32_16x16x128_f8f6f4 v[32:35], v[226:233], v[186:193], v[32:35]
	v_mfma_f32_16x16x128_f8f6f4 v[20:23], v[218:225], v[196:203], v[20:23]
	v_mfma_f32_16x16x128_f8f6f4 v[16:19], v[226:233], v[196:203], v[16:19]
	v_mfma_f32_16x16x128_f8f6f4 v[4:7], v[218:225], v[204:211], v[4:7]
	v_mfma_f32_16x16x128_f8f6f4 v[0:3], v[226:233], v[204:211], v[0:3]
	s_setprio 0
	s_barrier
	s_mov_b32 m0, s71
	v_lshl_add_u64 v[140:141], s[44:45], 0, v[128:129]
	global_load_lds_dwordx4 v[140:141], off
	v_lshl_add_u64 v[140:141], s[44:45], 0, v[130:131]
	s_mov_b32 m0, s72
	s_andn2_b64 vcc, exec, s[40:41]
	global_load_lds_dwordx4 v[140:141], off
	s_mov_b64 s[42:43], -1
	s_mov_b64 s[40:41], 0
	s_mov_b64 s[44:45], 0x100
	s_cbranch_vccz .LBB0_1961
	s_branch .Lpeel_after_1961
.LBB0_1961:
	s_add_u32 s52, s12, s44
	s_addc_u32 s53, s13, s45
	s_add_u32 s29, s52, 0x100
	s_addc_u32 s48, s53, 0
	s_and_b64 s[46:47], s[42:43], exec
	s_cselect_b32 s46, s12, s29
	s_cselect_b32 s47, s13, s48
	s_add_u32 s29, s38, s44
	s_addc_u32 s44, s39, s45
	s_add_u32 s29, s29, 0x100
	s_addc_u32 s48, s44, 0
	ds_read_b128 v[162:165], v147
	ds_read_b128 v[170:173], v147 offset:2048
	ds_read_b128 v[166:169], v148
	ds_read_b128 v[174:177], v148 offset:2048
	s_and_b64 s[44:45], s[42:43], exec
	s_cselect_b32 s51, s35, s48
	s_cselect_b32 s50, s34, s29
	ds_read_b128 v[178:181], v145
	ds_read_b128 v[186:189], v145 offset:2048
	ds_read_b128 v[182:185], v146
	ds_read_b128 v[190:193], v146 offset:2048
	ds_read_b128 v[196:199], v145 offset:4096
	ds_read_b128 v[204:207], v145 offset:6144
	ds_read_b128 v[200:203], v146 offset:4096
	ds_read_b128 v[208:211], v146 offset:6144
	s_waitcnt vmcnt(6)
	s_waitcnt lgkmcnt(8)
	s_barrier
	s_waitcnt lgkmcnt(0)
	v_cndmask_b32_e64 v140, v134, v158, s[42:43]
	s_setprio 1
	s_waitcnt lgkmcnt(0)
	v_mfma_f32_16x16x128_f8f6f4 v[124:127], v[162:169], v[178:185], v[124:127]
	v_mfma_f32_16x16x128_f8f6f4 v[120:123], v[170:177], v[178:185], v[120:123]
	v_mfma_f32_16x16x128_f8f6f4 v[108:111], v[162:169], v[186:193], v[108:111]
	v_mfma_f32_16x16x128_f8f6f4 v[104:107], v[170:177], v[186:193], v[104:107]
	v_mfma_f32_16x16x128_f8f6f4 v[92:95], v[162:169], v[196:203], v[92:95]
	v_mfma_f32_16x16x128_f8f6f4 v[88:91], v[170:177], v[196:203], v[88:91]
	v_mfma_f32_16x16x128_f8f6f4 v[76:79], v[162:169], v[204:211], v[76:79]
	v_mfma_f32_16x16x128_f8f6f4 v[72:75], v[170:177], v[204:211], v[72:75]
	s_setprio 0
	s_barrier
	ds_read_b128 v[218:221], v147 offset:16384
	ds_read_b128 v[226:229], v147 offset:18432
	ds_read_b128 v[222:225], v148 offset:16384
	ds_read_b128 v[230:233], v148 offset:18432
	s_add_i32 m0, s0, 0xc000
	s_add_i32 s29, s0, 0xe000
	s_add_u32 s48, s50, 0x1000
	s_addc_u32 s49, s51, 0
	s_add_u32 s44, s50, 0x1080
	s_addc_u32 s45, s51, 0
	v_cndmask_b32_e64 v132, v135, v157, s[42:43]
	v_cndmask_b32_e64 v161, v136, v159, s[42:43]
	v_lshl_add_u64 v[252:253], s[52:53], 0, v[136:137]
	v_lshl_add_u64 v[252:253], v[252:253], 0, s[20:21]
	global_load_lds_dwordx4 v[252:253], off
	v_lshl_add_u64 v[252:253], s[52:53], 0, v[138:139]
	v_lshl_add_u64 v[252:253], v[252:253], 0, s[20:21]
	s_mov_b32 m0, s29
	s_nop 0
	global_load_lds_dwordx4 v[252:253], off
	s_barrier
	s_waitcnt lgkmcnt(0)
	s_setprio 1
	s_waitcnt lgkmcnt(0)
	v_mfma_f32_16x16x128_f8f6f4 v[116:119], v[218:225], v[178:185], v[116:119]
	v_mfma_f32_16x16x128_f8f6f4 v[112:115], v[226:233], v[178:185], v[112:115]
	v_mfma_f32_16x16x128_f8f6f4 v[100:103], v[218:225], v[186:193], v[100:103]
	v_mfma_f32_16x16x128_f8f6f4 v[96:99], v[226:233], v[186:193], v[96:99]
	v_mfma_f32_16x16x128_f8f6f4 v[84:87], v[218:225], v[196:203], v[84:87]
	v_mfma_f32_16x16x128_f8f6f4 v[80:83], v[226:233], v[196:203], v[80:83]
	v_mfma_f32_16x16x128_f8f6f4 v[68:71], v[218:225], v[204:211], v[68:71]
	v_mfma_f32_16x16x128_f8f6f4 v[64:67], v[226:233], v[204:211], v[64:67]
	s_setprio 0
	s_barrier
	s_mov_b32 m0, s0
	ds_read_b128 v[178:181], v145 offset:16384
	ds_read_b128 v[186:189], v145 offset:18432
	ds_read_b128 v[182:185], v146 offset:16384
	ds_read_b128 v[190:193], v146 offset:18432
	ds_read_b128 v[196:199], v145 offset:20480
	ds_read_b128 v[204:207], v145 offset:22528
	ds_read_b128 v[200:203], v146 offset:20480
	ds_read_b128 v[208:211], v146 offset:22528
	global_load_lds_dwordx4 v132, s[46:47]
	s_mov_b32 m0, s56
	v_mov_b32_e32 v141, v133
	global_load_lds_dwordx4 v140, s[46:47]
	s_waitcnt lgkmcnt(8)
	s_barrier
	s_waitcnt lgkmcnt(0)
	v_lshl_add_u64 v[212:213], s[46:47], 0, v[132:133]
	v_lshl_add_u64 v[214:215], s[46:47], 0, v[140:141]
	s_setprio 1
	s_waitcnt lgkmcnt(0)
	v_mfma_f32_16x16x128_f8f6f4 v[60:63], v[162:169], v[178:185], v[60:63]
	v_mfma_f32_16x16x128_f8f6f4 v[56:59], v[170:177], v[178:185], v[56:59]
	v_mfma_f32_16x16x128_f8f6f4 v[44:47], v[162:169], v[186:193], v[44:47]
	v_mfma_f32_16x16x128_f8f6f4 v[40:43], v[170:177], v[186:193], v[40:43]
	v_mfma_f32_16x16x128_f8f6f4 v[28:31], v[162:169], v[196:203], v[28:31]
	v_mfma_f32_16x16x128_f8f6f4 v[24:27], v[170:177], v[196:203], v[24:27]
	v_mfma_f32_16x16x128_f8f6f4 v[12:15], v[162:169], v[204:211], v[12:15]
	v_mfma_f32_16x16x128_f8f6f4 v[8:11], v[170:177], v[204:211], v[8:11]
	s_setprio 0
	s_barrier
	s_mov_b32 m0, s1
	v_lshl_add_u64 v[140:141], s[50:51], 0, v[128:129]
	global_load_lds_dwordx4 v[140:141], off
	v_lshl_add_u64 v[142:143], s[50:51], 0, v[130:131]
	s_mov_b32 m0, s37
	s_nop 0
	global_load_lds_dwordx4 v[142:143], off
	s_waitcnt vmcnt(8)
	s_waitcnt lgkmcnt(0)
	s_barrier
	s_setprio 1
	s_waitcnt lgkmcnt(0)
	v_mfma_f32_16x16x128_f8f6f4 v[52:55], v[218:225], v[178:185], v[52:55]
	v_mfma_f32_16x16x128_f8f6f4 v[48:51], v[226:233], v[178:185], v[48:51]
	v_mfma_f32_16x16x128_f8f6f4 v[36:39], v[218:225], v[186:193], v[36:39]
	v_mfma_f32_16x16x128_f8f6f4 v[32:35], v[226:233], v[186:193], v[32:35]
	v_mfma_f32_16x16x128_f8f6f4 v[20:23], v[218:225], v[196:203], v[20:23]
	v_mfma_f32_16x16x128_f8f6f4 v[16:19], v[226:233], v[196:203], v[16:19]
	v_mfma_f32_16x16x128_f8f6f4 v[4:7], v[218:225], v[204:211], v[4:7]
	v_mfma_f32_16x16x128_f8f6f4 v[0:3], v[226:233], v[204:211], v[0:3]
	s_setprio 0
	s_barrier
	ds_read_b128 v[162:165], v147 offset:32768
	ds_read_b128 v[170:173], v147 offset:34816
	ds_read_b128 v[166:169], v148 offset:32768
	ds_read_b128 v[174:177], v148 offset:34816
	s_mov_b32 m0, s65
	ds_read_b128 v[178:181], v145 offset:32768
	ds_read_b128 v[186:189], v145 offset:34816
	ds_read_b128 v[182:185], v146 offset:32768
	ds_read_b128 v[190:193], v146 offset:34816
	ds_read_b128 v[196:199], v145 offset:36864
	ds_read_b128 v[204:207], v145 offset:38912
	ds_read_b128 v[200:203], v146 offset:36864
	ds_read_b128 v[208:211], v146 offset:38912
	v_cndmask_b32_e64 v132, v138, v160, s[42:43]
	global_load_lds_dwordx4 v161, s[46:47]
	s_mov_b32 m0, s66
	s_nop 0
	global_load_lds_dwordx4 v132, s[46:47]
	s_waitcnt vmcnt(8)
	s_waitcnt lgkmcnt(8)
	s_barrier
	s_waitcnt lgkmcnt(0)
	s_setprio 1
	s_waitcnt lgkmcnt(0)
	v_mfma_f32_16x16x128_f8f6f4 v[124:127], v[162:169], v[178:185], v[124:127]
	v_mfma_f32_16x16x128_f8f6f4 v[120:123], v[170:177], v[178:185], v[120:123]
	v_mfma_f32_16x16x128_f8f6f4 v[108:111], v[162:169], v[186:193], v[108:111]
	v_mfma_f32_16x16x128_f8f6f4 v[104:107], v[170:177], v[186:193], v[104:107]
	v_mfma_f32_16x16x128_f8f6f4 v[92:95], v[162:169], v[196:203], v[92:95]
	v_mfma_f32_16x16x128_f8f6f4 v[88:91], v[170:177], v[196:203], v[88:91]
	v_mfma_f32_16x16x128_f8f6f4 v[76:79], v[162:169], v[204:211], v[76:79]
	v_mfma_f32_16x16x128_f8f6f4 v[72:75], v[170:177], v[204:211], v[72:75]
	s_setprio 0
	s_barrier
	ds_read_b128 v[218:221], v147 offset:49152
	ds_read_b128 v[226:229], v147 offset:51200
	ds_read_b128 v[222:225], v148 offset:49152
	ds_read_b128 v[230:233], v148 offset:51200
	v_lshl_add_u64 v[216:217], s[48:49], 0, v[128:129]
	s_mov_b32 m0, s57
	s_nop 0
	global_load_lds_dwordx4 v[216:217], off
	v_lshl_add_u64 v[216:217], s[48:49], 0, v[130:131]
	s_mov_b32 m0, s64
	s_nop 0
	global_load_lds_dwordx4 v[216:217], off
	s_waitcnt vmcnt(8)
	s_barrier
	s_waitcnt lgkmcnt(0)
	s_setprio 1
	s_waitcnt lgkmcnt(0)
	v_mfma_f32_16x16x128_f8f6f4 v[116:119], v[218:225], v[178:185], v[116:119]
	v_mfma_f32_16x16x128_f8f6f4 v[112:115], v[226:233], v[178:185], v[112:115]
	v_mfma_f32_16x16x128_f8f6f4 v[100:103], v[218:225], v[186:193], v[100:103]
	v_mfma_f32_16x16x128_f8f6f4 v[96:99], v[226:233], v[186:193], v[96:99]
	v_mfma_f32_16x16x128_f8f6f4 v[84:87], v[218:225], v[196:203], v[84:87]
	v_mfma_f32_16x16x128_f8f6f4 v[80:83], v[226:233], v[196:203], v[80:83]
	v_mfma_f32_16x16x128_f8f6f4 v[68:71], v[218:225], v[204:211], v[68:71]
	v_mfma_f32_16x16x128_f8f6f4 v[64:67], v[226:233], v[204:211], v[64:67]
	s_setprio 0
	s_barrier
	s_mov_b32 m0, s69
	v_lshl_add_u64 v[212:213], v[212:213], 0, s[20:21]
	ds_read_b128 v[178:181], v145 offset:49152
	ds_read_b128 v[186:189], v145 offset:51200
	ds_read_b128 v[182:185], v146 offset:49152
	ds_read_b128 v[190:193], v146 offset:51200
	ds_read_b128 v[196:199], v145 offset:53248
	ds_read_b128 v[204:207], v145 offset:55296
	ds_read_b128 v[200:203], v146 offset:53248
	ds_read_b128 v[208:211], v146 offset:55296
	global_load_lds_dwordx4 v[212:213], off
	v_lshl_add_u64 v[212:213], v[214:215], 0, s[20:21]
	s_mov_b32 m0, s70
	s_nop 0
	global_load_lds_dwordx4 v[212:213], off
	s_waitcnt lgkmcnt(8)
	s_barrier
	s_waitcnt lgkmcnt(0)
	s_setprio 1
	s_waitcnt lgkmcnt(0)
	v_mfma_f32_16x16x128_f8f6f4 v[60:63], v[162:169], v[178:185], v[60:63]
	v_mfma_f32_16x16x128_f8f6f4 v[56:59], v[170:177], v[178:185], v[56:59]
	v_mfma_f32_16x16x128_f8f6f4 v[44:47], v[162:169], v[186:193], v[44:47]
	v_mfma_f32_16x16x128_f8f6f4 v[40:43], v[170:177], v[186:193], v[40:43]
	v_mfma_f32_16x16x128_f8f6f4 v[28:31], v[162:169], v[196:203], v[28:31]
	v_mfma_f32_16x16x128_f8f6f4 v[24:27], v[170:177], v[196:203], v[24:27]
	v_mfma_f32_16x16x128_f8f6f4 v[12:15], v[162:169], v[204:211], v[12:15]
	v_mfma_f32_16x16x128_f8f6f4 v[8:11], v[170:177], v[204:211], v[8:11]
	s_setprio 0
	s_barrier
	s_mov_b32 m0, s67
	v_lshl_add_u64 v[140:141], v[140:141], 0, s[20:21]
	global_load_lds_dwordx4 v[140:141], off
	v_lshl_add_u64 v[140:141], v[142:143], 0, s[20:21]
	s_mov_b32 m0, s68
	s_nop 0
	global_load_lds_dwordx4 v[140:141], off
	s_waitcnt vmcnt(8)
	s_waitcnt lgkmcnt(0)
	s_barrier
	s_setprio 1
	s_waitcnt lgkmcnt(0)
	v_mfma_f32_16x16x128_f8f6f4 v[52:55], v[218:225], v[178:185], v[52:55]
	v_mfma_f32_16x16x128_f8f6f4 v[48:51], v[226:233], v[178:185], v[48:51]
	v_mfma_f32_16x16x128_f8f6f4 v[36:39], v[218:225], v[186:193], v[36:39]
	v_mfma_f32_16x16x128_f8f6f4 v[32:35], v[226:233], v[186:193], v[32:35]
	v_mfma_f32_16x16x128_f8f6f4 v[20:23], v[218:225], v[196:203], v[20:23]
	v_mfma_f32_16x16x128_f8f6f4 v[16:19], v[226:233], v[196:203], v[16:19]
	v_mfma_f32_16x16x128_f8f6f4 v[4:7], v[218:225], v[204:211], v[4:7]
	v_mfma_f32_16x16x128_f8f6f4 v[0:3], v[226:233], v[204:211], v[0:3]
	s_setprio 0
	s_barrier
	s_mov_b32 m0, s71
	v_lshl_add_u64 v[140:141], s[44:45], 0, v[128:129]
	global_load_lds_dwordx4 v[140:141], off
	v_lshl_add_u64 v[140:141], s[44:45], 0, v[130:131]
	s_mov_b32 m0, s72
	s_andn2_b64 vcc, exec, s[40:41]
	global_load_lds_dwordx4 v[140:141], off
	s_mov_b64 s[42:43], -1
	s_mov_b64 s[40:41], 0
	s_mov_b64 s[44:45], 0x100
	s_cbranch_vccz .LBB0_1961

.LBB0_1988:
	v_mov_b32_e32 v137, v133
	v_mov_b32_e32 v139, v133
	s_mov_b64 s[34:35], 0
	s_mov_b64 s[28:29], -1
	s_mov_b64 s[30:31], 0
	s_add_u32 s42, s10, s34
	s_addc_u32 s43, s11, s35
	s_add_u32 s38, s42, 0x100
	s_addc_u32 s39, s43, 0
	s_and_b64 s[36:37], s[30:31], exec
	s_cselect_b32 s36, s10, s38
	s_cselect_b32 s37, s11, s39
	s_add_u32 s34, s26, s34
	s_addc_u32 s35, s27, s35
	s_add_u32 s38, s34, 0x100
	s_addc_u32 s39, s35, 0
	ds_read_b128 v[160:163], v147
	ds_read_b128 v[168:171], v147 offset:2048
	ds_read_b128 v[164:167], v148
	ds_read_b128 v[172:175], v148 offset:2048
	s_and_b64 s[34:35], s[30:31], exec
	s_cselect_b32 s41, s25, s39
	s_cselect_b32 s40, s24, s38
	ds_read_b128 v[176:179], v145
	ds_read_b128 v[184:187], v145 offset:2048
	ds_read_b128 v[180:183], v146
	ds_read_b128 v[188:191], v146 offset:2048
	ds_read_b128 v[196:199], v145 offset:4096
	ds_read_b128 v[204:207], v145 offset:6144
	ds_read_b128 v[200:203], v146 offset:4096
	ds_read_b128 v[208:211], v146 offset:6144
	s_waitcnt vmcnt(6)
	s_waitcnt lgkmcnt(8)
	s_barrier
	s_waitcnt lgkmcnt(0)
	v_cndmask_b32_e64 v140, v134, v156, s[30:31]
	s_setprio 1
	s_waitcnt lgkmcnt(0)
	v_mfma_f32_16x16x128_f8f6f4 v[124:127], v[160:167], v[176:183], 0
	v_mfma_f32_16x16x128_f8f6f4 v[120:123], v[168:175], v[176:183], 0
	v_mfma_f32_16x16x128_f8f6f4 v[108:111], v[160:167], v[184:191], 0
	v_mfma_f32_16x16x128_f8f6f4 v[104:107], v[168:175], v[184:191], 0
	v_mfma_f32_16x16x128_f8f6f4 v[92:95], v[160:167], v[196:203], 0
	v_mfma_f32_16x16x128_f8f6f4 v[88:91], v[168:175], v[196:203], 0
	v_mfma_f32_16x16x128_f8f6f4 v[76:79], v[160:167], v[204:211], 0
	v_mfma_f32_16x16x128_f8f6f4 v[72:75], v[168:175], v[204:211], 0
	s_setprio 0
	s_barrier
	ds_read_b128 v[218:221], v147 offset:16384
	ds_read_b128 v[226:229], v147 offset:18432
	ds_read_b128 v[222:225], v148 offset:16384
	ds_read_b128 v[230:233], v148 offset:18432
	s_add_i32 m0, s0, 0xc000
	s_add_i32 s62, s0, 0xe000
	s_add_u32 s38, s40, 0x1000
	s_addc_u32 s39, s41, 0
	s_add_u32 s34, s40, 0x1080
	s_addc_u32 s35, s41, 0
	v_cndmask_b32_e64 v132, v135, v155, s[30:31]
	v_cndmask_b32_e64 v159, v136, v157, s[30:31]
	v_lshl_add_u64 v[252:253], s[42:43], 0, v[136:137]
	v_lshl_add_u64 v[252:253], v[252:253], 0, s[16:17]
	global_load_lds_dwordx4 v[252:253], off
	v_lshl_add_u64 v[252:253], s[42:43], 0, v[138:139]
	v_lshl_add_u64 v[252:253], v[252:253], 0, s[16:17]
	s_mov_b32 m0, s62
	s_nop 0
	global_load_lds_dwordx4 v[252:253], off
	s_barrier
	s_waitcnt lgkmcnt(0)
	s_setprio 1
	s_waitcnt lgkmcnt(0)
	v_mfma_f32_16x16x128_f8f6f4 v[116:119], v[218:225], v[176:183], 0
	v_mfma_f32_16x16x128_f8f6f4 v[112:115], v[226:233], v[176:183], 0
	v_mfma_f32_16x16x128_f8f6f4 v[100:103], v[218:225], v[184:191], 0
	v_mfma_f32_16x16x128_f8f6f4 v[96:99], v[226:233], v[184:191], 0
	v_mfma_f32_16x16x128_f8f6f4 v[84:87], v[218:225], v[196:203], 0
	v_mfma_f32_16x16x128_f8f6f4 v[80:83], v[226:233], v[196:203], 0
	v_mfma_f32_16x16x128_f8f6f4 v[68:71], v[218:225], v[204:211], 0
	v_mfma_f32_16x16x128_f8f6f4 v[64:67], v[226:233], v[204:211], 0
	s_setprio 0
	s_barrier
	s_mov_b32 m0, s0
	ds_read_b128 v[176:179], v145 offset:16384
	ds_read_b128 v[184:187], v145 offset:18432
	ds_read_b128 v[180:183], v146 offset:16384
	ds_read_b128 v[188:191], v146 offset:18432
	ds_read_b128 v[196:199], v145 offset:20480
	ds_read_b128 v[204:207], v145 offset:22528
	ds_read_b128 v[200:203], v146 offset:20480
	ds_read_b128 v[208:211], v146 offset:22528
	global_load_lds_dwordx4 v132, s[36:37]
	s_mov_b32 m0, s47
	v_mov_b32_e32 v141, v133
	global_load_lds_dwordx4 v140, s[36:37]
	s_waitcnt lgkmcnt(8)
	s_barrier
	s_waitcnt lgkmcnt(0)
	v_lshl_add_u64 v[192:193], s[36:37], 0, v[132:133]
	v_lshl_add_u64 v[212:213], s[36:37], 0, v[140:141]
	s_setprio 1
	s_waitcnt lgkmcnt(0)
	v_mfma_f32_16x16x128_f8f6f4 v[60:63], v[160:167], v[176:183], 0
	v_mfma_f32_16x16x128_f8f6f4 v[56:59], v[168:175], v[176:183], 0
	v_mfma_f32_16x16x128_f8f6f4 v[44:47], v[160:167], v[184:191], 0
	v_mfma_f32_16x16x128_f8f6f4 v[40:43], v[168:175], v[184:191], 0
	v_mfma_f32_16x16x128_f8f6f4 v[28:31], v[160:167], v[196:203], 0
	v_mfma_f32_16x16x128_f8f6f4 v[24:27], v[168:175], v[196:203], 0
	v_mfma_f32_16x16x128_f8f6f4 v[12:15], v[160:167], v[204:211], 0
	v_mfma_f32_16x16x128_f8f6f4 v[8:11], v[168:175], v[204:211], 0
	s_setprio 0
	s_barrier
	s_mov_b32 m0, s1
	v_lshl_add_u64 v[140:141], s[40:41], 0, v[128:129]
	global_load_lds_dwordx4 v[140:141], off
	v_lshl_add_u64 v[142:143], s[40:41], 0, v[130:131]
	s_mov_b32 m0, s46
	s_nop 0
	global_load_lds_dwordx4 v[142:143], off
	s_waitcnt vmcnt(8)
	s_waitcnt lgkmcnt(0)
	s_barrier
	s_setprio 1
	s_waitcnt lgkmcnt(0)
	v_mfma_f32_16x16x128_f8f6f4 v[52:55], v[218:225], v[176:183], 0
	v_mfma_f32_16x16x128_f8f6f4 v[48:51], v[226:233], v[176:183], 0
	v_mfma_f32_16x16x128_f8f6f4 v[36:39], v[218:225], v[184:191], 0
	v_mfma_f32_16x16x128_f8f6f4 v[32:35], v[226:233], v[184:191], 0
	v_mfma_f32_16x16x128_f8f6f4 v[20:23], v[218:225], v[196:203], 0
	v_mfma_f32_16x16x128_f8f6f4 v[16:19], v[226:233], v[196:203], 0
	v_mfma_f32_16x16x128_f8f6f4 v[4:7], v[218:225], v[204:211], 0
	v_mfma_f32_16x16x128_f8f6f4 v[0:3], v[226:233], v[204:211], 0
	s_setprio 0
	s_barrier
	ds_read_b128 v[160:163], v147 offset:32768
	ds_read_b128 v[168:171], v147 offset:34816
	ds_read_b128 v[164:167], v148 offset:32768
	ds_read_b128 v[172:175], v148 offset:34816
	s_mov_b32 m0, s50
	ds_read_b128 v[176:179], v145 offset:32768
	ds_read_b128 v[184:187], v145 offset:34816
	ds_read_b128 v[180:183], v146 offset:32768
	ds_read_b128 v[188:191], v146 offset:34816
	ds_read_b128 v[196:199], v145 offset:36864
	ds_read_b128 v[204:207], v145 offset:38912
	ds_read_b128 v[200:203], v146 offset:36864
	ds_read_b128 v[208:211], v146 offset:38912
	v_cndmask_b32_e64 v132, v138, v158, s[30:31]
	global_load_lds_dwordx4 v159, s[36:37]
	s_mov_b32 m0, s51
	s_nop 0
	global_load_lds_dwordx4 v132, s[36:37]
	s_waitcnt vmcnt(8)
	s_waitcnt lgkmcnt(8)
	s_barrier
	s_waitcnt lgkmcnt(0)
	s_setprio 1
	s_waitcnt lgkmcnt(0)
	v_mfma_f32_16x16x128_f8f6f4 v[124:127], v[160:167], v[176:183], v[124:127]
	v_mfma_f32_16x16x128_f8f6f4 v[120:123], v[168:175], v[176:183], v[120:123]
	v_mfma_f32_16x16x128_f8f6f4 v[108:111], v[160:167], v[184:191], v[108:111]
	v_mfma_f32_16x16x128_f8f6f4 v[104:107], v[168:175], v[184:191], v[104:107]
	v_mfma_f32_16x16x128_f8f6f4 v[92:95], v[160:167], v[196:203], v[92:95]
	v_mfma_f32_16x16x128_f8f6f4 v[88:91], v[168:175], v[196:203], v[88:91]
	v_mfma_f32_16x16x128_f8f6f4 v[76:79], v[160:167], v[204:211], v[76:79]
	v_mfma_f32_16x16x128_f8f6f4 v[72:75], v[168:175], v[204:211], v[72:75]
	s_setprio 0
	s_barrier
	ds_read_b128 v[218:221], v147 offset:49152
	ds_read_b128 v[226:229], v147 offset:51200
	ds_read_b128 v[222:225], v148 offset:49152
	ds_read_b128 v[230:233], v148 offset:51200
	v_lshl_add_u64 v[214:215], s[38:39], 0, v[128:129]
	s_mov_b32 m0, s48
	s_nop 0
	global_load_lds_dwordx4 v[214:215], off
	v_lshl_add_u64 v[214:215], s[38:39], 0, v[130:131]
	s_mov_b32 m0, s49
	s_nop 0
	global_load_lds_dwordx4 v[214:215], off
	s_waitcnt vmcnt(8)
	s_barrier
	s_waitcnt lgkmcnt(0)
	s_setprio 1
	s_waitcnt lgkmcnt(0)
	v_mfma_f32_16x16x128_f8f6f4 v[116:119], v[218:225], v[176:183], v[116:119]
	v_mfma_f32_16x16x128_f8f6f4 v[112:115], v[226:233], v[176:183], v[112:115]
	v_mfma_f32_16x16x128_f8f6f4 v[100:103], v[218:225], v[184:191], v[100:103]
	v_mfma_f32_16x16x128_f8f6f4 v[96:99], v[226:233], v[184:191], v[96:99]
	v_mfma_f32_16x16x128_f8f6f4 v[84:87], v[218:225], v[196:203], v[84:87]
	v_mfma_f32_16x16x128_f8f6f4 v[80:83], v[226:233], v[196:203], v[80:83]
	v_mfma_f32_16x16x128_f8f6f4 v[68:71], v[218:225], v[204:211], v[68:71]
	v_mfma_f32_16x16x128_f8f6f4 v[64:67], v[226:233], v[204:211], v[64:67]
	s_setprio 0
	s_barrier
	s_mov_b32 m0, s55
	v_lshl_add_u64 v[192:193], v[192:193], 0, s[16:17]
	ds_read_b128 v[176:179], v145 offset:49152
	ds_read_b128 v[184:187], v145 offset:51200
	ds_read_b128 v[180:183], v146 offset:49152
	ds_read_b128 v[188:191], v146 offset:51200
	ds_read_b128 v[196:199], v145 offset:53248
	ds_read_b128 v[204:207], v145 offset:55296
	ds_read_b128 v[200:203], v146 offset:53248
	ds_read_b128 v[208:211], v146 offset:55296
	global_load_lds_dwordx4 v[192:193], off
	v_lshl_add_u64 v[192:193], v[212:213], 0, s[16:17]
	s_mov_b32 m0, s56
	s_nop 0
	global_load_lds_dwordx4 v[192:193], off
	s_waitcnt lgkmcnt(8)
	s_barrier
	s_waitcnt lgkmcnt(0)
	s_setprio 1
	s_waitcnt lgkmcnt(0)
	v_mfma_f32_16x16x128_f8f6f4 v[60:63], v[160:167], v[176:183], v[60:63]
	v_mfma_f32_16x16x128_f8f6f4 v[56:59], v[168:175], v[176:183], v[56:59]
	v_mfma_f32_16x16x128_f8f6f4 v[44:47], v[160:167], v[184:191], v[44:47]
	v_mfma_f32_16x16x128_f8f6f4 v[40:43], v[168:175], v[184:191], v[40:43]
	v_mfma_f32_16x16x128_f8f6f4 v[28:31], v[160:167], v[196:203], v[28:31]
	v_mfma_f32_16x16x128_f8f6f4 v[24:27], v[168:175], v[196:203], v[24:27]
	v_mfma_f32_16x16x128_f8f6f4 v[12:15], v[160:167], v[204:211], v[12:15]
	v_mfma_f32_16x16x128_f8f6f4 v[8:11], v[168:175], v[204:211], v[8:11]
	s_setprio 0
	s_barrier
	s_mov_b32 m0, s53
	v_lshl_add_u64 v[140:141], v[140:141], 0, s[16:17]
	global_load_lds_dwordx4 v[140:141], off
	v_lshl_add_u64 v[140:141], v[142:143], 0, s[16:17]
	s_mov_b32 m0, s54
	s_nop 0
	global_load_lds_dwordx4 v[140:141], off
	s_waitcnt vmcnt(8)
	s_waitcnt lgkmcnt(0)
	s_barrier
	s_setprio 1
	s_waitcnt lgkmcnt(0)
	v_mfma_f32_16x16x128_f8f6f4 v[52:55], v[218:225], v[176:183], v[52:55]
	v_mfma_f32_16x16x128_f8f6f4 v[48:51], v[226:233], v[176:183], v[48:51]
	v_mfma_f32_16x16x128_f8f6f4 v[36:39], v[218:225], v[184:191], v[36:39]
	v_mfma_f32_16x16x128_f8f6f4 v[32:35], v[226:233], v[184:191], v[32:35]
	v_mfma_f32_16x16x128_f8f6f4 v[20:23], v[218:225], v[196:203], v[20:23]
	v_mfma_f32_16x16x128_f8f6f4 v[16:19], v[226:233], v[196:203], v[16:19]
	v_mfma_f32_16x16x128_f8f6f4 v[4:7], v[218:225], v[204:211], v[4:7]
	v_mfma_f32_16x16x128_f8f6f4 v[0:3], v[226:233], v[204:211], v[0:3]
	s_setprio 0
	s_barrier
	s_mov_b32 m0, s57
	v_lshl_add_u64 v[140:141], s[34:35], 0, v[128:129]
	global_load_lds_dwordx4 v[140:141], off
	v_lshl_add_u64 v[140:141], s[34:35], 0, v[130:131]
	s_mov_b32 m0, s58
	s_andn2_b64 vcc, exec, s[28:29]
	global_load_lds_dwordx4 v[140:141], off
	s_mov_b64 s[30:31], -1
	s_mov_b64 s[28:29], 0
	s_mov_b64 s[34:35], 0x100
	s_cbranch_vccz .LBB0_1989
	s_branch .Lpeel_after_1989
.LBB0_1989:
	s_add_u32 s42, s10, s34
	s_addc_u32 s43, s11, s35
	s_add_u32 s38, s42, 0x100
	s_addc_u32 s39, s43, 0
	s_and_b64 s[36:37], s[30:31], exec
	s_cselect_b32 s36, s10, s38
	s_cselect_b32 s37, s11, s39
	s_add_u32 s34, s26, s34
	s_addc_u32 s35, s27, s35
	s_add_u32 s38, s34, 0x100
	s_addc_u32 s39, s35, 0
	ds_read_b128 v[160:163], v147
	ds_read_b128 v[168:171], v147 offset:2048
	ds_read_b128 v[164:167], v148
	ds_read_b128 v[172:175], v148 offset:2048
	s_and_b64 s[34:35], s[30:31], exec
	s_cselect_b32 s41, s25, s39
	s_cselect_b32 s40, s24, s38
	ds_read_b128 v[176:179], v145
	ds_read_b128 v[184:187], v145 offset:2048
	ds_read_b128 v[180:183], v146
	ds_read_b128 v[188:191], v146 offset:2048
	ds_read_b128 v[196:199], v145 offset:4096
	ds_read_b128 v[204:207], v145 offset:6144
	ds_read_b128 v[200:203], v146 offset:4096
	ds_read_b128 v[208:211], v146 offset:6144
	s_waitcnt vmcnt(6)
	s_waitcnt lgkmcnt(8)
	s_barrier
	s_waitcnt lgkmcnt(0)
	v_cndmask_b32_e64 v140, v134, v156, s[30:31]
	s_setprio 1
	s_waitcnt lgkmcnt(0)
	v_mfma_f32_16x16x128_f8f6f4 v[124:127], v[160:167], v[176:183], v[124:127]
	v_mfma_f32_16x16x128_f8f6f4 v[120:123], v[168:175], v[176:183], v[120:123]
	v_mfma_f32_16x16x128_f8f6f4 v[108:111], v[160:167], v[184:191], v[108:111]
	v_mfma_f32_16x16x128_f8f6f4 v[104:107], v[168:175], v[184:191], v[104:107]
	v_mfma_f32_16x16x128_f8f6f4 v[92:95], v[160:167], v[196:203], v[92:95]
	v_mfma_f32_16x16x128_f8f6f4 v[88:91], v[168:175], v[196:203], v[88:91]
	v_mfma_f32_16x16x128_f8f6f4 v[76:79], v[160:167], v[204:211], v[76:79]
	v_mfma_f32_16x16x128_f8f6f4 v[72:75], v[168:175], v[204:211], v[72:75]
	s_setprio 0
	s_barrier
	ds_read_b128 v[218:221], v147 offset:16384
	ds_read_b128 v[226:229], v147 offset:18432
	ds_read_b128 v[222:225], v148 offset:16384
	ds_read_b128 v[230:233], v148 offset:18432
	s_add_i32 m0, s0, 0xc000
	s_add_i32 s62, s0, 0xe000
	s_add_u32 s38, s40, 0x1000
	s_addc_u32 s39, s41, 0
	s_add_u32 s34, s40, 0x1080
	s_addc_u32 s35, s41, 0
	v_cndmask_b32_e64 v132, v135, v155, s[30:31]
	v_cndmask_b32_e64 v159, v136, v157, s[30:31]
	v_lshl_add_u64 v[252:253], s[42:43], 0, v[136:137]
	v_lshl_add_u64 v[252:253], v[252:253], 0, s[16:17]
	global_load_lds_dwordx4 v[252:253], off
	v_lshl_add_u64 v[252:253], s[42:43], 0, v[138:139]
	v_lshl_add_u64 v[252:253], v[252:253], 0, s[16:17]
	s_mov_b32 m0, s62
	s_nop 0
	global_load_lds_dwordx4 v[252:253], off
	s_barrier
	s_waitcnt lgkmcnt(0)
	s_setprio 1
	s_waitcnt lgkmcnt(0)
	v_mfma_f32_16x16x128_f8f6f4 v[116:119], v[218:225], v[176:183], v[116:119]
	v_mfma_f32_16x16x128_f8f6f4 v[112:115], v[226:233], v[176:183], v[112:115]
	v_mfma_f32_16x16x128_f8f6f4 v[100:103], v[218:225], v[184:191], v[100:103]
	v_mfma_f32_16x16x128_f8f6f4 v[96:99], v[226:233], v[184:191], v[96:99]
	v_mfma_f32_16x16x128_f8f6f4 v[84:87], v[218:225], v[196:203], v[84:87]
	v_mfma_f32_16x16x128_f8f6f4 v[80:83], v[226:233], v[196:203], v[80:83]
	v_mfma_f32_16x16x128_f8f6f4 v[68:71], v[218:225], v[204:211], v[68:71]
	v_mfma_f32_16x16x128_f8f6f4 v[64:67], v[226:233], v[204:211], v[64:67]
	s_setprio 0
	s_barrier
	s_mov_b32 m0, s0
	ds_read_b128 v[176:179], v145 offset:16384
	ds_read_b128 v[184:187], v145 offset:18432
	ds_read_b128 v[180:183], v146 offset:16384
	ds_read_b128 v[188:191], v146 offset:18432
	ds_read_b128 v[196:199], v145 offset:20480
	ds_read_b128 v[204:207], v145 offset:22528
	ds_read_b128 v[200:203], v146 offset:20480
	ds_read_b128 v[208:211], v146 offset:22528
	global_load_lds_dwordx4 v132, s[36:37]
	s_mov_b32 m0, s47
	v_mov_b32_e32 v141, v133
	global_load_lds_dwordx4 v140, s[36:37]
	s_waitcnt lgkmcnt(8)
	s_barrier
	s_waitcnt lgkmcnt(0)
	v_lshl_add_u64 v[192:193], s[36:37], 0, v[132:133]
	v_lshl_add_u64 v[212:213], s[36:37], 0, v[140:141]
	s_setprio 1
	s_waitcnt lgkmcnt(0)
	v_mfma_f32_16x16x128_f8f6f4 v[60:63], v[160:167], v[176:183], v[60:63]
	v_mfma_f32_16x16x128_f8f6f4 v[56:59], v[168:175], v[176:183], v[56:59]
	v_mfma_f32_16x16x128_f8f6f4 v[44:47], v[160:167], v[184:191], v[44:47]
	v_mfma_f32_16x16x128_f8f6f4 v[40:43], v[168:175], v[184:191], v[40:43]
	v_mfma_f32_16x16x128_f8f6f4 v[28:31], v[160:167], v[196:203], v[28:31]
	v_mfma_f32_16x16x128_f8f6f4 v[24:27], v[168:175], v[196:203], v[24:27]
	v_mfma_f32_16x16x128_f8f6f4 v[12:15], v[160:167], v[204:211], v[12:15]
	v_mfma_f32_16x16x128_f8f6f4 v[8:11], v[168:175], v[204:211], v[8:11]
	s_setprio 0
	s_barrier
	s_mov_b32 m0, s1
	v_lshl_add_u64 v[140:141], s[40:41], 0, v[128:129]
	global_load_lds_dwordx4 v[140:141], off
	v_lshl_add_u64 v[142:143], s[40:41], 0, v[130:131]
	s_mov_b32 m0, s46
	s_nop 0
	global_load_lds_dwordx4 v[142:143], off
	s_waitcnt vmcnt(8)
	s_waitcnt lgkmcnt(0)
	s_barrier
	s_setprio 1
	s_waitcnt lgkmcnt(0)
	v_mfma_f32_16x16x128_f8f6f4 v[52:55], v[218:225], v[176:183], v[52:55]
	v_mfma_f32_16x16x128_f8f6f4 v[48:51], v[226:233], v[176:183], v[48:51]
	v_mfma_f32_16x16x128_f8f6f4 v[36:39], v[218:225], v[184:191], v[36:39]
	v_mfma_f32_16x16x128_f8f6f4 v[32:35], v[226:233], v[184:191], v[32:35]
	v_mfma_f32_16x16x128_f8f6f4 v[20:23], v[218:225], v[196:203], v[20:23]
	v_mfma_f32_16x16x128_f8f6f4 v[16:19], v[226:233], v[196:203], v[16:19]
	v_mfma_f32_16x16x128_f8f6f4 v[4:7], v[218:225], v[204:211], v[4:7]
	v_mfma_f32_16x16x128_f8f6f4 v[0:3], v[226:233], v[204:211], v[0:3]
	s_setprio 0
	s_barrier
	ds_read_b128 v[160:163], v147 offset:32768
	ds_read_b128 v[168:171], v147 offset:34816
	ds_read_b128 v[164:167], v148 offset:32768
	ds_read_b128 v[172:175], v148 offset:34816
	s_mov_b32 m0, s50
	ds_read_b128 v[176:179], v145 offset:32768
	ds_read_b128 v[184:187], v145 offset:34816
	ds_read_b128 v[180:183], v146 offset:32768
	ds_read_b128 v[188:191], v146 offset:34816
	ds_read_b128 v[196:199], v145 offset:36864
	ds_read_b128 v[204:207], v145 offset:38912
	ds_read_b128 v[200:203], v146 offset:36864
	ds_read_b128 v[208:211], v146 offset:38912
	v_cndmask_b32_e64 v132, v138, v158, s[30:31]
	global_load_lds_dwordx4 v159, s[36:37]
	s_mov_b32 m0, s51
	s_nop 0
	global_load_lds_dwordx4 v132, s[36:37]
	s_waitcnt vmcnt(8)
	s_waitcnt lgkmcnt(8)
	s_barrier
	s_waitcnt lgkmcnt(0)
	s_setprio 1
	s_waitcnt lgkmcnt(0)
	v_mfma_f32_16x16x128_f8f6f4 v[124:127], v[160:167], v[176:183], v[124:127]
	v_mfma_f32_16x16x128_f8f6f4 v[120:123], v[168:175], v[176:183], v[120:123]
	v_mfma_f32_16x16x128_f8f6f4 v[108:111], v[160:167], v[184:191], v[108:111]
	v_mfma_f32_16x16x128_f8f6f4 v[104:107], v[168:175], v[184:191], v[104:107]
	v_mfma_f32_16x16x128_f8f6f4 v[92:95], v[160:167], v[196:203], v[92:95]
	v_mfma_f32_16x16x128_f8f6f4 v[88:91], v[168:175], v[196:203], v[88:91]
	v_mfma_f32_16x16x128_f8f6f4 v[76:79], v[160:167], v[204:211], v[76:79]
	v_mfma_f32_16x16x128_f8f6f4 v[72:75], v[168:175], v[204:211], v[72:75]
	s_setprio 0
	s_barrier
	ds_read_b128 v[218:221], v147 offset:49152
	ds_read_b128 v[226:229], v147 offset:51200
	ds_read_b128 v[222:225], v148 offset:49152
	ds_read_b128 v[230:233], v148 offset:51200
	v_lshl_add_u64 v[214:215], s[38:39], 0, v[128:129]
	s_mov_b32 m0, s48
	s_nop 0
	global_load_lds_dwordx4 v[214:215], off
	v_lshl_add_u64 v[214:215], s[38:39], 0, v[130:131]
	s_mov_b32 m0, s49
	s_nop 0
	global_load_lds_dwordx4 v[214:215], off
	s_waitcnt vmcnt(8)
	s_barrier
	s_waitcnt lgkmcnt(0)
	s_setprio 1
	s_waitcnt lgkmcnt(0)
	v_mfma_f32_16x16x128_f8f6f4 v[116:119], v[218:225], v[176:183], v[116:119]
	v_mfma_f32_16x16x128_f8f6f4 v[112:115], v[226:233], v[176:183], v[112:115]
	v_mfma_f32_16x16x128_f8f6f4 v[100:103], v[218:225], v[184:191], v[100:103]
	v_mfma_f32_16x16x128_f8f6f4 v[96:99], v[226:233], v[184:191], v[96:99]
	v_mfma_f32_16x16x128_f8f6f4 v[84:87], v[218:225], v[196:203], v[84:87]
	v_mfma_f32_16x16x128_f8f6f4 v[80:83], v[226:233], v[196:203], v[80:83]
	v_mfma_f32_16x16x128_f8f6f4 v[68:71], v[218:225], v[204:211], v[68:71]
	v_mfma_f32_16x16x128_f8f6f4 v[64:67], v[226:233], v[204:211], v[64:67]
	s_setprio 0
	s_barrier
	s_mov_b32 m0, s55
	v_lshl_add_u64 v[192:193], v[192:193], 0, s[16:17]
	ds_read_b128 v[176:179], v145 offset:49152
	ds_read_b128 v[184:187], v145 offset:51200
	ds_read_b128 v[180:183], v146 offset:49152
	ds_read_b128 v[188:191], v146 offset:51200
	ds_read_b128 v[196:199], v145 offset:53248
	ds_read_b128 v[204:207], v145 offset:55296
	ds_read_b128 v[200:203], v146 offset:53248
	ds_read_b128 v[208:211], v146 offset:55296
	global_load_lds_dwordx4 v[192:193], off
	v_lshl_add_u64 v[192:193], v[212:213], 0, s[16:17]
	s_mov_b32 m0, s56
	s_nop 0
	global_load_lds_dwordx4 v[192:193], off
	s_waitcnt lgkmcnt(8)
	s_barrier
	s_waitcnt lgkmcnt(0)
	s_setprio 1
	s_waitcnt lgkmcnt(0)
	v_mfma_f32_16x16x128_f8f6f4 v[60:63], v[160:167], v[176:183], v[60:63]
	v_mfma_f32_16x16x128_f8f6f4 v[56:59], v[168:175], v[176:183], v[56:59]
	v_mfma_f32_16x16x128_f8f6f4 v[44:47], v[160:167], v[184:191], v[44:47]
	v_mfma_f32_16x16x128_f8f6f4 v[40:43], v[168:175], v[184:191], v[40:43]
	v_mfma_f32_16x16x128_f8f6f4 v[28:31], v[160:167], v[196:203], v[28:31]
	v_mfma_f32_16x16x128_f8f6f4 v[24:27], v[168:175], v[196:203], v[24:27]
	v_mfma_f32_16x16x128_f8f6f4 v[12:15], v[160:167], v[204:211], v[12:15]
	v_mfma_f32_16x16x128_f8f6f4 v[8:11], v[168:175], v[204:211], v[8:11]
	s_setprio 0
	s_barrier
	s_mov_b32 m0, s53
	v_lshl_add_u64 v[140:141], v[140:141], 0, s[16:17]
	global_load_lds_dwordx4 v[140:141], off
	v_lshl_add_u64 v[140:141], v[142:143], 0, s[16:17]
	s_mov_b32 m0, s54
	s_nop 0
	global_load_lds_dwordx4 v[140:141], off
	s_waitcnt vmcnt(8)
	s_waitcnt lgkmcnt(0)
	s_barrier
	s_setprio 1
	s_waitcnt lgkmcnt(0)
	v_mfma_f32_16x16x128_f8f6f4 v[52:55], v[218:225], v[176:183], v[52:55]
	v_mfma_f32_16x16x128_f8f6f4 v[48:51], v[226:233], v[176:183], v[48:51]
	v_mfma_f32_16x16x128_f8f6f4 v[36:39], v[218:225], v[184:191], v[36:39]
	v_mfma_f32_16x16x128_f8f6f4 v[32:35], v[226:233], v[184:191], v[32:35]
	v_mfma_f32_16x16x128_f8f6f4 v[20:23], v[218:225], v[196:203], v[20:23]
	v_mfma_f32_16x16x128_f8f6f4 v[16:19], v[226:233], v[196:203], v[16:19]
	v_mfma_f32_16x16x128_f8f6f4 v[4:7], v[218:225], v[204:211], v[4:7]
	v_mfma_f32_16x16x128_f8f6f4 v[0:3], v[226:233], v[204:211], v[0:3]
	s_setprio 0
	s_barrier
	s_mov_b32 m0, s57
	v_lshl_add_u64 v[140:141], s[34:35], 0, v[128:129]
	global_load_lds_dwordx4 v[140:141], off
	v_lshl_add_u64 v[140:141], s[34:35], 0, v[130:131]
	s_mov_b32 m0, s58
	s_andn2_b64 vcc, exec, s[28:29]
	global_load_lds_dwordx4 v[140:141], off
	s_mov_b64 s[30:31], -1
	s_mov_b64 s[28:29], 0
	s_mov_b64 s[34:35], 0x100
	s_cbranch_vccz .LBB0_1989
